# expert weight conversion in grid barriers 0..7, 12 tile slots per workgroup per barrier
# baseline (speedup 1.0000x reference)
.LBB0_11:
	s_or_b64 exec, exec, s[4:5]
	s_load_dwordx16 s[4:19], s[0:1], 0x40
	s_lshl_b32 s26, s74, 3
	s_lshl_b32 s0, s96, 3
	v_writelane_b32 v239, s62, 44
	v_writelane_b32 v239, s63, 45
	s_cmp_lt_i32 s64, 1
	s_waitcnt lgkmcnt(0)
	v_writelane_b32 v239, s4, 7
	s_nop 1
	v_writelane_b32 v239, s5, 8
	v_writelane_b32 v239, s6, 9
	v_writelane_b32 v239, s7, 10
	v_writelane_b32 v239, s8, 11
	v_writelane_b32 v239, s9, 12
	v_writelane_b32 v239, s10, 13
	v_writelane_b32 v239, s11, 14
	v_writelane_b32 v239, s12, 15
	v_writelane_b32 v239, s13, 16
	v_writelane_b32 v239, s14, 17
	v_writelane_b32 v239, s15, 18
	v_writelane_b32 v239, s16, 19
	v_writelane_b32 v239, s17, 20
	v_writelane_b32 v239, s18, 21
	v_writelane_b32 v239, s19, 22
	v_writelane_b32 v239, s0, 23
	s_cselect_b64 s[0:1], -1, 0
	s_cmp_gt_i32 s65, 0
	s_cselect_b64 s[2:3], -1, 0
	s_and_b64 s[4:5], s[0:1], s[2:3]
	s_andn2_b64 vcc, exec, s[4:5]
	s_cbranch_vccnz .LBB0_54
	v_mov_b32_e32 v2, v0
	s_mov_b32 s0, 0x10000
	v_mul_lo_u32 v1, v2, s74
	v_add_u32_e32 v1, s96, v1
	v_readfirstlane_b32 s2, v2
	v_cmp_gt_i32_e32 vcc, s0, v1
	s_and_saveexec_b64 s[6:7], vcc
	s_cbranch_execz .LBB0_15
	v_and_b32_e32 v4, 31, v1
	s_mov_b32 s0, 0x979a371
	v_cvt_f64_u32_e32 v[4:5], v4
	s_mov_b32 s1, 0xbfda934f
	v_mul_f64 v[4:5], v[4:5], s[0:1]
	v_rndne_f64_e32 v[6:7], v[4:5]
	s_mov_b32 s0, 0x3b39803f
	v_add_f64 v[8:9], v[4:5], -v[6:7]
	s_mov_b32 s1, 0x3c7abc9e
	v_mul_f64 v[10:11], v[8:9], s[0:1]
	s_mov_b32 s0, 0xfefa39ef
	s_mov_b32 s1, 0x3fe62e42
	v_fmac_f64_e32 v[10:11], s[0:1], v[8:9]
	s_mov_b32 s0, 0x6a5dcb37
	v_mov_b32_e32 v8, 0xfca7ab0c
	v_mov_b32_e32 v9, 0x3e928af3
	s_mov_b32 s1, 0x3e5ade15
	v_fmac_f64_e32 v[8:9], s[0:1], v[10:11]
	v_mov_b32_e32 v12, 0x623fde64
	v_mov_b32_e32 v13, 0x3ec71dee
	v_fmac_f64_e32 v[12:13], v[10:11], v[8:9]
	v_mov_b32_e32 v8, 0x7c89e6b0
	v_mov_b32_e32 v9, 0x3efa0199
	v_fmac_f64_e32 v[8:9], v[10:11], v[12:13]
	v_mov_b32_e32 v12, 0x14761f6e
	v_mov_b32_e32 v13, 0x3f2a01a0
	v_fmac_f64_e32 v[12:13], v[10:11], v[8:9]
	v_mov_b32_e32 v8, 0x1852b7b0
	v_mov_b32_e32 v9, 0x3f56c16c
	v_fmac_f64_e32 v[8:9], v[10:11], v[12:13]
	v_mov_b32_e32 v12, 0x11122322
	v_mov_b32_e32 v13, 0x3f811111
	v_fmac_f64_e32 v[12:13], v[10:11], v[8:9]
	v_mov_b32_e32 v8, 0x555502a1
	v_mov_b32_e32 v9, 0x3fa55555
	v_fmac_f64_e32 v[8:9], v[10:11], v[12:13]
	v_mov_b32_e32 v12, 0x55555511
	v_mov_b32_e32 v13, 0x3fc55555
	v_fmac_f64_e32 v[12:13], v[10:11], v[8:9]
	v_mov_b32_e32 v8, 11
	v_mov_b32_e32 v9, 0x3fe00000
	s_mov_b32 s0, 0
	v_fmac_f64_e32 v[8:9], v[10:11], v[12:13]
	s_mov_b32 s1, 0x40900000
	v_fma_f64 v[8:9], v[10:11], v[8:9], 1.0
	v_cmp_nlt_f64_e32 vcc, s[0:1], v[4:5]
	s_mov_b32 s0, 0
	v_fma_f64 v[8:9], v[10:11], v[8:9], 1.0
	v_cvt_i32_f64_e32 v6, v[6:7]
	s_mov_b32 s1, 0xc090cc00
	s_add_u32 s8, s62, 0x100000
	v_ldexp_f64 v[6:7], v[8:9], v6
	v_mov_b32_e32 v8, 0x7ff00000
	v_cmp_ngt_f64_e64 s[0:1], s[0:1], v[4:5]
	s_addc_u32 s9, s63, 0
	v_cndmask_b32_e32 v7, v8, v7, vcc
	s_and_b64 vcc, s[0:1], vcc
	s_mov_b32 s10, 0x6dc9c883
	s_mov_b32 s12, 0x54442d18
	s_lshl_b32 s3, s74, 9
	v_and_b32_e32 v3, 3, v1
	v_cndmask_b32_e64 v5, 0, v7, s[0:1]
	v_cndmask_b32_e32 v4, 0, v6, vcc
	v_bfe_u32 v6, v1, 3, 2
	v_lshlrev_b32_e32 v7, 13, v1
	s_lshl_b32 s15, s74, 22
	s_mov_b64 s[0:1], 0
	s_mov_b32 s11, 0x3fc45f30
	s_mov_b32 s13, 0xc01921fb
	s_mov_b32 s14, 0x3d000000
	s_mov_b32 s16, 0x3fffffc
	s_mov_b32 s17, 0xffff

.Lhw_seam0:
	s_mov_b64 exec, -1
	v_readlane_b32 s2, v239, 0
	s_lshr_b32 s2, s2, 6
	s_add_i32 s2, s2, -1
	s_cmp_gt_u32 s2, 11
	s_cbranch_scc1 .Lhw_seam0_done
	s_add_i32 s2, s2, 0
	s_mul_i32 s2, s2, s74
	v_readlane_b32 s9, v239, 23
	s_lshr_b32 s9, s9, 3
	s_add_i32 s2, s2, s9
	s_cmp_gt_u32 s2, 24575
	s_cbranch_scc1 .Lhw_seam0_done
	v_mbcnt_lo_u32_b32 v178, -1, 0
	v_mbcnt_hi_u32_b32 v178, -1, v178
	v_and_b32_e32 v179, 60, v178
	v_lshlrev_b32_e32 v179, 10, v179
	v_and_b32_e32 v180, 3, v178
	v_lshl_or_b32 v179, v180, 4, v179
	v_add_u32_e32 v180, 0x400, v179
	v_add_u32_e32 v181, 0x800, v179
	v_add_u32_e32 v190, 0xc00, v179
	v_lshlrev_b32_e32 v178, 2, v178
	s_cmp_lt_u32 s2, 16384
	s_cbranch_scc0 .Lhw_dn_s0_0
	s_lshr_b32 s9, s2, 9
	s_bfe_u32 s32, s2, 0x40005
	s_and_b32 s53, s2, 31
	s_lshl_b32 s69, s9, 23
	s_lshl_b32 s100, s32, 19
	s_add_i32 s69, s69, s100
	s_lshl_b32 s100, s53, 8
	s_add_i32 s69, s69, s100
	s_lshl_b32 s98, s9, 11
	s_bfe_u32 s100, s53, 0x30001
	s_lshl_b32 s100, s100, 8
	s_add_i32 s98, s98, s100
	s_lshr_b32 s100, s53, 4
	s_lshl_b32 s100, s100, 7
	s_add_i32 s98, s98, s100
	s_and_b32 s100, s53, 1
	s_lshl_b32 s100, s100, 6
	s_add_i32 s98, s98, s100
	s_lshl_b32 s98, s98, 10
	s_lshl_b32 s100, s32, 6
	s_add_i32 s98, s98, s100
	s_add_i32 s98, s98, 0x2000000
	v_readlane_b32 s82, v239, 11
	v_readlane_b32 s83, v239, 12
	s_movk_i32 s89, 8192
	s_branch .Lhw_go_s0_0

.Lhw_go_s0_0:
	s_add_u32 s100, s82, s69
	s_addc_u32 s101, s83, 0
	v_readlane_b32 s82, v239, 44
	v_readlane_b32 s83, v239, 45
	s_add_u32 s82, s82, s98
	s_addc_u32 s83, s83, 0
	global_load_dword v34, v178, s[100:101] nt
	s_add_u32 s100, s100, s89
	s_addc_u32 s101, s101, 0
	global_load_dword v35, v178, s[100:101] nt
	s_add_u32 s100, s100, s89
	s_addc_u32 s101, s101, 0
	global_load_dword v36, v178, s[100:101] nt
	s_add_u32 s100, s100, s89
	s_addc_u32 s101, s101, 0
	global_load_dword v37, v178, s[100:101] nt
	s_add_u32 s100, s100, s89
	s_addc_u32 s101, s101, 0
	global_load_dword v38, v178, s[100:101] nt
	s_add_u32 s100, s100, s89
	s_addc_u32 s101, s101, 0
	global_load_dword v39, v178, s[100:101] nt
	s_add_u32 s100, s100, s89
	s_addc_u32 s101, s101, 0
	global_load_dword v40, v178, s[100:101] nt
	s_add_u32 s100, s100, s89
	s_addc_u32 s101, s101, 0
	global_load_dword v41, v178, s[100:101] nt
	s_add_u32 s100, s100, s89
	s_addc_u32 s101, s101, 0
	global_load_dword v42, v178, s[100:101] nt
	s_add_u32 s100, s100, s89
	s_addc_u32 s101, s101, 0
	global_load_dword v43, v178, s[100:101] nt
	s_add_u32 s100, s100, s89
	s_addc_u32 s101, s101, 0
	global_load_dword v44, v178, s[100:101] nt
	s_add_u32 s100, s100, s89
	s_addc_u32 s101, s101, 0
	global_load_dword v45, v178, s[100:101] nt
	s_add_u32 s100, s100, s89
	s_addc_u32 s101, s101, 0
	global_load_dword v46, v178, s[100:101] nt
	s_add_u32 s100, s100, s89
	s_addc_u32 s101, s101, 0
	global_load_dword v47, v178, s[100:101] nt
	s_add_u32 s100, s100, s89
	s_addc_u32 s101, s101, 0
	global_load_dword v48, v178, s[100:101] nt
	s_add_u32 s100, s100, s89
	s_addc_u32 s101, s101, 0
	global_load_dword v49, v178, s[100:101] nt
	s_add_u32 s100, s100, s89
	s_addc_u32 s101, s101, 0
	global_load_dword v50, v178, s[100:101] nt
	s_add_u32 s100, s100, s89
	s_addc_u32 s101, s101, 0
	global_load_dword v51, v178, s[100:101] nt
	s_add_u32 s100, s100, s89
	s_addc_u32 s101, s101, 0
	global_load_dword v52, v178, s[100:101] nt
	s_add_u32 s100, s100, s89
	s_addc_u32 s101, s101, 0
	global_load_dword v53, v178, s[100:101] nt
	s_add_u32 s100, s100, s89
	s_addc_u32 s101, s101, 0
	global_load_dword v54, v178, s[100:101] nt
	s_add_u32 s100, s100, s89
	s_addc_u32 s101, s101, 0
	global_load_dword v55, v178, s[100:101] nt
	s_add_u32 s100, s100, s89
	s_addc_u32 s101, s101, 0
	global_load_dword v56, v178, s[100:101] nt
	s_add_u32 s100, s100, s89
	s_addc_u32 s101, s101, 0
	global_load_dword v57, v178, s[100:101] nt
	s_add_u32 s100, s100, s89
	s_addc_u32 s101, s101, 0
	global_load_dword v58, v178, s[100:101] nt
	s_add_u32 s100, s100, s89
	s_addc_u32 s101, s101, 0
	global_load_dword v59, v178, s[100:101] nt
	s_add_u32 s100, s100, s89
	s_addc_u32 s101, s101, 0
	global_load_dword v60, v178, s[100:101] nt
	s_add_u32 s100, s100, s89
	s_addc_u32 s101, s101, 0
	global_load_dword v61, v178, s[100:101] nt
	s_add_u32 s100, s100, s89
	s_addc_u32 s101, s101, 0
	global_load_dword v62, v178, s[100:101] nt
	s_add_u32 s100, s100, s89
	s_addc_u32 s101, s101, 0
	global_load_dword v63, v178, s[100:101] nt
	s_add_u32 s100, s100, s89
	s_addc_u32 s101, s101, 0
	global_load_dword v64, v178, s[100:101] nt
	s_add_u32 s100, s100, s89
	s_addc_u32 s101, s101, 0
	global_load_dword v65, v178, s[100:101] nt
	s_add_u32 s100, s100, s89
	s_addc_u32 s101, s101, 0
	global_load_dword v66, v178, s[100:101] nt
	s_add_u32 s100, s100, s89
	s_addc_u32 s101, s101, 0
	global_load_dword v67, v178, s[100:101] nt
	s_add_u32 s100, s100, s89
	s_addc_u32 s101, s101, 0
	global_load_dword v68, v178, s[100:101] nt
	s_add_u32 s100, s100, s89
	s_addc_u32 s101, s101, 0
	global_load_dword v69, v178, s[100:101] nt
	s_add_u32 s100, s100, s89
	s_addc_u32 s101, s101, 0
	global_load_dword v70, v178, s[100:101] nt
	s_add_u32 s100, s100, s89
	s_addc_u32 s101, s101, 0
	global_load_dword v71, v178, s[100:101] nt
	s_add_u32 s100, s100, s89
	s_addc_u32 s101, s101, 0
	global_load_dword v72, v178, s[100:101] nt
	s_add_u32 s100, s100, s89
	s_addc_u32 s101, s101, 0
	global_load_dword v73, v178, s[100:101] nt
	s_add_u32 s100, s100, s89
	s_addc_u32 s101, s101, 0
	global_load_dword v74, v178, s[100:101] nt
	s_add_u32 s100, s100, s89
	s_addc_u32 s101, s101, 0
	global_load_dword v75, v178, s[100:101] nt
	s_add_u32 s100, s100, s89
	s_addc_u32 s101, s101, 0
	global_load_dword v76, v178, s[100:101] nt
	s_add_u32 s100, s100, s89
	s_addc_u32 s101, s101, 0
	global_load_dword v77, v178, s[100:101] nt
	s_add_u32 s100, s100, s89
	s_addc_u32 s101, s101, 0
	global_load_dword v78, v178, s[100:101] nt
	s_add_u32 s100, s100, s89
	s_addc_u32 s101, s101, 0
	global_load_dword v79, v178, s[100:101] nt
	s_add_u32 s100, s100, s89
	s_addc_u32 s101, s101, 0
	global_load_dword v80, v178, s[100:101] nt
	s_add_u32 s100, s100, s89
	s_addc_u32 s101, s101, 0
	global_load_dword v81, v178, s[100:101] nt
	s_add_u32 s100, s100, s89
	s_addc_u32 s101, s101, 0
	global_load_dword v82, v178, s[100:101] nt
	s_add_u32 s100, s100, s89
	s_addc_u32 s101, s101, 0
	global_load_dword v83, v178, s[100:101] nt
	s_add_u32 s100, s100, s89
	s_addc_u32 s101, s101, 0
	global_load_dword v84, v178, s[100:101] nt
	s_add_u32 s100, s100, s89
	s_addc_u32 s101, s101, 0
	global_load_dword v85, v178, s[100:101] nt
	s_add_u32 s100, s100, s89
	s_addc_u32 s101, s101, 0
	global_load_dword v86, v178, s[100:101] nt
	s_add_u32 s100, s100, s89
	s_addc_u32 s101, s101, 0
	global_load_dword v87, v178, s[100:101] nt
	s_add_u32 s100, s100, s89
	s_addc_u32 s101, s101, 0
	global_load_dword v88, v178, s[100:101] nt
	s_add_u32 s100, s100, s89
	s_addc_u32 s101, s101, 0
	global_load_dword v89, v178, s[100:101] nt
	s_add_u32 s100, s100, s89
	s_addc_u32 s101, s101, 0
	global_load_dword v90, v178, s[100:101] nt
	s_add_u32 s100, s100, s89
	s_addc_u32 s101, s101, 0
	global_load_dword v91, v178, s[100:101] nt
	s_add_u32 s100, s100, s89
	s_addc_u32 s101, s101, 0
	global_load_dword v92, v178, s[100:101] nt
	s_add_u32 s100, s100, s89
	s_addc_u32 s101, s101, 0
	global_load_dword v93, v178, s[100:101] nt
	s_add_u32 s100, s100, s89
	s_addc_u32 s101, s101, 0
	global_load_dword v94, v178, s[100:101] nt
	s_add_u32 s100, s100, s89
	s_addc_u32 s101, s101, 0
	global_load_dword v95, v178, s[100:101] nt
	s_add_u32 s100, s100, s89
	s_addc_u32 s101, s101, 0
	global_load_dword v96, v178, s[100:101] nt
	s_add_u32 s100, s100, s89
	s_addc_u32 s101, s101, 0
	global_load_dword v97, v178, s[100:101] nt
	s_add_u32 s100, s100, s89
	s_addc_u32 s101, s101, 0
	s_waitcnt vmcnt(48)
	v_mul_f32_e32 v34, 0x42000000, v34
	v_mul_f32_e32 v35, 0x42000000, v35
	v_mul_f32_e32 v36, 0x42000000, v36
	v_mul_f32_e32 v37, 0x42000000, v37
	v_mul_f32_e32 v38, 0x42000000, v38
	v_mul_f32_e32 v39, 0x42000000, v39
	v_mul_f32_e32 v40, 0x42000000, v40
	v_mul_f32_e32 v41, 0x42000000, v41
	v_mul_f32_e32 v42, 0x42000000, v42
	v_mul_f32_e32 v43, 0x42000000, v43
	v_mul_f32_e32 v44, 0x42000000, v44
	v_mul_f32_e32 v45, 0x42000000, v45
	v_mul_f32_e32 v46, 0x42000000, v46
	v_mul_f32_e32 v47, 0x42000000, v47
	v_mul_f32_e32 v48, 0x42000000, v48
	v_mul_f32_e32 v49, 0x42000000, v49
	v_cvt_pk_fp8_f32 v154, v34, v35
	v_cvt_pk_fp8_f32 v155, v38, v39
	v_cvt_pk_fp8_f32 v156, v42, v43
	v_cvt_pk_fp8_f32 v157, v46, v47
	v_cvt_pk_fp8_f32 v154, v36, v37 op_sel:[0,0,1]
	v_cvt_pk_fp8_f32 v155, v40, v41 op_sel:[0,0,1]
	v_cvt_pk_fp8_f32 v156, v44, v45 op_sel:[0,0,1]
	v_cvt_pk_fp8_f32 v157, v48, v49 op_sel:[0,0,1]
	s_waitcnt vmcnt(32)
	v_mul_f32_e32 v50, 0x42000000, v50
	v_mul_f32_e32 v51, 0x42000000, v51
	v_mul_f32_e32 v52, 0x42000000, v52
	v_mul_f32_e32 v53, 0x42000000, v53
	v_mul_f32_e32 v54, 0x42000000, v54
	v_mul_f32_e32 v55, 0x42000000, v55
	v_mul_f32_e32 v56, 0x42000000, v56
	v_mul_f32_e32 v57, 0x42000000, v57
	v_mul_f32_e32 v58, 0x42000000, v58
	v_mul_f32_e32 v59, 0x42000000, v59
	v_mul_f32_e32 v60, 0x42000000, v60
	v_mul_f32_e32 v61, 0x42000000, v61
	v_mul_f32_e32 v62, 0x42000000, v62
	v_mul_f32_e32 v63, 0x42000000, v63
	v_mul_f32_e32 v64, 0x42000000, v64
	v_mul_f32_e32 v65, 0x42000000, v65
	v_cvt_pk_fp8_f32 v158, v50, v51
	v_cvt_pk_fp8_f32 v159, v54, v55
	v_cvt_pk_fp8_f32 v160, v58, v59
	v_cvt_pk_fp8_f32 v161, v62, v63
	v_cvt_pk_fp8_f32 v158, v52, v53 op_sel:[0,0,1]
	v_cvt_pk_fp8_f32 v159, v56, v57 op_sel:[0,0,1]
	v_cvt_pk_fp8_f32 v160, v60, v61 op_sel:[0,0,1]
	v_cvt_pk_fp8_f32 v161, v64, v65 op_sel:[0,0,1]
	s_waitcnt vmcnt(16)
	v_mul_f32_e32 v66, 0x42000000, v66
	v_mul_f32_e32 v67, 0x42000000, v67
	v_mul_f32_e32 v68, 0x42000000, v68
	v_mul_f32_e32 v69, 0x42000000, v69
	v_mul_f32_e32 v70, 0x42000000, v70
	v_mul_f32_e32 v71, 0x42000000, v71
	v_mul_f32_e32 v72, 0x42000000, v72
	v_mul_f32_e32 v73, 0x42000000, v73
	v_mul_f32_e32 v74, 0x42000000, v74
	v_mul_f32_e32 v75, 0x42000000, v75
	v_mul_f32_e32 v76, 0x42000000, v76
	v_mul_f32_e32 v77, 0x42000000, v77
	v_mul_f32_e32 v78, 0x42000000, v78
	v_mul_f32_e32 v79, 0x42000000, v79
	v_mul_f32_e32 v80, 0x42000000, v80
	v_mul_f32_e32 v81, 0x42000000, v81
	v_cvt_pk_fp8_f32 v162, v66, v67
	v_cvt_pk_fp8_f32 v163, v70, v71
	v_cvt_pk_fp8_f32 v164, v74, v75
	v_cvt_pk_fp8_f32 v165, v78, v79
	v_cvt_pk_fp8_f32 v162, v68, v69 op_sel:[0,0,1]
	v_cvt_pk_fp8_f32 v163, v72, v73 op_sel:[0,0,1]
	v_cvt_pk_fp8_f32 v164, v76, v77 op_sel:[0,0,1]
	v_cvt_pk_fp8_f32 v165, v80, v81 op_sel:[0,0,1]
	s_waitcnt vmcnt(0)
	v_mul_f32_e32 v82, 0x42000000, v82
	v_mul_f32_e32 v83, 0x42000000, v83
	v_mul_f32_e32 v84, 0x42000000, v84
	v_mul_f32_e32 v85, 0x42000000, v85
	v_mul_f32_e32 v86, 0x42000000, v86
	v_mul_f32_e32 v87, 0x42000000, v87
	v_mul_f32_e32 v88, 0x42000000, v88
	v_mul_f32_e32 v89, 0x42000000, v89
	v_mul_f32_e32 v90, 0x42000000, v90
	v_mul_f32_e32 v91, 0x42000000, v91
	v_mul_f32_e32 v92, 0x42000000, v92
	v_mul_f32_e32 v93, 0x42000000, v93
	v_mul_f32_e32 v94, 0x42000000, v94
	v_mul_f32_e32 v95, 0x42000000, v95
	v_mul_f32_e32 v96, 0x42000000, v96
	v_mul_f32_e32 v97, 0x42000000, v97
	v_cvt_pk_fp8_f32 v166, v82, v83
	v_cvt_pk_fp8_f32 v167, v86, v87
	v_cvt_pk_fp8_f32 v168, v90, v91
	v_cvt_pk_fp8_f32 v169, v94, v95
	v_cvt_pk_fp8_f32 v166, v84, v85 op_sel:[0,0,1]
	v_cvt_pk_fp8_f32 v167, v88, v89 op_sel:[0,0,1]
	v_cvt_pk_fp8_f32 v168, v92, v93 op_sel:[0,0,1]
	v_cvt_pk_fp8_f32 v169, v96, v97 op_sel:[0,0,1]
	s_mov_b32 vcc_lo, 0xaaaaaaaa
	s_mov_b32 vcc_hi, 0xaaaaaaaa
	s_nop 1
	v_cndmask_b32_dpp v170, v154, v158, vcc quad_perm:[1,0,3,2] row_mask:0xf bank_mask:0xf
	v_cndmask_b32_dpp v174, v162, v166, vcc quad_perm:[1,0,3,2] row_mask:0xf bank_mask:0xf
	v_cndmask_b32_dpp v171, v155, v159, vcc quad_perm:[1,0,3,2] row_mask:0xf bank_mask:0xf
	v_cndmask_b32_dpp v175, v163, v167, vcc quad_perm:[1,0,3,2] row_mask:0xf bank_mask:0xf
	v_cndmask_b32_dpp v172, v156, v160, vcc quad_perm:[1,0,3,2] row_mask:0xf bank_mask:0xf
	v_cndmask_b32_dpp v176, v164, v168, vcc quad_perm:[1,0,3,2] row_mask:0xf bank_mask:0xf
	v_cndmask_b32_dpp v173, v157, v161, vcc quad_perm:[1,0,3,2] row_mask:0xf bank_mask:0xf
	v_cndmask_b32_dpp v177, v165, v169, vcc quad_perm:[1,0,3,2] row_mask:0xf bank_mask:0xf
	s_mov_b32 vcc_lo, 0x55555555
	s_mov_b32 vcc_hi, 0x55555555
	s_nop 1
	v_cndmask_b32_dpp v154, v158, v154, vcc quad_perm:[1,0,3,2] row_mask:0xf bank_mask:0xf
	v_cndmask_b32_dpp v162, v166, v162, vcc quad_perm:[1,0,3,2] row_mask:0xf bank_mask:0xf
	v_cndmask_b32_dpp v155, v159, v155, vcc quad_perm:[1,0,3,2] row_mask:0xf bank_mask:0xf
	v_cndmask_b32_dpp v163, v167, v163, vcc quad_perm:[1,0,3,2] row_mask:0xf bank_mask:0xf
	v_cndmask_b32_dpp v156, v160, v156, vcc quad_perm:[1,0,3,2] row_mask:0xf bank_mask:0xf
	v_cndmask_b32_dpp v164, v168, v164, vcc quad_perm:[1,0,3,2] row_mask:0xf bank_mask:0xf
	v_cndmask_b32_dpp v157, v161, v157, vcc quad_perm:[1,0,3,2] row_mask:0xf bank_mask:0xf
	v_cndmask_b32_dpp v165, v169, v165, vcc quad_perm:[1,0,3,2] row_mask:0xf bank_mask:0xf
	s_mov_b32 vcc_lo, 0xcccccccc
	s_mov_b32 vcc_hi, 0xcccccccc
	s_nop 1
	v_cndmask_b32_dpp v158, v154, v162, vcc quad_perm:[2,3,0,1] row_mask:0xf bank_mask:0xf
	v_cndmask_b32_dpp v166, v170, v174, vcc quad_perm:[2,3,0,1] row_mask:0xf bank_mask:0xf
	v_cndmask_b32_dpp v159, v155, v163, vcc quad_perm:[2,3,0,1] row_mask:0xf bank_mask:0xf
	v_cndmask_b32_dpp v167, v171, v175, vcc quad_perm:[2,3,0,1] row_mask:0xf bank_mask:0xf
	v_cndmask_b32_dpp v160, v156, v164, vcc quad_perm:[2,3,0,1] row_mask:0xf bank_mask:0xf
	v_cndmask_b32_dpp v168, v172, v176, vcc quad_perm:[2,3,0,1] row_mask:0xf bank_mask:0xf
	v_cndmask_b32_dpp v161, v157, v165, vcc quad_perm:[2,3,0,1] row_mask:0xf bank_mask:0xf
	v_cndmask_b32_dpp v169, v173, v177, vcc quad_perm:[2,3,0,1] row_mask:0xf bank_mask:0xf
	s_mov_b32 vcc_lo, 0x33333333
	s_mov_b32 vcc_hi, 0x33333333
	s_nop 1
	v_cndmask_b32_dpp v154, v162, v154, vcc quad_perm:[2,3,0,1] row_mask:0xf bank_mask:0xf
	v_cndmask_b32_dpp v170, v174, v170, vcc quad_perm:[2,3,0,1] row_mask:0xf bank_mask:0xf
	v_cndmask_b32_dpp v155, v163, v155, vcc quad_perm:[2,3,0,1] row_mask:0xf bank_mask:0xf
	v_cndmask_b32_dpp v171, v175, v171, vcc quad_perm:[2,3,0,1] row_mask:0xf bank_mask:0xf
	v_cndmask_b32_dpp v156, v164, v156, vcc quad_perm:[2,3,0,1] row_mask:0xf bank_mask:0xf
	v_cndmask_b32_dpp v172, v176, v172, vcc quad_perm:[2,3,0,1] row_mask:0xf bank_mask:0xf
	v_cndmask_b32_dpp v157, v165, v157, vcc quad_perm:[2,3,0,1] row_mask:0xf bank_mask:0xf
	v_cndmask_b32_dpp v173, v177, v173, vcc quad_perm:[2,3,0,1] row_mask:0xf bank_mask:0xf
	global_store_dwordx4 v179, v[154:157], s[82:83] nt
	global_store_dwordx4 v180, v[170:173], s[82:83] nt
	global_store_dwordx4 v181, v[158:161], s[82:83] nt
	global_store_dwordx4 v190, v[166:169], s[82:83] nt
	v_readlane_b32 s2, v239, 0
	s_lshr_b32 s2, s2, 6
	s_add_i32 s2, s2, 6
	s_cmp_gt_u32 s2, 11
	s_cbranch_scc1 .Lhw_seam0_done
	s_add_i32 s2, s2, 0
	s_mul_i32 s2, s2, s74
	v_readlane_b32 s9, v239, 23
	s_lshr_b32 s9, s9, 3
	s_add_i32 s2, s2, s9
	s_cmp_gt_u32 s2, 24575
	s_cbranch_scc1 .Lhw_seam0_done
	v_mbcnt_lo_u32_b32 v178, -1, 0
	v_mbcnt_hi_u32_b32 v178, -1, v178
	v_and_b32_e32 v179, 60, v178
	v_lshlrev_b32_e32 v179, 10, v179
	v_and_b32_e32 v180, 3, v178
	v_lshl_or_b32 v179, v180, 4, v179
	v_add_u32_e32 v180, 0x400, v179
	v_add_u32_e32 v181, 0x800, v179
	v_add_u32_e32 v190, 0xc00, v179
	v_lshlrev_b32_e32 v178, 2, v178
	s_cmp_lt_u32 s2, 16384
	s_cbranch_scc0 .Lhw_dn_s0_1
	s_lshr_b32 s9, s2, 9
	s_bfe_u32 s32, s2, 0x40005
	s_and_b32 s53, s2, 31
	s_lshl_b32 s69, s9, 23
	s_lshl_b32 s100, s32, 19
	s_add_i32 s69, s69, s100
	s_lshl_b32 s100, s53, 8
	s_add_i32 s69, s69, s100
	s_lshl_b32 s98, s9, 11
	s_bfe_u32 s100, s53, 0x30001
	s_lshl_b32 s100, s100, 8
	s_add_i32 s98, s98, s100
	s_lshr_b32 s100, s53, 4
	s_lshl_b32 s100, s100, 7
	s_add_i32 s98, s98, s100
	s_and_b32 s100, s53, 1
	s_lshl_b32 s100, s100, 6
	s_add_i32 s98, s98, s100
	s_lshl_b32 s98, s98, 10
	s_lshl_b32 s100, s32, 6
	s_add_i32 s98, s98, s100
	s_add_i32 s98, s98, 0x2000000
	v_readlane_b32 s82, v239, 11
	v_readlane_b32 s83, v239, 12
	s_movk_i32 s89, 8192
	s_branch .Lhw_go_s0_1

.Lhw_seam1:
	s_mov_b64 exec, -1
	v_readlane_b32 s2, v239, 0
	s_lshr_b32 s2, s2, 6
	s_add_i32 s2, s2, -1
	s_cmp_gt_u32 s2, 11
	s_cbranch_scc1 .Lhw_seam1_done
	s_add_i32 s2, s2, 12
	s_mul_i32 s2, s2, s74
	v_readlane_b32 s9, v239, 23
	s_lshr_b32 s9, s9, 3
	s_add_i32 s2, s2, s9
	s_cmp_gt_u32 s2, 24575
	s_cbranch_scc1 .Lhw_seam1_done
	v_mbcnt_lo_u32_b32 v178, -1, 0
	v_mbcnt_hi_u32_b32 v178, -1, v178
	v_and_b32_e32 v179, 60, v178
	v_lshlrev_b32_e32 v179, 10, v179
	v_and_b32_e32 v180, 3, v178
	v_lshl_or_b32 v179, v180, 4, v179
	v_add_u32_e32 v180, 0x400, v179
	v_add_u32_e32 v181, 0x800, v179
	v_add_u32_e32 v190, 0xc00, v179
	v_lshlrev_b32_e32 v178, 2, v178
	s_cmp_lt_u32 s2, 16384
	s_cbranch_scc0 .Lhw_dn_s1_0
	s_lshr_b32 s9, s2, 9
	s_bfe_u32 s32, s2, 0x40005
	s_and_b32 s53, s2, 31
	s_lshl_b32 s69, s9, 23
	s_lshl_b32 s100, s32, 19
	s_add_i32 s69, s69, s100
	s_lshl_b32 s100, s53, 8
	s_add_i32 s69, s69, s100
	s_lshl_b32 s98, s9, 11
	s_bfe_u32 s100, s53, 0x30001
	s_lshl_b32 s100, s100, 8
	s_add_i32 s98, s98, s100
	s_lshr_b32 s100, s53, 4
	s_lshl_b32 s100, s100, 7
	s_add_i32 s98, s98, s100
	s_and_b32 s100, s53, 1
	s_lshl_b32 s100, s100, 6
	s_add_i32 s98, s98, s100
	s_lshl_b32 s98, s98, 10
	s_lshl_b32 s100, s32, 6
	s_add_i32 s98, s98, s100
	s_add_i32 s98, s98, 0x2000000
	v_readlane_b32 s82, v239, 11
	v_readlane_b32 s83, v239, 12
	s_movk_i32 s89, 8192
	s_branch .Lhw_go_s1_0

.Lhw_go_s1_0:
	s_add_u32 s100, s82, s69
	s_addc_u32 s101, s83, 0
	v_readlane_b32 s82, v239, 44
	v_readlane_b32 s83, v239, 45
	s_add_u32 s82, s82, s98
	s_addc_u32 s83, s83, 0
	global_load_dword v34, v178, s[100:101] nt
	s_add_u32 s100, s100, s89
	s_addc_u32 s101, s101, 0
	global_load_dword v35, v178, s[100:101] nt
	s_add_u32 s100, s100, s89
	s_addc_u32 s101, s101, 0
	global_load_dword v36, v178, s[100:101] nt
	s_add_u32 s100, s100, s89
	s_addc_u32 s101, s101, 0
	global_load_dword v37, v178, s[100:101] nt
	s_add_u32 s100, s100, s89
	s_addc_u32 s101, s101, 0
	global_load_dword v38, v178, s[100:101] nt
	s_add_u32 s100, s100, s89
	s_addc_u32 s101, s101, 0
	global_load_dword v39, v178, s[100:101] nt
	s_add_u32 s100, s100, s89
	s_addc_u32 s101, s101, 0
	global_load_dword v40, v178, s[100:101] nt
	s_add_u32 s100, s100, s89
	s_addc_u32 s101, s101, 0
	global_load_dword v41, v178, s[100:101] nt
	s_add_u32 s100, s100, s89
	s_addc_u32 s101, s101, 0
	global_load_dword v42, v178, s[100:101] nt
	s_add_u32 s100, s100, s89
	s_addc_u32 s101, s101, 0
	global_load_dword v43, v178, s[100:101] nt
	s_add_u32 s100, s100, s89
	s_addc_u32 s101, s101, 0
	global_load_dword v44, v178, s[100:101] nt
	s_add_u32 s100, s100, s89
	s_addc_u32 s101, s101, 0
	global_load_dword v45, v178, s[100:101] nt
	s_add_u32 s100, s100, s89
	s_addc_u32 s101, s101, 0
	global_load_dword v46, v178, s[100:101] nt
	s_add_u32 s100, s100, s89
	s_addc_u32 s101, s101, 0
	global_load_dword v47, v178, s[100:101] nt
	s_add_u32 s100, s100, s89
	s_addc_u32 s101, s101, 0
	global_load_dword v48, v178, s[100:101] nt
	s_add_u32 s100, s100, s89
	s_addc_u32 s101, s101, 0
	global_load_dword v49, v178, s[100:101] nt
	s_add_u32 s100, s100, s89
	s_addc_u32 s101, s101, 0
	global_load_dword v50, v178, s[100:101] nt
	s_add_u32 s100, s100, s89
	s_addc_u32 s101, s101, 0
	global_load_dword v51, v178, s[100:101] nt
	s_add_u32 s100, s100, s89
	s_addc_u32 s101, s101, 0
	global_load_dword v52, v178, s[100:101] nt
	s_add_u32 s100, s100, s89
	s_addc_u32 s101, s101, 0
	global_load_dword v53, v178, s[100:101] nt
	s_add_u32 s100, s100, s89
	s_addc_u32 s101, s101, 0
	global_load_dword v54, v178, s[100:101] nt
	s_add_u32 s100, s100, s89
	s_addc_u32 s101, s101, 0
	global_load_dword v55, v178, s[100:101] nt
	s_add_u32 s100, s100, s89
	s_addc_u32 s101, s101, 0
	global_load_dword v56, v178, s[100:101] nt
	s_add_u32 s100, s100, s89
	s_addc_u32 s101, s101, 0
	global_load_dword v57, v178, s[100:101] nt
	s_add_u32 s100, s100, s89
	s_addc_u32 s101, s101, 0
	global_load_dword v58, v178, s[100:101] nt
	s_add_u32 s100, s100, s89
	s_addc_u32 s101, s101, 0
	global_load_dword v59, v178, s[100:101] nt
	s_add_u32 s100, s100, s89
	s_addc_u32 s101, s101, 0
	global_load_dword v60, v178, s[100:101] nt
	s_add_u32 s100, s100, s89
	s_addc_u32 s101, s101, 0
	global_load_dword v61, v178, s[100:101] nt
	s_add_u32 s100, s100, s89
	s_addc_u32 s101, s101, 0
	global_load_dword v62, v178, s[100:101] nt
	s_add_u32 s100, s100, s89
	s_addc_u32 s101, s101, 0
	global_load_dword v63, v178, s[100:101] nt
	s_add_u32 s100, s100, s89
	s_addc_u32 s101, s101, 0
	global_load_dword v64, v178, s[100:101] nt
	s_add_u32 s100, s100, s89
	s_addc_u32 s101, s101, 0
	global_load_dword v65, v178, s[100:101] nt
	s_add_u32 s100, s100, s89
	s_addc_u32 s101, s101, 0
	global_load_dword v66, v178, s[100:101] nt
	s_add_u32 s100, s100, s89
	s_addc_u32 s101, s101, 0
	global_load_dword v67, v178, s[100:101] nt
	s_add_u32 s100, s100, s89
	s_addc_u32 s101, s101, 0
	global_load_dword v68, v178, s[100:101] nt
	s_add_u32 s100, s100, s89
	s_addc_u32 s101, s101, 0
	global_load_dword v69, v178, s[100:101] nt
	s_add_u32 s100, s100, s89
	s_addc_u32 s101, s101, 0
	global_load_dword v70, v178, s[100:101] nt
	s_add_u32 s100, s100, s89
	s_addc_u32 s101, s101, 0
	global_load_dword v71, v178, s[100:101] nt
	s_add_u32 s100, s100, s89
	s_addc_u32 s101, s101, 0
	global_load_dword v72, v178, s[100:101] nt
	s_add_u32 s100, s100, s89
	s_addc_u32 s101, s101, 0
	global_load_dword v73, v178, s[100:101] nt
	s_add_u32 s100, s100, s89
	s_addc_u32 s101, s101, 0
	global_load_dword v74, v178, s[100:101] nt
	s_add_u32 s100, s100, s89
	s_addc_u32 s101, s101, 0
	global_load_dword v75, v178, s[100:101] nt
	s_add_u32 s100, s100, s89
	s_addc_u32 s101, s101, 0
	global_load_dword v76, v178, s[100:101] nt
	s_add_u32 s100, s100, s89
	s_addc_u32 s101, s101, 0
	global_load_dword v77, v178, s[100:101] nt
	s_add_u32 s100, s100, s89
	s_addc_u32 s101, s101, 0
	global_load_dword v78, v178, s[100:101] nt
	s_add_u32 s100, s100, s89
	s_addc_u32 s101, s101, 0
	global_load_dword v79, v178, s[100:101] nt
	s_add_u32 s100, s100, s89
	s_addc_u32 s101, s101, 0
	global_load_dword v80, v178, s[100:101] nt
	s_add_u32 s100, s100, s89
	s_addc_u32 s101, s101, 0
	global_load_dword v81, v178, s[100:101] nt
	s_add_u32 s100, s100, s89
	s_addc_u32 s101, s101, 0
	global_load_dword v82, v178, s[100:101] nt
	s_add_u32 s100, s100, s89
	s_addc_u32 s101, s101, 0
	global_load_dword v83, v178, s[100:101] nt
	s_add_u32 s100, s100, s89
	s_addc_u32 s101, s101, 0
	global_load_dword v84, v178, s[100:101] nt
	s_add_u32 s100, s100, s89
	s_addc_u32 s101, s101, 0
	global_load_dword v85, v178, s[100:101] nt
	s_add_u32 s100, s100, s89
	s_addc_u32 s101, s101, 0
	global_load_dword v86, v178, s[100:101] nt
	s_add_u32 s100, s100, s89
	s_addc_u32 s101, s101, 0
	global_load_dword v87, v178, s[100:101] nt
	s_add_u32 s100, s100, s89
	s_addc_u32 s101, s101, 0
	global_load_dword v88, v178, s[100:101] nt
	s_add_u32 s100, s100, s89
	s_addc_u32 s101, s101, 0
	global_load_dword v89, v178, s[100:101] nt
	s_add_u32 s100, s100, s89
	s_addc_u32 s101, s101, 0
	global_load_dword v90, v178, s[100:101] nt
	s_add_u32 s100, s100, s89
	s_addc_u32 s101, s101, 0
	global_load_dword v91, v178, s[100:101] nt
	s_add_u32 s100, s100, s89
	s_addc_u32 s101, s101, 0
	global_load_dword v92, v178, s[100:101] nt
	s_add_u32 s100, s100, s89
	s_addc_u32 s101, s101, 0
	global_load_dword v93, v178, s[100:101] nt
	s_add_u32 s100, s100, s89
	s_addc_u32 s101, s101, 0
	global_load_dword v94, v178, s[100:101] nt
	s_add_u32 s100, s100, s89
	s_addc_u32 s101, s101, 0
	global_load_dword v95, v178, s[100:101] nt
	s_add_u32 s100, s100, s89
	s_addc_u32 s101, s101, 0
	global_load_dword v96, v178, s[100:101] nt
	s_add_u32 s100, s100, s89
	s_addc_u32 s101, s101, 0
	global_load_dword v97, v178, s[100:101] nt
	s_add_u32 s100, s100, s89
	s_addc_u32 s101, s101, 0
	s_waitcnt vmcnt(48)
	v_mul_f32_e32 v34, 0x42000000, v34
	v_mul_f32_e32 v35, 0x42000000, v35
	v_mul_f32_e32 v36, 0x42000000, v36
	v_mul_f32_e32 v37, 0x42000000, v37
	v_mul_f32_e32 v38, 0x42000000, v38
	v_mul_f32_e32 v39, 0x42000000, v39
	v_mul_f32_e32 v40, 0x42000000, v40
	v_mul_f32_e32 v41, 0x42000000, v41
	v_mul_f32_e32 v42, 0x42000000, v42
	v_mul_f32_e32 v43, 0x42000000, v43
	v_mul_f32_e32 v44, 0x42000000, v44
	v_mul_f32_e32 v45, 0x42000000, v45
	v_mul_f32_e32 v46, 0x42000000, v46
	v_mul_f32_e32 v47, 0x42000000, v47
	v_mul_f32_e32 v48, 0x42000000, v48
	v_mul_f32_e32 v49, 0x42000000, v49
	v_cvt_pk_fp8_f32 v154, v34, v35
	v_cvt_pk_fp8_f32 v155, v38, v39
	v_cvt_pk_fp8_f32 v156, v42, v43
	v_cvt_pk_fp8_f32 v157, v46, v47
	v_cvt_pk_fp8_f32 v154, v36, v37 op_sel:[0,0,1]
	v_cvt_pk_fp8_f32 v155, v40, v41 op_sel:[0,0,1]
	v_cvt_pk_fp8_f32 v156, v44, v45 op_sel:[0,0,1]
	v_cvt_pk_fp8_f32 v157, v48, v49 op_sel:[0,0,1]
	s_waitcnt vmcnt(32)
	v_mul_f32_e32 v50, 0x42000000, v50
	v_mul_f32_e32 v51, 0x42000000, v51
	v_mul_f32_e32 v52, 0x42000000, v52
	v_mul_f32_e32 v53, 0x42000000, v53
	v_mul_f32_e32 v54, 0x42000000, v54
	v_mul_f32_e32 v55, 0x42000000, v55
	v_mul_f32_e32 v56, 0x42000000, v56
	v_mul_f32_e32 v57, 0x42000000, v57
	v_mul_f32_e32 v58, 0x42000000, v58
	v_mul_f32_e32 v59, 0x42000000, v59
	v_mul_f32_e32 v60, 0x42000000, v60
	v_mul_f32_e32 v61, 0x42000000, v61
	v_mul_f32_e32 v62, 0x42000000, v62
	v_mul_f32_e32 v63, 0x42000000, v63
	v_mul_f32_e32 v64, 0x42000000, v64
	v_mul_f32_e32 v65, 0x42000000, v65
	v_cvt_pk_fp8_f32 v158, v50, v51
	v_cvt_pk_fp8_f32 v159, v54, v55
	v_cvt_pk_fp8_f32 v160, v58, v59
	v_cvt_pk_fp8_f32 v161, v62, v63
	v_cvt_pk_fp8_f32 v158, v52, v53 op_sel:[0,0,1]
	v_cvt_pk_fp8_f32 v159, v56, v57 op_sel:[0,0,1]
	v_cvt_pk_fp8_f32 v160, v60, v61 op_sel:[0,0,1]
	v_cvt_pk_fp8_f32 v161, v64, v65 op_sel:[0,0,1]
	s_waitcnt vmcnt(16)
	v_mul_f32_e32 v66, 0x42000000, v66
	v_mul_f32_e32 v67, 0x42000000, v67
	v_mul_f32_e32 v68, 0x42000000, v68
	v_mul_f32_e32 v69, 0x42000000, v69
	v_mul_f32_e32 v70, 0x42000000, v70
	v_mul_f32_e32 v71, 0x42000000, v71
	v_mul_f32_e32 v72, 0x42000000, v72
	v_mul_f32_e32 v73, 0x42000000, v73
	v_mul_f32_e32 v74, 0x42000000, v74
	v_mul_f32_e32 v75, 0x42000000, v75
	v_mul_f32_e32 v76, 0x42000000, v76
	v_mul_f32_e32 v77, 0x42000000, v77
	v_mul_f32_e32 v78, 0x42000000, v78
	v_mul_f32_e32 v79, 0x42000000, v79
	v_mul_f32_e32 v80, 0x42000000, v80
	v_mul_f32_e32 v81, 0x42000000, v81
	v_cvt_pk_fp8_f32 v162, v66, v67
	v_cvt_pk_fp8_f32 v163, v70, v71
	v_cvt_pk_fp8_f32 v164, v74, v75
	v_cvt_pk_fp8_f32 v165, v78, v79
	v_cvt_pk_fp8_f32 v162, v68, v69 op_sel:[0,0,1]
	v_cvt_pk_fp8_f32 v163, v72, v73 op_sel:[0,0,1]
	v_cvt_pk_fp8_f32 v164, v76, v77 op_sel:[0,0,1]
	v_cvt_pk_fp8_f32 v165, v80, v81 op_sel:[0,0,1]
	s_waitcnt vmcnt(0)
	v_mul_f32_e32 v82, 0x42000000, v82
	v_mul_f32_e32 v83, 0x42000000, v83
	v_mul_f32_e32 v84, 0x42000000, v84
	v_mul_f32_e32 v85, 0x42000000, v85
	v_mul_f32_e32 v86, 0x42000000, v86
	v_mul_f32_e32 v87, 0x42000000, v87
	v_mul_f32_e32 v88, 0x42000000, v88
	v_mul_f32_e32 v89, 0x42000000, v89
	v_mul_f32_e32 v90, 0x42000000, v90
	v_mul_f32_e32 v91, 0x42000000, v91
	v_mul_f32_e32 v92, 0x42000000, v92
	v_mul_f32_e32 v93, 0x42000000, v93
	v_mul_f32_e32 v94, 0x42000000, v94
	v_mul_f32_e32 v95, 0x42000000, v95
	v_mul_f32_e32 v96, 0x42000000, v96
	v_mul_f32_e32 v97, 0x42000000, v97
	v_cvt_pk_fp8_f32 v166, v82, v83
	v_cvt_pk_fp8_f32 v167, v86, v87
	v_cvt_pk_fp8_f32 v168, v90, v91
	v_cvt_pk_fp8_f32 v169, v94, v95
	v_cvt_pk_fp8_f32 v166, v84, v85 op_sel:[0,0,1]
	v_cvt_pk_fp8_f32 v167, v88, v89 op_sel:[0,0,1]
	v_cvt_pk_fp8_f32 v168, v92, v93 op_sel:[0,0,1]
	v_cvt_pk_fp8_f32 v169, v96, v97 op_sel:[0,0,1]
	s_mov_b32 vcc_lo, 0xaaaaaaaa
	s_mov_b32 vcc_hi, 0xaaaaaaaa
	s_nop 1
	v_cndmask_b32_dpp v170, v154, v158, vcc quad_perm:[1,0,3,2] row_mask:0xf bank_mask:0xf
	v_cndmask_b32_dpp v174, v162, v166, vcc quad_perm:[1,0,3,2] row_mask:0xf bank_mask:0xf
	v_cndmask_b32_dpp v171, v155, v159, vcc quad_perm:[1,0,3,2] row_mask:0xf bank_mask:0xf
	v_cndmask_b32_dpp v175, v163, v167, vcc quad_perm:[1,0,3,2] row_mask:0xf bank_mask:0xf
	v_cndmask_b32_dpp v172, v156, v160, vcc quad_perm:[1,0,3,2] row_mask:0xf bank_mask:0xf
	v_cndmask_b32_dpp v176, v164, v168, vcc quad_perm:[1,0,3,2] row_mask:0xf bank_mask:0xf
	v_cndmask_b32_dpp v173, v157, v161, vcc quad_perm:[1,0,3,2] row_mask:0xf bank_mask:0xf
	v_cndmask_b32_dpp v177, v165, v169, vcc quad_perm:[1,0,3,2] row_mask:0xf bank_mask:0xf
	s_mov_b32 vcc_lo, 0x55555555
	s_mov_b32 vcc_hi, 0x55555555
	s_nop 1
	v_cndmask_b32_dpp v154, v158, v154, vcc quad_perm:[1,0,3,2] row_mask:0xf bank_mask:0xf
	v_cndmask_b32_dpp v162, v166, v162, vcc quad_perm:[1,0,3,2] row_mask:0xf bank_mask:0xf
	v_cndmask_b32_dpp v155, v159, v155, vcc quad_perm:[1,0,3,2] row_mask:0xf bank_mask:0xf
	v_cndmask_b32_dpp v163, v167, v163, vcc quad_perm:[1,0,3,2] row_mask:0xf bank_mask:0xf
	v_cndmask_b32_dpp v156, v160, v156, vcc quad_perm:[1,0,3,2] row_mask:0xf bank_mask:0xf
	v_cndmask_b32_dpp v164, v168, v164, vcc quad_perm:[1,0,3,2] row_mask:0xf bank_mask:0xf
	v_cndmask_b32_dpp v157, v161, v157, vcc quad_perm:[1,0,3,2] row_mask:0xf bank_mask:0xf
	v_cndmask_b32_dpp v165, v169, v165, vcc quad_perm:[1,0,3,2] row_mask:0xf bank_mask:0xf
	s_mov_b32 vcc_lo, 0xcccccccc
	s_mov_b32 vcc_hi, 0xcccccccc
	s_nop 1
	v_cndmask_b32_dpp v158, v154, v162, vcc quad_perm:[2,3,0,1] row_mask:0xf bank_mask:0xf
	v_cndmask_b32_dpp v166, v170, v174, vcc quad_perm:[2,3,0,1] row_mask:0xf bank_mask:0xf
	v_cndmask_b32_dpp v159, v155, v163, vcc quad_perm:[2,3,0,1] row_mask:0xf bank_mask:0xf
	v_cndmask_b32_dpp v167, v171, v175, vcc quad_perm:[2,3,0,1] row_mask:0xf bank_mask:0xf
	v_cndmask_b32_dpp v160, v156, v164, vcc quad_perm:[2,3,0,1] row_mask:0xf bank_mask:0xf
	v_cndmask_b32_dpp v168, v172, v176, vcc quad_perm:[2,3,0,1] row_mask:0xf bank_mask:0xf
	v_cndmask_b32_dpp v161, v157, v165, vcc quad_perm:[2,3,0,1] row_mask:0xf bank_mask:0xf
	v_cndmask_b32_dpp v169, v173, v177, vcc quad_perm:[2,3,0,1] row_mask:0xf bank_mask:0xf
	s_mov_b32 vcc_lo, 0x33333333
	s_mov_b32 vcc_hi, 0x33333333
	s_nop 1
	v_cndmask_b32_dpp v154, v162, v154, vcc quad_perm:[2,3,0,1] row_mask:0xf bank_mask:0xf
	v_cndmask_b32_dpp v170, v174, v170, vcc quad_perm:[2,3,0,1] row_mask:0xf bank_mask:0xf
	v_cndmask_b32_dpp v155, v163, v155, vcc quad_perm:[2,3,0,1] row_mask:0xf bank_mask:0xf
	v_cndmask_b32_dpp v171, v175, v171, vcc quad_perm:[2,3,0,1] row_mask:0xf bank_mask:0xf
	v_cndmask_b32_dpp v156, v164, v156, vcc quad_perm:[2,3,0,1] row_mask:0xf bank_mask:0xf
	v_cndmask_b32_dpp v172, v176, v172, vcc quad_perm:[2,3,0,1] row_mask:0xf bank_mask:0xf
	v_cndmask_b32_dpp v157, v165, v157, vcc quad_perm:[2,3,0,1] row_mask:0xf bank_mask:0xf
	v_cndmask_b32_dpp v173, v177, v173, vcc quad_perm:[2,3,0,1] row_mask:0xf bank_mask:0xf
	global_store_dwordx4 v179, v[154:157], s[82:83] nt
	global_store_dwordx4 v180, v[170:173], s[82:83] nt
	global_store_dwordx4 v181, v[158:161], s[82:83] nt
	global_store_dwordx4 v190, v[166:169], s[82:83] nt
	v_readlane_b32 s2, v239, 0
	s_lshr_b32 s2, s2, 6
	s_add_i32 s2, s2, 6
	s_cmp_gt_u32 s2, 11
	s_cbranch_scc1 .Lhw_seam1_done
	s_add_i32 s2, s2, 12
	s_mul_i32 s2, s2, s74
	v_readlane_b32 s9, v239, 23
	s_lshr_b32 s9, s9, 3
	s_add_i32 s2, s2, s9
	s_cmp_gt_u32 s2, 24575
	s_cbranch_scc1 .Lhw_seam1_done
	v_mbcnt_lo_u32_b32 v178, -1, 0
	v_mbcnt_hi_u32_b32 v178, -1, v178
	v_and_b32_e32 v179, 60, v178
	v_lshlrev_b32_e32 v179, 10, v179
	v_and_b32_e32 v180, 3, v178
	v_lshl_or_b32 v179, v180, 4, v179
	v_add_u32_e32 v180, 0x400, v179
	v_add_u32_e32 v181, 0x800, v179
	v_add_u32_e32 v190, 0xc00, v179
	v_lshlrev_b32_e32 v178, 2, v178
	s_cmp_lt_u32 s2, 16384
	s_cbranch_scc0 .Lhw_dn_s1_1
	s_lshr_b32 s9, s2, 9
	s_bfe_u32 s32, s2, 0x40005
	s_and_b32 s53, s2, 31
	s_lshl_b32 s69, s9, 23
	s_lshl_b32 s100, s32, 19
	s_add_i32 s69, s69, s100
	s_lshl_b32 s100, s53, 8
	s_add_i32 s69, s69, s100
	s_lshl_b32 s98, s9, 11
	s_bfe_u32 s100, s53, 0x30001
	s_lshl_b32 s100, s100, 8
	s_add_i32 s98, s98, s100
	s_lshr_b32 s100, s53, 4
	s_lshl_b32 s100, s100, 7
	s_add_i32 s98, s98, s100
	s_and_b32 s100, s53, 1
	s_lshl_b32 s100, s100, 6
	s_add_i32 s98, s98, s100
	s_lshl_b32 s98, s98, 10
	s_lshl_b32 s100, s32, 6
	s_add_i32 s98, s98, s100
	s_add_i32 s98, s98, 0x2000000
	v_readlane_b32 s82, v239, 11
	v_readlane_b32 s83, v239, 12
	s_movk_i32 s89, 8192
	s_branch .Lhw_go_s1_1

.Lhw_seam2:
	s_mov_b64 exec, -1
	v_readlane_b32 s2, v239, 0
	s_lshr_b32 s2, s2, 6
	s_add_i32 s2, s2, -1
	s_cmp_gt_u32 s2, 11
	s_cbranch_scc1 .Lhw_seam2_done
	s_add_i32 s2, s2, 24
	s_mul_i32 s2, s2, s74
	v_readlane_b32 s9, v239, 23
	s_lshr_b32 s9, s9, 3
	s_add_i32 s2, s2, s9
	s_cmp_gt_u32 s2, 24575
	s_cbranch_scc1 .Lhw_seam2_done
	v_mbcnt_lo_u32_b32 v178, -1, 0
	v_mbcnt_hi_u32_b32 v178, -1, v178
	v_and_b32_e32 v179, 60, v178
	v_lshlrev_b32_e32 v179, 10, v179
	v_and_b32_e32 v180, 3, v178
	v_lshl_or_b32 v179, v180, 4, v179
	v_add_u32_e32 v180, 0x400, v179
	v_add_u32_e32 v181, 0x800, v179
	v_add_u32_e32 v190, 0xc00, v179
	v_lshlrev_b32_e32 v178, 2, v178
	s_cmp_lt_u32 s2, 16384
	s_cbranch_scc0 .Lhw_dn_s2_0
	s_lshr_b32 s9, s2, 9
	s_bfe_u32 s32, s2, 0x40005
	s_and_b32 s53, s2, 31
	s_lshl_b32 s69, s9, 23
	s_lshl_b32 s100, s32, 19
	s_add_i32 s69, s69, s100
	s_lshl_b32 s100, s53, 8
	s_add_i32 s69, s69, s100
	s_lshl_b32 s98, s9, 11
	s_bfe_u32 s100, s53, 0x30001
	s_lshl_b32 s100, s100, 8
	s_add_i32 s98, s98, s100
	s_lshr_b32 s100, s53, 4
	s_lshl_b32 s100, s100, 7
	s_add_i32 s98, s98, s100
	s_and_b32 s100, s53, 1
	s_lshl_b32 s100, s100, 6
	s_add_i32 s98, s98, s100
	s_lshl_b32 s98, s98, 10
	s_lshl_b32 s100, s32, 6
	s_add_i32 s98, s98, s100
	s_add_i32 s98, s98, 0x2000000
	v_readlane_b32 s82, v239, 11
	v_readlane_b32 s83, v239, 12
	s_movk_i32 s89, 8192
	s_branch .Lhw_go_s2_0

.Lhw_go_s2_0:
	s_add_u32 s100, s82, s69
	s_addc_u32 s101, s83, 0
	v_readlane_b32 s82, v239, 44
	v_readlane_b32 s83, v239, 45
	s_add_u32 s82, s82, s98
	s_addc_u32 s83, s83, 0
	global_load_dword v34, v178, s[100:101] nt
	s_add_u32 s100, s100, s89
	s_addc_u32 s101, s101, 0
	global_load_dword v35, v178, s[100:101] nt
	s_add_u32 s100, s100, s89
	s_addc_u32 s101, s101, 0
	global_load_dword v36, v178, s[100:101] nt
	s_add_u32 s100, s100, s89
	s_addc_u32 s101, s101, 0
	global_load_dword v37, v178, s[100:101] nt
	s_add_u32 s100, s100, s89
	s_addc_u32 s101, s101, 0
	global_load_dword v38, v178, s[100:101] nt
	s_add_u32 s100, s100, s89
	s_addc_u32 s101, s101, 0
	global_load_dword v39, v178, s[100:101] nt
	s_add_u32 s100, s100, s89
	s_addc_u32 s101, s101, 0
	global_load_dword v40, v178, s[100:101] nt
	s_add_u32 s100, s100, s89
	s_addc_u32 s101, s101, 0
	global_load_dword v41, v178, s[100:101] nt
	s_add_u32 s100, s100, s89
	s_addc_u32 s101, s101, 0
	global_load_dword v42, v178, s[100:101] nt
	s_add_u32 s100, s100, s89
	s_addc_u32 s101, s101, 0
	global_load_dword v43, v178, s[100:101] nt
	s_add_u32 s100, s100, s89
	s_addc_u32 s101, s101, 0
	global_load_dword v44, v178, s[100:101] nt
	s_add_u32 s100, s100, s89
	s_addc_u32 s101, s101, 0
	global_load_dword v45, v178, s[100:101] nt
	s_add_u32 s100, s100, s89
	s_addc_u32 s101, s101, 0
	global_load_dword v46, v178, s[100:101] nt
	s_add_u32 s100, s100, s89
	s_addc_u32 s101, s101, 0
	global_load_dword v47, v178, s[100:101] nt
	s_add_u32 s100, s100, s89
	s_addc_u32 s101, s101, 0
	global_load_dword v48, v178, s[100:101] nt
	s_add_u32 s100, s100, s89
	s_addc_u32 s101, s101, 0
	global_load_dword v49, v178, s[100:101] nt
	s_add_u32 s100, s100, s89
	s_addc_u32 s101, s101, 0
	global_load_dword v50, v178, s[100:101] nt
	s_add_u32 s100, s100, s89
	s_addc_u32 s101, s101, 0
	global_load_dword v51, v178, s[100:101] nt
	s_add_u32 s100, s100, s89
	s_addc_u32 s101, s101, 0
	global_load_dword v52, v178, s[100:101] nt
	s_add_u32 s100, s100, s89
	s_addc_u32 s101, s101, 0
	global_load_dword v53, v178, s[100:101] nt
	s_add_u32 s100, s100, s89
	s_addc_u32 s101, s101, 0
	global_load_dword v54, v178, s[100:101] nt
	s_add_u32 s100, s100, s89
	s_addc_u32 s101, s101, 0
	global_load_dword v55, v178, s[100:101] nt
	s_add_u32 s100, s100, s89
	s_addc_u32 s101, s101, 0
	global_load_dword v56, v178, s[100:101] nt
	s_add_u32 s100, s100, s89
	s_addc_u32 s101, s101, 0
	global_load_dword v57, v178, s[100:101] nt
	s_add_u32 s100, s100, s89
	s_addc_u32 s101, s101, 0
	global_load_dword v58, v178, s[100:101] nt
	s_add_u32 s100, s100, s89
	s_addc_u32 s101, s101, 0
	global_load_dword v59, v178, s[100:101] nt
	s_add_u32 s100, s100, s89
	s_addc_u32 s101, s101, 0
	global_load_dword v60, v178, s[100:101] nt
	s_add_u32 s100, s100, s89
	s_addc_u32 s101, s101, 0
	global_load_dword v61, v178, s[100:101] nt
	s_add_u32 s100, s100, s89
	s_addc_u32 s101, s101, 0
	global_load_dword v62, v178, s[100:101] nt
	s_add_u32 s100, s100, s89
	s_addc_u32 s101, s101, 0
	global_load_dword v63, v178, s[100:101] nt
	s_add_u32 s100, s100, s89
	s_addc_u32 s101, s101, 0
	global_load_dword v64, v178, s[100:101] nt
	s_add_u32 s100, s100, s89
	s_addc_u32 s101, s101, 0
	global_load_dword v65, v178, s[100:101] nt
	s_add_u32 s100, s100, s89
	s_addc_u32 s101, s101, 0
	global_load_dword v66, v178, s[100:101] nt
	s_add_u32 s100, s100, s89
	s_addc_u32 s101, s101, 0
	global_load_dword v67, v178, s[100:101] nt
	s_add_u32 s100, s100, s89
	s_addc_u32 s101, s101, 0
	global_load_dword v68, v178, s[100:101] nt
	s_add_u32 s100, s100, s89
	s_addc_u32 s101, s101, 0
	global_load_dword v69, v178, s[100:101] nt
	s_add_u32 s100, s100, s89
	s_addc_u32 s101, s101, 0
	global_load_dword v70, v178, s[100:101] nt
	s_add_u32 s100, s100, s89
	s_addc_u32 s101, s101, 0
	global_load_dword v71, v178, s[100:101] nt
	s_add_u32 s100, s100, s89
	s_addc_u32 s101, s101, 0
	global_load_dword v72, v178, s[100:101] nt
	s_add_u32 s100, s100, s89
	s_addc_u32 s101, s101, 0
	global_load_dword v73, v178, s[100:101] nt
	s_add_u32 s100, s100, s89
	s_addc_u32 s101, s101, 0
	global_load_dword v74, v178, s[100:101] nt
	s_add_u32 s100, s100, s89
	s_addc_u32 s101, s101, 0
	global_load_dword v75, v178, s[100:101] nt
	s_add_u32 s100, s100, s89
	s_addc_u32 s101, s101, 0
	global_load_dword v76, v178, s[100:101] nt
	s_add_u32 s100, s100, s89
	s_addc_u32 s101, s101, 0
	global_load_dword v77, v178, s[100:101] nt
	s_add_u32 s100, s100, s89
	s_addc_u32 s101, s101, 0
	global_load_dword v78, v178, s[100:101] nt
	s_add_u32 s100, s100, s89
	s_addc_u32 s101, s101, 0
	global_load_dword v79, v178, s[100:101] nt
	s_add_u32 s100, s100, s89
	s_addc_u32 s101, s101, 0
	global_load_dword v80, v178, s[100:101] nt
	s_add_u32 s100, s100, s89
	s_addc_u32 s101, s101, 0
	global_load_dword v81, v178, s[100:101] nt
	s_add_u32 s100, s100, s89
	s_addc_u32 s101, s101, 0
	global_load_dword v82, v178, s[100:101] nt
	s_add_u32 s100, s100, s89
	s_addc_u32 s101, s101, 0
	global_load_dword v83, v178, s[100:101] nt
	s_add_u32 s100, s100, s89
	s_addc_u32 s101, s101, 0
	global_load_dword v84, v178, s[100:101] nt
	s_add_u32 s100, s100, s89
	s_addc_u32 s101, s101, 0
	global_load_dword v85, v178, s[100:101] nt
	s_add_u32 s100, s100, s89
	s_addc_u32 s101, s101, 0
	global_load_dword v86, v178, s[100:101] nt
	s_add_u32 s100, s100, s89
	s_addc_u32 s101, s101, 0
	global_load_dword v87, v178, s[100:101] nt
	s_add_u32 s100, s100, s89
	s_addc_u32 s101, s101, 0
	global_load_dword v88, v178, s[100:101] nt
	s_add_u32 s100, s100, s89
	s_addc_u32 s101, s101, 0
	global_load_dword v89, v178, s[100:101] nt
	s_add_u32 s100, s100, s89
	s_addc_u32 s101, s101, 0
	global_load_dword v90, v178, s[100:101] nt
	s_add_u32 s100, s100, s89
	s_addc_u32 s101, s101, 0
	global_load_dword v91, v178, s[100:101] nt
	s_add_u32 s100, s100, s89
	s_addc_u32 s101, s101, 0
	global_load_dword v92, v178, s[100:101] nt
	s_add_u32 s100, s100, s89
	s_addc_u32 s101, s101, 0
	global_load_dword v93, v178, s[100:101] nt
	s_add_u32 s100, s100, s89
	s_addc_u32 s101, s101, 0
	global_load_dword v94, v178, s[100:101] nt
	s_add_u32 s100, s100, s89
	s_addc_u32 s101, s101, 0
	global_load_dword v95, v178, s[100:101] nt
	s_add_u32 s100, s100, s89
	s_addc_u32 s101, s101, 0
	global_load_dword v96, v178, s[100:101] nt
	s_add_u32 s100, s100, s89
	s_addc_u32 s101, s101, 0
	global_load_dword v97, v178, s[100:101] nt
	s_add_u32 s100, s100, s89
	s_addc_u32 s101, s101, 0
	s_waitcnt vmcnt(48)
	v_mul_f32_e32 v34, 0x42000000, v34
	v_mul_f32_e32 v35, 0x42000000, v35
	v_mul_f32_e32 v36, 0x42000000, v36
	v_mul_f32_e32 v37, 0x42000000, v37
	v_mul_f32_e32 v38, 0x42000000, v38
	v_mul_f32_e32 v39, 0x42000000, v39
	v_mul_f32_e32 v40, 0x42000000, v40
	v_mul_f32_e32 v41, 0x42000000, v41
	v_mul_f32_e32 v42, 0x42000000, v42
	v_mul_f32_e32 v43, 0x42000000, v43
	v_mul_f32_e32 v44, 0x42000000, v44
	v_mul_f32_e32 v45, 0x42000000, v45
	v_mul_f32_e32 v46, 0x42000000, v46
	v_mul_f32_e32 v47, 0x42000000, v47
	v_mul_f32_e32 v48, 0x42000000, v48
	v_mul_f32_e32 v49, 0x42000000, v49
	v_cvt_pk_fp8_f32 v154, v34, v35
	v_cvt_pk_fp8_f32 v155, v38, v39
	v_cvt_pk_fp8_f32 v156, v42, v43
	v_cvt_pk_fp8_f32 v157, v46, v47
	v_cvt_pk_fp8_f32 v154, v36, v37 op_sel:[0,0,1]
	v_cvt_pk_fp8_f32 v155, v40, v41 op_sel:[0,0,1]
	v_cvt_pk_fp8_f32 v156, v44, v45 op_sel:[0,0,1]
	v_cvt_pk_fp8_f32 v157, v48, v49 op_sel:[0,0,1]
	s_waitcnt vmcnt(32)
	v_mul_f32_e32 v50, 0x42000000, v50
	v_mul_f32_e32 v51, 0x42000000, v51
	v_mul_f32_e32 v52, 0x42000000, v52
	v_mul_f32_e32 v53, 0x42000000, v53
	v_mul_f32_e32 v54, 0x42000000, v54
	v_mul_f32_e32 v55, 0x42000000, v55
	v_mul_f32_e32 v56, 0x42000000, v56
	v_mul_f32_e32 v57, 0x42000000, v57
	v_mul_f32_e32 v58, 0x42000000, v58
	v_mul_f32_e32 v59, 0x42000000, v59
	v_mul_f32_e32 v60, 0x42000000, v60
	v_mul_f32_e32 v61, 0x42000000, v61
	v_mul_f32_e32 v62, 0x42000000, v62
	v_mul_f32_e32 v63, 0x42000000, v63
	v_mul_f32_e32 v64, 0x42000000, v64
	v_mul_f32_e32 v65, 0x42000000, v65
	v_cvt_pk_fp8_f32 v158, v50, v51
	v_cvt_pk_fp8_f32 v159, v54, v55
	v_cvt_pk_fp8_f32 v160, v58, v59
	v_cvt_pk_fp8_f32 v161, v62, v63
	v_cvt_pk_fp8_f32 v158, v52, v53 op_sel:[0,0,1]
	v_cvt_pk_fp8_f32 v159, v56, v57 op_sel:[0,0,1]
	v_cvt_pk_fp8_f32 v160, v60, v61 op_sel:[0,0,1]
	v_cvt_pk_fp8_f32 v161, v64, v65 op_sel:[0,0,1]
	s_waitcnt vmcnt(16)
	v_mul_f32_e32 v66, 0x42000000, v66
	v_mul_f32_e32 v67, 0x42000000, v67
	v_mul_f32_e32 v68, 0x42000000, v68
	v_mul_f32_e32 v69, 0x42000000, v69
	v_mul_f32_e32 v70, 0x42000000, v70
	v_mul_f32_e32 v71, 0x42000000, v71
	v_mul_f32_e32 v72, 0x42000000, v72
	v_mul_f32_e32 v73, 0x42000000, v73
	v_mul_f32_e32 v74, 0x42000000, v74
	v_mul_f32_e32 v75, 0x42000000, v75
	v_mul_f32_e32 v76, 0x42000000, v76
	v_mul_f32_e32 v77, 0x42000000, v77
	v_mul_f32_e32 v78, 0x42000000, v78
	v_mul_f32_e32 v79, 0x42000000, v79
	v_mul_f32_e32 v80, 0x42000000, v80
	v_mul_f32_e32 v81, 0x42000000, v81
	v_cvt_pk_fp8_f32 v162, v66, v67
	v_cvt_pk_fp8_f32 v163, v70, v71
	v_cvt_pk_fp8_f32 v164, v74, v75
	v_cvt_pk_fp8_f32 v165, v78, v79
	v_cvt_pk_fp8_f32 v162, v68, v69 op_sel:[0,0,1]
	v_cvt_pk_fp8_f32 v163, v72, v73 op_sel:[0,0,1]
	v_cvt_pk_fp8_f32 v164, v76, v77 op_sel:[0,0,1]
	v_cvt_pk_fp8_f32 v165, v80, v81 op_sel:[0,0,1]
	s_waitcnt vmcnt(0)
	v_mul_f32_e32 v82, 0x42000000, v82
	v_mul_f32_e32 v83, 0x42000000, v83
	v_mul_f32_e32 v84, 0x42000000, v84
	v_mul_f32_e32 v85, 0x42000000, v85
	v_mul_f32_e32 v86, 0x42000000, v86
	v_mul_f32_e32 v87, 0x42000000, v87
	v_mul_f32_e32 v88, 0x42000000, v88
	v_mul_f32_e32 v89, 0x42000000, v89
	v_mul_f32_e32 v90, 0x42000000, v90
	v_mul_f32_e32 v91, 0x42000000, v91
	v_mul_f32_e32 v92, 0x42000000, v92
	v_mul_f32_e32 v93, 0x42000000, v93
	v_mul_f32_e32 v94, 0x42000000, v94
	v_mul_f32_e32 v95, 0x42000000, v95
	v_mul_f32_e32 v96, 0x42000000, v96
	v_mul_f32_e32 v97, 0x42000000, v97
	v_cvt_pk_fp8_f32 v166, v82, v83
	v_cvt_pk_fp8_f32 v167, v86, v87
	v_cvt_pk_fp8_f32 v168, v90, v91
	v_cvt_pk_fp8_f32 v169, v94, v95
	v_cvt_pk_fp8_f32 v166, v84, v85 op_sel:[0,0,1]
	v_cvt_pk_fp8_f32 v167, v88, v89 op_sel:[0,0,1]
	v_cvt_pk_fp8_f32 v168, v92, v93 op_sel:[0,0,1]
	v_cvt_pk_fp8_f32 v169, v96, v97 op_sel:[0,0,1]
	s_mov_b32 vcc_lo, 0xaaaaaaaa
	s_mov_b32 vcc_hi, 0xaaaaaaaa
	s_nop 1
	v_cndmask_b32_dpp v170, v154, v158, vcc quad_perm:[1,0,3,2] row_mask:0xf bank_mask:0xf
	v_cndmask_b32_dpp v174, v162, v166, vcc quad_perm:[1,0,3,2] row_mask:0xf bank_mask:0xf
	v_cndmask_b32_dpp v171, v155, v159, vcc quad_perm:[1,0,3,2] row_mask:0xf bank_mask:0xf
	v_cndmask_b32_dpp v175, v163, v167, vcc quad_perm:[1,0,3,2] row_mask:0xf bank_mask:0xf
	v_cndmask_b32_dpp v172, v156, v160, vcc quad_perm:[1,0,3,2] row_mask:0xf bank_mask:0xf
	v_cndmask_b32_dpp v176, v164, v168, vcc quad_perm:[1,0,3,2] row_mask:0xf bank_mask:0xf
	v_cndmask_b32_dpp v173, v157, v161, vcc quad_perm:[1,0,3,2] row_mask:0xf bank_mask:0xf
	v_cndmask_b32_dpp v177, v165, v169, vcc quad_perm:[1,0,3,2] row_mask:0xf bank_mask:0xf
	s_mov_b32 vcc_lo, 0x55555555
	s_mov_b32 vcc_hi, 0x55555555
	s_nop 1
	v_cndmask_b32_dpp v154, v158, v154, vcc quad_perm:[1,0,3,2] row_mask:0xf bank_mask:0xf
	v_cndmask_b32_dpp v162, v166, v162, vcc quad_perm:[1,0,3,2] row_mask:0xf bank_mask:0xf
	v_cndmask_b32_dpp v155, v159, v155, vcc quad_perm:[1,0,3,2] row_mask:0xf bank_mask:0xf
	v_cndmask_b32_dpp v163, v167, v163, vcc quad_perm:[1,0,3,2] row_mask:0xf bank_mask:0xf
	v_cndmask_b32_dpp v156, v160, v156, vcc quad_perm:[1,0,3,2] row_mask:0xf bank_mask:0xf
	v_cndmask_b32_dpp v164, v168, v164, vcc quad_perm:[1,0,3,2] row_mask:0xf bank_mask:0xf
	v_cndmask_b32_dpp v157, v161, v157, vcc quad_perm:[1,0,3,2] row_mask:0xf bank_mask:0xf
	v_cndmask_b32_dpp v165, v169, v165, vcc quad_perm:[1,0,3,2] row_mask:0xf bank_mask:0xf
	s_mov_b32 vcc_lo, 0xcccccccc
	s_mov_b32 vcc_hi, 0xcccccccc
	s_nop 1
	v_cndmask_b32_dpp v158, v154, v162, vcc quad_perm:[2,3,0,1] row_mask:0xf bank_mask:0xf
	v_cndmask_b32_dpp v166, v170, v174, vcc quad_perm:[2,3,0,1] row_mask:0xf bank_mask:0xf
	v_cndmask_b32_dpp v159, v155, v163, vcc quad_perm:[2,3,0,1] row_mask:0xf bank_mask:0xf
	v_cndmask_b32_dpp v167, v171, v175, vcc quad_perm:[2,3,0,1] row_mask:0xf bank_mask:0xf
	v_cndmask_b32_dpp v160, v156, v164, vcc quad_perm:[2,3,0,1] row_mask:0xf bank_mask:0xf
	v_cndmask_b32_dpp v168, v172, v176, vcc quad_perm:[2,3,0,1] row_mask:0xf bank_mask:0xf
	v_cndmask_b32_dpp v161, v157, v165, vcc quad_perm:[2,3,0,1] row_mask:0xf bank_mask:0xf
	v_cndmask_b32_dpp v169, v173, v177, vcc quad_perm:[2,3,0,1] row_mask:0xf bank_mask:0xf
	s_mov_b32 vcc_lo, 0x33333333
	s_mov_b32 vcc_hi, 0x33333333
	s_nop 1
	v_cndmask_b32_dpp v154, v162, v154, vcc quad_perm:[2,3,0,1] row_mask:0xf bank_mask:0xf
	v_cndmask_b32_dpp v170, v174, v170, vcc quad_perm:[2,3,0,1] row_mask:0xf bank_mask:0xf
	v_cndmask_b32_dpp v155, v163, v155, vcc quad_perm:[2,3,0,1] row_mask:0xf bank_mask:0xf
	v_cndmask_b32_dpp v171, v175, v171, vcc quad_perm:[2,3,0,1] row_mask:0xf bank_mask:0xf
	v_cndmask_b32_dpp v156, v164, v156, vcc quad_perm:[2,3,0,1] row_mask:0xf bank_mask:0xf
	v_cndmask_b32_dpp v172, v176, v172, vcc quad_perm:[2,3,0,1] row_mask:0xf bank_mask:0xf
	v_cndmask_b32_dpp v157, v165, v157, vcc quad_perm:[2,3,0,1] row_mask:0xf bank_mask:0xf
	v_cndmask_b32_dpp v173, v177, v173, vcc quad_perm:[2,3,0,1] row_mask:0xf bank_mask:0xf
	global_store_dwordx4 v179, v[154:157], s[82:83] nt
	global_store_dwordx4 v180, v[170:173], s[82:83] nt
	global_store_dwordx4 v181, v[158:161], s[82:83] nt
	global_store_dwordx4 v190, v[166:169], s[82:83] nt
	v_readlane_b32 s2, v239, 0
	s_lshr_b32 s2, s2, 6
	s_add_i32 s2, s2, 6
	s_cmp_gt_u32 s2, 11
	s_cbranch_scc1 .Lhw_seam2_done
	s_add_i32 s2, s2, 24
	s_mul_i32 s2, s2, s74
	v_readlane_b32 s9, v239, 23
	s_lshr_b32 s9, s9, 3
	s_add_i32 s2, s2, s9
	s_cmp_gt_u32 s2, 24575
	s_cbranch_scc1 .Lhw_seam2_done
	v_mbcnt_lo_u32_b32 v178, -1, 0
	v_mbcnt_hi_u32_b32 v178, -1, v178
	v_and_b32_e32 v179, 60, v178
	v_lshlrev_b32_e32 v179, 10, v179
	v_and_b32_e32 v180, 3, v178
	v_lshl_or_b32 v179, v180, 4, v179
	v_add_u32_e32 v180, 0x400, v179
	v_add_u32_e32 v181, 0x800, v179
	v_add_u32_e32 v190, 0xc00, v179
	v_lshlrev_b32_e32 v178, 2, v178
	s_cmp_lt_u32 s2, 16384
	s_cbranch_scc0 .Lhw_dn_s2_1
	s_lshr_b32 s9, s2, 9
	s_bfe_u32 s32, s2, 0x40005
	s_and_b32 s53, s2, 31
	s_lshl_b32 s69, s9, 23
	s_lshl_b32 s100, s32, 19
	s_add_i32 s69, s69, s100
	s_lshl_b32 s100, s53, 8
	s_add_i32 s69, s69, s100
	s_lshl_b32 s98, s9, 11
	s_bfe_u32 s100, s53, 0x30001
	s_lshl_b32 s100, s100, 8
	s_add_i32 s98, s98, s100
	s_lshr_b32 s100, s53, 4
	s_lshl_b32 s100, s100, 7
	s_add_i32 s98, s98, s100
	s_and_b32 s100, s53, 1
	s_lshl_b32 s100, s100, 6
	s_add_i32 s98, s98, s100
	s_lshl_b32 s98, s98, 10
	s_lshl_b32 s100, s32, 6
	s_add_i32 s98, s98, s100
	s_add_i32 s98, s98, 0x2000000
	v_readlane_b32 s82, v239, 11
	v_readlane_b32 s83, v239, 12
	s_movk_i32 s89, 8192
	s_branch .Lhw_go_s2_1

.Lhw_seam3:
	s_mov_b64 exec, -1
	v_readlane_b32 s2, v239, 0
	s_lshr_b32 s2, s2, 6
	s_add_i32 s2, s2, -1
	s_cmp_gt_u32 s2, 11
	s_cbranch_scc1 .Lhw_seam3_done
	s_add_i32 s2, s2, 36
	s_mul_i32 s2, s2, s74
	v_readlane_b32 s9, v239, 23
	s_lshr_b32 s9, s9, 3
	s_add_i32 s2, s2, s9
	s_cmp_gt_u32 s2, 24575
	s_cbranch_scc1 .Lhw_seam3_done
	v_mbcnt_lo_u32_b32 v178, -1, 0
	v_mbcnt_hi_u32_b32 v178, -1, v178
	v_and_b32_e32 v179, 60, v178
	v_lshlrev_b32_e32 v179, 10, v179
	v_and_b32_e32 v180, 3, v178
	v_lshl_or_b32 v179, v180, 4, v179
	v_add_u32_e32 v180, 0x400, v179
	v_add_u32_e32 v181, 0x800, v179
	v_add_u32_e32 v190, 0xc00, v179
	v_lshlrev_b32_e32 v178, 2, v178
	s_cmp_lt_u32 s2, 16384
	s_cbranch_scc0 .Lhw_dn_s3_0
	s_lshr_b32 s9, s2, 9
	s_bfe_u32 s32, s2, 0x40005
	s_and_b32 s53, s2, 31
	s_lshl_b32 s69, s9, 23
	s_lshl_b32 s100, s32, 19
	s_add_i32 s69, s69, s100
	s_lshl_b32 s100, s53, 8
	s_add_i32 s69, s69, s100
	s_lshl_b32 s98, s9, 11
	s_bfe_u32 s100, s53, 0x30001
	s_lshl_b32 s100, s100, 8
	s_add_i32 s98, s98, s100
	s_lshr_b32 s100, s53, 4
	s_lshl_b32 s100, s100, 7
	s_add_i32 s98, s98, s100
	s_and_b32 s100, s53, 1
	s_lshl_b32 s100, s100, 6
	s_add_i32 s98, s98, s100
	s_lshl_b32 s98, s98, 10
	s_lshl_b32 s100, s32, 6
	s_add_i32 s98, s98, s100
	s_add_i32 s98, s98, 0x2000000
	v_readlane_b32 s82, v239, 11
	v_readlane_b32 s83, v239, 12
	s_movk_i32 s89, 8192
	s_branch .Lhw_go_s3_0

.Lhw_go_s3_0:
	s_add_u32 s100, s82, s69
	s_addc_u32 s101, s83, 0
	v_readlane_b32 s82, v239, 44
	v_readlane_b32 s83, v239, 45
	s_add_u32 s82, s82, s98
	s_addc_u32 s83, s83, 0
	global_load_dword v34, v178, s[100:101] nt
	s_add_u32 s100, s100, s89
	s_addc_u32 s101, s101, 0
	global_load_dword v35, v178, s[100:101] nt
	s_add_u32 s100, s100, s89
	s_addc_u32 s101, s101, 0
	global_load_dword v36, v178, s[100:101] nt
	s_add_u32 s100, s100, s89
	s_addc_u32 s101, s101, 0
	global_load_dword v37, v178, s[100:101] nt
	s_add_u32 s100, s100, s89
	s_addc_u32 s101, s101, 0
	global_load_dword v38, v178, s[100:101] nt
	s_add_u32 s100, s100, s89
	s_addc_u32 s101, s101, 0
	global_load_dword v39, v178, s[100:101] nt
	s_add_u32 s100, s100, s89
	s_addc_u32 s101, s101, 0
	global_load_dword v40, v178, s[100:101] nt
	s_add_u32 s100, s100, s89
	s_addc_u32 s101, s101, 0
	global_load_dword v41, v178, s[100:101] nt
	s_add_u32 s100, s100, s89
	s_addc_u32 s101, s101, 0
	global_load_dword v42, v178, s[100:101] nt
	s_add_u32 s100, s100, s89
	s_addc_u32 s101, s101, 0
	global_load_dword v43, v178, s[100:101] nt
	s_add_u32 s100, s100, s89
	s_addc_u32 s101, s101, 0
	global_load_dword v44, v178, s[100:101] nt
	s_add_u32 s100, s100, s89
	s_addc_u32 s101, s101, 0
	global_load_dword v45, v178, s[100:101] nt
	s_add_u32 s100, s100, s89
	s_addc_u32 s101, s101, 0
	global_load_dword v46, v178, s[100:101] nt
	s_add_u32 s100, s100, s89
	s_addc_u32 s101, s101, 0
	global_load_dword v47, v178, s[100:101] nt
	s_add_u32 s100, s100, s89
	s_addc_u32 s101, s101, 0
	global_load_dword v48, v178, s[100:101] nt
	s_add_u32 s100, s100, s89
	s_addc_u32 s101, s101, 0
	global_load_dword v49, v178, s[100:101] nt
	s_add_u32 s100, s100, s89
	s_addc_u32 s101, s101, 0
	global_load_dword v50, v178, s[100:101] nt
	s_add_u32 s100, s100, s89
	s_addc_u32 s101, s101, 0
	global_load_dword v51, v178, s[100:101] nt
	s_add_u32 s100, s100, s89
	s_addc_u32 s101, s101, 0
	global_load_dword v52, v178, s[100:101] nt
	s_add_u32 s100, s100, s89
	s_addc_u32 s101, s101, 0
	global_load_dword v53, v178, s[100:101] nt
	s_add_u32 s100, s100, s89
	s_addc_u32 s101, s101, 0
	global_load_dword v54, v178, s[100:101] nt
	s_add_u32 s100, s100, s89
	s_addc_u32 s101, s101, 0
	global_load_dword v55, v178, s[100:101] nt
	s_add_u32 s100, s100, s89
	s_addc_u32 s101, s101, 0
	global_load_dword v56, v178, s[100:101] nt
	s_add_u32 s100, s100, s89
	s_addc_u32 s101, s101, 0
	global_load_dword v57, v178, s[100:101] nt
	s_add_u32 s100, s100, s89
	s_addc_u32 s101, s101, 0
	global_load_dword v58, v178, s[100:101] nt
	s_add_u32 s100, s100, s89
	s_addc_u32 s101, s101, 0
	global_load_dword v59, v178, s[100:101] nt
	s_add_u32 s100, s100, s89
	s_addc_u32 s101, s101, 0
	global_load_dword v60, v178, s[100:101] nt
	s_add_u32 s100, s100, s89
	s_addc_u32 s101, s101, 0
	global_load_dword v61, v178, s[100:101] nt
	s_add_u32 s100, s100, s89
	s_addc_u32 s101, s101, 0
	global_load_dword v62, v178, s[100:101] nt
	s_add_u32 s100, s100, s89
	s_addc_u32 s101, s101, 0
	global_load_dword v63, v178, s[100:101] nt
	s_add_u32 s100, s100, s89
	s_addc_u32 s101, s101, 0
	global_load_dword v64, v178, s[100:101] nt
	s_add_u32 s100, s100, s89
	s_addc_u32 s101, s101, 0
	global_load_dword v65, v178, s[100:101] nt
	s_add_u32 s100, s100, s89
	s_addc_u32 s101, s101, 0
	global_load_dword v66, v178, s[100:101] nt
	s_add_u32 s100, s100, s89
	s_addc_u32 s101, s101, 0
	global_load_dword v67, v178, s[100:101] nt
	s_add_u32 s100, s100, s89
	s_addc_u32 s101, s101, 0
	global_load_dword v68, v178, s[100:101] nt
	s_add_u32 s100, s100, s89
	s_addc_u32 s101, s101, 0
	global_load_dword v69, v178, s[100:101] nt
	s_add_u32 s100, s100, s89
	s_addc_u32 s101, s101, 0
	global_load_dword v70, v178, s[100:101] nt
	s_add_u32 s100, s100, s89
	s_addc_u32 s101, s101, 0
	global_load_dword v71, v178, s[100:101] nt
	s_add_u32 s100, s100, s89
	s_addc_u32 s101, s101, 0
	global_load_dword v72, v178, s[100:101] nt
	s_add_u32 s100, s100, s89
	s_addc_u32 s101, s101, 0
	global_load_dword v73, v178, s[100:101] nt
	s_add_u32 s100, s100, s89
	s_addc_u32 s101, s101, 0
	global_load_dword v74, v178, s[100:101] nt
	s_add_u32 s100, s100, s89
	s_addc_u32 s101, s101, 0
	global_load_dword v75, v178, s[100:101] nt
	s_add_u32 s100, s100, s89
	s_addc_u32 s101, s101, 0
	global_load_dword v76, v178, s[100:101] nt
	s_add_u32 s100, s100, s89
	s_addc_u32 s101, s101, 0
	global_load_dword v77, v178, s[100:101] nt
	s_add_u32 s100, s100, s89
	s_addc_u32 s101, s101, 0
	global_load_dword v78, v178, s[100:101] nt
	s_add_u32 s100, s100, s89
	s_addc_u32 s101, s101, 0
	global_load_dword v79, v178, s[100:101] nt
	s_add_u32 s100, s100, s89
	s_addc_u32 s101, s101, 0
	global_load_dword v80, v178, s[100:101] nt
	s_add_u32 s100, s100, s89
	s_addc_u32 s101, s101, 0
	global_load_dword v81, v178, s[100:101] nt
	s_add_u32 s100, s100, s89
	s_addc_u32 s101, s101, 0
	global_load_dword v82, v178, s[100:101] nt
	s_add_u32 s100, s100, s89
	s_addc_u32 s101, s101, 0
	global_load_dword v83, v178, s[100:101] nt
	s_add_u32 s100, s100, s89
	s_addc_u32 s101, s101, 0
	global_load_dword v84, v178, s[100:101] nt
	s_add_u32 s100, s100, s89
	s_addc_u32 s101, s101, 0
	global_load_dword v85, v178, s[100:101] nt
	s_add_u32 s100, s100, s89
	s_addc_u32 s101, s101, 0
	global_load_dword v86, v178, s[100:101] nt
	s_add_u32 s100, s100, s89
	s_addc_u32 s101, s101, 0
	global_load_dword v87, v178, s[100:101] nt
	s_add_u32 s100, s100, s89
	s_addc_u32 s101, s101, 0
	global_load_dword v88, v178, s[100:101] nt
	s_add_u32 s100, s100, s89
	s_addc_u32 s101, s101, 0
	global_load_dword v89, v178, s[100:101] nt
	s_add_u32 s100, s100, s89
	s_addc_u32 s101, s101, 0
	global_load_dword v90, v178, s[100:101] nt
	s_add_u32 s100, s100, s89
	s_addc_u32 s101, s101, 0
	global_load_dword v91, v178, s[100:101] nt
	s_add_u32 s100, s100, s89
	s_addc_u32 s101, s101, 0
	global_load_dword v92, v178, s[100:101] nt
	s_add_u32 s100, s100, s89
	s_addc_u32 s101, s101, 0
	global_load_dword v93, v178, s[100:101] nt
	s_add_u32 s100, s100, s89
	s_addc_u32 s101, s101, 0
	global_load_dword v94, v178, s[100:101] nt
	s_add_u32 s100, s100, s89
	s_addc_u32 s101, s101, 0
	global_load_dword v95, v178, s[100:101] nt
	s_add_u32 s100, s100, s89
	s_addc_u32 s101, s101, 0
	global_load_dword v96, v178, s[100:101] nt
	s_add_u32 s100, s100, s89
	s_addc_u32 s101, s101, 0
	global_load_dword v97, v178, s[100:101] nt
	s_add_u32 s100, s100, s89
	s_addc_u32 s101, s101, 0
	s_waitcnt vmcnt(48)
	v_mul_f32_e32 v34, 0x42000000, v34
	v_mul_f32_e32 v35, 0x42000000, v35
	v_mul_f32_e32 v36, 0x42000000, v36
	v_mul_f32_e32 v37, 0x42000000, v37
	v_mul_f32_e32 v38, 0x42000000, v38
	v_mul_f32_e32 v39, 0x42000000, v39
	v_mul_f32_e32 v40, 0x42000000, v40
	v_mul_f32_e32 v41, 0x42000000, v41
	v_mul_f32_e32 v42, 0x42000000, v42
	v_mul_f32_e32 v43, 0x42000000, v43
	v_mul_f32_e32 v44, 0x42000000, v44
	v_mul_f32_e32 v45, 0x42000000, v45
	v_mul_f32_e32 v46, 0x42000000, v46
	v_mul_f32_e32 v47, 0x42000000, v47
	v_mul_f32_e32 v48, 0x42000000, v48
	v_mul_f32_e32 v49, 0x42000000, v49
	v_cvt_pk_fp8_f32 v154, v34, v35
	v_cvt_pk_fp8_f32 v155, v38, v39
	v_cvt_pk_fp8_f32 v156, v42, v43
	v_cvt_pk_fp8_f32 v157, v46, v47
	v_cvt_pk_fp8_f32 v154, v36, v37 op_sel:[0,0,1]
	v_cvt_pk_fp8_f32 v155, v40, v41 op_sel:[0,0,1]
	v_cvt_pk_fp8_f32 v156, v44, v45 op_sel:[0,0,1]
	v_cvt_pk_fp8_f32 v157, v48, v49 op_sel:[0,0,1]
	s_waitcnt vmcnt(32)
	v_mul_f32_e32 v50, 0x42000000, v50
	v_mul_f32_e32 v51, 0x42000000, v51
	v_mul_f32_e32 v52, 0x42000000, v52
	v_mul_f32_e32 v53, 0x42000000, v53
	v_mul_f32_e32 v54, 0x42000000, v54
	v_mul_f32_e32 v55, 0x42000000, v55
	v_mul_f32_e32 v56, 0x42000000, v56
	v_mul_f32_e32 v57, 0x42000000, v57
	v_mul_f32_e32 v58, 0x42000000, v58
	v_mul_f32_e32 v59, 0x42000000, v59
	v_mul_f32_e32 v60, 0x42000000, v60
	v_mul_f32_e32 v61, 0x42000000, v61
	v_mul_f32_e32 v62, 0x42000000, v62
	v_mul_f32_e32 v63, 0x42000000, v63
	v_mul_f32_e32 v64, 0x42000000, v64
	v_mul_f32_e32 v65, 0x42000000, v65
	v_cvt_pk_fp8_f32 v158, v50, v51
	v_cvt_pk_fp8_f32 v159, v54, v55
	v_cvt_pk_fp8_f32 v160, v58, v59
	v_cvt_pk_fp8_f32 v161, v62, v63
	v_cvt_pk_fp8_f32 v158, v52, v53 op_sel:[0,0,1]
	v_cvt_pk_fp8_f32 v159, v56, v57 op_sel:[0,0,1]
	v_cvt_pk_fp8_f32 v160, v60, v61 op_sel:[0,0,1]
	v_cvt_pk_fp8_f32 v161, v64, v65 op_sel:[0,0,1]
	s_waitcnt vmcnt(16)
	v_mul_f32_e32 v66, 0x42000000, v66
	v_mul_f32_e32 v67, 0x42000000, v67
	v_mul_f32_e32 v68, 0x42000000, v68
	v_mul_f32_e32 v69, 0x42000000, v69
	v_mul_f32_e32 v70, 0x42000000, v70
	v_mul_f32_e32 v71, 0x42000000, v71
	v_mul_f32_e32 v72, 0x42000000, v72
	v_mul_f32_e32 v73, 0x42000000, v73
	v_mul_f32_e32 v74, 0x42000000, v74
	v_mul_f32_e32 v75, 0x42000000, v75
	v_mul_f32_e32 v76, 0x42000000, v76
	v_mul_f32_e32 v77, 0x42000000, v77
	v_mul_f32_e32 v78, 0x42000000, v78
	v_mul_f32_e32 v79, 0x42000000, v79
	v_mul_f32_e32 v80, 0x42000000, v80
	v_mul_f32_e32 v81, 0x42000000, v81
	v_cvt_pk_fp8_f32 v162, v66, v67
	v_cvt_pk_fp8_f32 v163, v70, v71
	v_cvt_pk_fp8_f32 v164, v74, v75
	v_cvt_pk_fp8_f32 v165, v78, v79
	v_cvt_pk_fp8_f32 v162, v68, v69 op_sel:[0,0,1]
	v_cvt_pk_fp8_f32 v163, v72, v73 op_sel:[0,0,1]
	v_cvt_pk_fp8_f32 v164, v76, v77 op_sel:[0,0,1]
	v_cvt_pk_fp8_f32 v165, v80, v81 op_sel:[0,0,1]
	s_waitcnt vmcnt(0)
	v_mul_f32_e32 v82, 0x42000000, v82
	v_mul_f32_e32 v83, 0x42000000, v83
	v_mul_f32_e32 v84, 0x42000000, v84
	v_mul_f32_e32 v85, 0x42000000, v85
	v_mul_f32_e32 v86, 0x42000000, v86
	v_mul_f32_e32 v87, 0x42000000, v87
	v_mul_f32_e32 v88, 0x42000000, v88
	v_mul_f32_e32 v89, 0x42000000, v89
	v_mul_f32_e32 v90, 0x42000000, v90
	v_mul_f32_e32 v91, 0x42000000, v91
	v_mul_f32_e32 v92, 0x42000000, v92
	v_mul_f32_e32 v93, 0x42000000, v93
	v_mul_f32_e32 v94, 0x42000000, v94
	v_mul_f32_e32 v95, 0x42000000, v95
	v_mul_f32_e32 v96, 0x42000000, v96
	v_mul_f32_e32 v97, 0x42000000, v97
	v_cvt_pk_fp8_f32 v166, v82, v83
	v_cvt_pk_fp8_f32 v167, v86, v87
	v_cvt_pk_fp8_f32 v168, v90, v91
	v_cvt_pk_fp8_f32 v169, v94, v95
	v_cvt_pk_fp8_f32 v166, v84, v85 op_sel:[0,0,1]
	v_cvt_pk_fp8_f32 v167, v88, v89 op_sel:[0,0,1]
	v_cvt_pk_fp8_f32 v168, v92, v93 op_sel:[0,0,1]
	v_cvt_pk_fp8_f32 v169, v96, v97 op_sel:[0,0,1]
	s_mov_b32 vcc_lo, 0xaaaaaaaa
	s_mov_b32 vcc_hi, 0xaaaaaaaa
	s_nop 1
	v_cndmask_b32_dpp v170, v154, v158, vcc quad_perm:[1,0,3,2] row_mask:0xf bank_mask:0xf
	v_cndmask_b32_dpp v174, v162, v166, vcc quad_perm:[1,0,3,2] row_mask:0xf bank_mask:0xf
	v_cndmask_b32_dpp v171, v155, v159, vcc quad_perm:[1,0,3,2] row_mask:0xf bank_mask:0xf
	v_cndmask_b32_dpp v175, v163, v167, vcc quad_perm:[1,0,3,2] row_mask:0xf bank_mask:0xf
	v_cndmask_b32_dpp v172, v156, v160, vcc quad_perm:[1,0,3,2] row_mask:0xf bank_mask:0xf
	v_cndmask_b32_dpp v176, v164, v168, vcc quad_perm:[1,0,3,2] row_mask:0xf bank_mask:0xf
	v_cndmask_b32_dpp v173, v157, v161, vcc quad_perm:[1,0,3,2] row_mask:0xf bank_mask:0xf
	v_cndmask_b32_dpp v177, v165, v169, vcc quad_perm:[1,0,3,2] row_mask:0xf bank_mask:0xf
	s_mov_b32 vcc_lo, 0x55555555
	s_mov_b32 vcc_hi, 0x55555555
	s_nop 1
	v_cndmask_b32_dpp v154, v158, v154, vcc quad_perm:[1,0,3,2] row_mask:0xf bank_mask:0xf
	v_cndmask_b32_dpp v162, v166, v162, vcc quad_perm:[1,0,3,2] row_mask:0xf bank_mask:0xf
	v_cndmask_b32_dpp v155, v159, v155, vcc quad_perm:[1,0,3,2] row_mask:0xf bank_mask:0xf
	v_cndmask_b32_dpp v163, v167, v163, vcc quad_perm:[1,0,3,2] row_mask:0xf bank_mask:0xf
	v_cndmask_b32_dpp v156, v160, v156, vcc quad_perm:[1,0,3,2] row_mask:0xf bank_mask:0xf
	v_cndmask_b32_dpp v164, v168, v164, vcc quad_perm:[1,0,3,2] row_mask:0xf bank_mask:0xf
	v_cndmask_b32_dpp v157, v161, v157, vcc quad_perm:[1,0,3,2] row_mask:0xf bank_mask:0xf
	v_cndmask_b32_dpp v165, v169, v165, vcc quad_perm:[1,0,3,2] row_mask:0xf bank_mask:0xf
	s_mov_b32 vcc_lo, 0xcccccccc
	s_mov_b32 vcc_hi, 0xcccccccc
	s_nop 1
	v_cndmask_b32_dpp v158, v154, v162, vcc quad_perm:[2,3,0,1] row_mask:0xf bank_mask:0xf
	v_cndmask_b32_dpp v166, v170, v174, vcc quad_perm:[2,3,0,1] row_mask:0xf bank_mask:0xf
	v_cndmask_b32_dpp v159, v155, v163, vcc quad_perm:[2,3,0,1] row_mask:0xf bank_mask:0xf
	v_cndmask_b32_dpp v167, v171, v175, vcc quad_perm:[2,3,0,1] row_mask:0xf bank_mask:0xf
	v_cndmask_b32_dpp v160, v156, v164, vcc quad_perm:[2,3,0,1] row_mask:0xf bank_mask:0xf
	v_cndmask_b32_dpp v168, v172, v176, vcc quad_perm:[2,3,0,1] row_mask:0xf bank_mask:0xf
	v_cndmask_b32_dpp v161, v157, v165, vcc quad_perm:[2,3,0,1] row_mask:0xf bank_mask:0xf
	v_cndmask_b32_dpp v169, v173, v177, vcc quad_perm:[2,3,0,1] row_mask:0xf bank_mask:0xf
	s_mov_b32 vcc_lo, 0x33333333
	s_mov_b32 vcc_hi, 0x33333333
	s_nop 1
	v_cndmask_b32_dpp v154, v162, v154, vcc quad_perm:[2,3,0,1] row_mask:0xf bank_mask:0xf
	v_cndmask_b32_dpp v170, v174, v170, vcc quad_perm:[2,3,0,1] row_mask:0xf bank_mask:0xf
	v_cndmask_b32_dpp v155, v163, v155, vcc quad_perm:[2,3,0,1] row_mask:0xf bank_mask:0xf
	v_cndmask_b32_dpp v171, v175, v171, vcc quad_perm:[2,3,0,1] row_mask:0xf bank_mask:0xf
	v_cndmask_b32_dpp v156, v164, v156, vcc quad_perm:[2,3,0,1] row_mask:0xf bank_mask:0xf
	v_cndmask_b32_dpp v172, v176, v172, vcc quad_perm:[2,3,0,1] row_mask:0xf bank_mask:0xf
	v_cndmask_b32_dpp v157, v165, v157, vcc quad_perm:[2,3,0,1] row_mask:0xf bank_mask:0xf
	v_cndmask_b32_dpp v173, v177, v173, vcc quad_perm:[2,3,0,1] row_mask:0xf bank_mask:0xf
	global_store_dwordx4 v179, v[154:157], s[82:83] nt
	global_store_dwordx4 v180, v[170:173], s[82:83] nt
	global_store_dwordx4 v181, v[158:161], s[82:83] nt
	global_store_dwordx4 v190, v[166:169], s[82:83] nt
	v_readlane_b32 s2, v239, 0
	s_lshr_b32 s2, s2, 6
	s_add_i32 s2, s2, 6
	s_cmp_gt_u32 s2, 11
	s_cbranch_scc1 .Lhw_seam3_done
	s_add_i32 s2, s2, 36
	s_mul_i32 s2, s2, s74
	v_readlane_b32 s9, v239, 23
	s_lshr_b32 s9, s9, 3
	s_add_i32 s2, s2, s9
	s_cmp_gt_u32 s2, 24575
	s_cbranch_scc1 .Lhw_seam3_done
	v_mbcnt_lo_u32_b32 v178, -1, 0
	v_mbcnt_hi_u32_b32 v178, -1, v178
	v_and_b32_e32 v179, 60, v178
	v_lshlrev_b32_e32 v179, 10, v179
	v_and_b32_e32 v180, 3, v178
	v_lshl_or_b32 v179, v180, 4, v179
	v_add_u32_e32 v180, 0x400, v179
	v_add_u32_e32 v181, 0x800, v179
	v_add_u32_e32 v190, 0xc00, v179
	v_lshlrev_b32_e32 v178, 2, v178
	s_cmp_lt_u32 s2, 16384
	s_cbranch_scc0 .Lhw_dn_s3_1
	s_lshr_b32 s9, s2, 9
	s_bfe_u32 s32, s2, 0x40005
	s_and_b32 s53, s2, 31
	s_lshl_b32 s69, s9, 23
	s_lshl_b32 s100, s32, 19
	s_add_i32 s69, s69, s100
	s_lshl_b32 s100, s53, 8
	s_add_i32 s69, s69, s100
	s_lshl_b32 s98, s9, 11
	s_bfe_u32 s100, s53, 0x30001
	s_lshl_b32 s100, s100, 8
	s_add_i32 s98, s98, s100
	s_lshr_b32 s100, s53, 4
	s_lshl_b32 s100, s100, 7
	s_add_i32 s98, s98, s100
	s_and_b32 s100, s53, 1
	s_lshl_b32 s100, s100, 6
	s_add_i32 s98, s98, s100
	s_lshl_b32 s98, s98, 10
	s_lshl_b32 s100, s32, 6
	s_add_i32 s98, s98, s100
	s_add_i32 s98, s98, 0x2000000
	v_readlane_b32 s82, v239, 11
	v_readlane_b32 s83, v239, 12
	s_movk_i32 s89, 8192
	s_branch .Lhw_go_s3_1

.Lhw_seam4:
	s_mov_b64 exec, -1
	v_readlane_b32 s2, v239, 0
	s_lshr_b32 s2, s2, 6
	s_add_i32 s2, s2, -1
	s_cmp_gt_u32 s2, 11
	s_cbranch_scc1 .Lhw_seam4_done
	s_add_i32 s2, s2, 48
	s_mul_i32 s2, s2, s74
	v_readlane_b32 s9, v239, 23
	s_lshr_b32 s9, s9, 3
	s_add_i32 s2, s2, s9
	s_cmp_gt_u32 s2, 24575
	s_cbranch_scc1 .Lhw_seam4_done
	v_mbcnt_lo_u32_b32 v178, -1, 0
	v_mbcnt_hi_u32_b32 v178, -1, v178
	v_and_b32_e32 v179, 60, v178
	v_lshlrev_b32_e32 v179, 10, v179
	v_and_b32_e32 v180, 3, v178
	v_lshl_or_b32 v179, v180, 4, v179
	v_add_u32_e32 v180, 0x400, v179
	v_add_u32_e32 v181, 0x800, v179
	v_add_u32_e32 v190, 0xc00, v179
	v_lshlrev_b32_e32 v178, 2, v178
	s_cmp_lt_u32 s2, 16384
	s_cbranch_scc0 .Lhw_dn_s4_0
	s_lshr_b32 s9, s2, 9
	s_bfe_u32 s32, s2, 0x40005
	s_and_b32 s53, s2, 31
	s_lshl_b32 s69, s9, 23
	s_lshl_b32 s100, s32, 19
	s_add_i32 s69, s69, s100
	s_lshl_b32 s100, s53, 8
	s_add_i32 s69, s69, s100
	s_lshl_b32 s98, s9, 11
	s_bfe_u32 s100, s53, 0x30001
	s_lshl_b32 s100, s100, 8
	s_add_i32 s98, s98, s100
	s_lshr_b32 s100, s53, 4
	s_lshl_b32 s100, s100, 7
	s_add_i32 s98, s98, s100
	s_and_b32 s100, s53, 1
	s_lshl_b32 s100, s100, 6
	s_add_i32 s98, s98, s100
	s_lshl_b32 s98, s98, 10
	s_lshl_b32 s100, s32, 6
	s_add_i32 s98, s98, s100
	s_add_i32 s98, s98, 0x2000000
	v_readlane_b32 s82, v239, 11
	v_readlane_b32 s83, v239, 12
	s_movk_i32 s89, 8192
	s_branch .Lhw_go_s4_0

.Lhw_go_s4_0:
	s_add_u32 s100, s82, s69
	s_addc_u32 s101, s83, 0
	v_readlane_b32 s82, v239, 44
	v_readlane_b32 s83, v239, 45
	s_add_u32 s82, s82, s98
	s_addc_u32 s83, s83, 0
	global_load_dword v34, v178, s[100:101] nt
	s_add_u32 s100, s100, s89
	s_addc_u32 s101, s101, 0
	global_load_dword v35, v178, s[100:101] nt
	s_add_u32 s100, s100, s89
	s_addc_u32 s101, s101, 0
	global_load_dword v36, v178, s[100:101] nt
	s_add_u32 s100, s100, s89
	s_addc_u32 s101, s101, 0
	global_load_dword v37, v178, s[100:101] nt
	s_add_u32 s100, s100, s89
	s_addc_u32 s101, s101, 0
	global_load_dword v38, v178, s[100:101] nt
	s_add_u32 s100, s100, s89
	s_addc_u32 s101, s101, 0
	global_load_dword v39, v178, s[100:101] nt
	s_add_u32 s100, s100, s89
	s_addc_u32 s101, s101, 0
	global_load_dword v40, v178, s[100:101] nt
	s_add_u32 s100, s100, s89
	s_addc_u32 s101, s101, 0
	global_load_dword v41, v178, s[100:101] nt
	s_add_u32 s100, s100, s89
	s_addc_u32 s101, s101, 0
	global_load_dword v42, v178, s[100:101] nt
	s_add_u32 s100, s100, s89
	s_addc_u32 s101, s101, 0
	global_load_dword v43, v178, s[100:101] nt
	s_add_u32 s100, s100, s89
	s_addc_u32 s101, s101, 0
	global_load_dword v44, v178, s[100:101] nt
	s_add_u32 s100, s100, s89
	s_addc_u32 s101, s101, 0
	global_load_dword v45, v178, s[100:101] nt
	s_add_u32 s100, s100, s89
	s_addc_u32 s101, s101, 0
	global_load_dword v46, v178, s[100:101] nt
	s_add_u32 s100, s100, s89
	s_addc_u32 s101, s101, 0
	global_load_dword v47, v178, s[100:101] nt
	s_add_u32 s100, s100, s89
	s_addc_u32 s101, s101, 0
	global_load_dword v48, v178, s[100:101] nt
	s_add_u32 s100, s100, s89
	s_addc_u32 s101, s101, 0
	global_load_dword v49, v178, s[100:101] nt
	s_add_u32 s100, s100, s89
	s_addc_u32 s101, s101, 0
	global_load_dword v50, v178, s[100:101] nt
	s_add_u32 s100, s100, s89
	s_addc_u32 s101, s101, 0
	global_load_dword v51, v178, s[100:101] nt
	s_add_u32 s100, s100, s89
	s_addc_u32 s101, s101, 0
	global_load_dword v52, v178, s[100:101] nt
	s_add_u32 s100, s100, s89
	s_addc_u32 s101, s101, 0
	global_load_dword v53, v178, s[100:101] nt
	s_add_u32 s100, s100, s89
	s_addc_u32 s101, s101, 0
	global_load_dword v54, v178, s[100:101] nt
	s_add_u32 s100, s100, s89
	s_addc_u32 s101, s101, 0
	global_load_dword v55, v178, s[100:101] nt
	s_add_u32 s100, s100, s89
	s_addc_u32 s101, s101, 0
	global_load_dword v56, v178, s[100:101] nt
	s_add_u32 s100, s100, s89
	s_addc_u32 s101, s101, 0
	global_load_dword v57, v178, s[100:101] nt
	s_add_u32 s100, s100, s89
	s_addc_u32 s101, s101, 0
	global_load_dword v58, v178, s[100:101] nt
	s_add_u32 s100, s100, s89
	s_addc_u32 s101, s101, 0
	global_load_dword v59, v178, s[100:101] nt
	s_add_u32 s100, s100, s89
	s_addc_u32 s101, s101, 0
	global_load_dword v60, v178, s[100:101] nt
	s_add_u32 s100, s100, s89
	s_addc_u32 s101, s101, 0
	global_load_dword v61, v178, s[100:101] nt
	s_add_u32 s100, s100, s89
	s_addc_u32 s101, s101, 0
	global_load_dword v62, v178, s[100:101] nt
	s_add_u32 s100, s100, s89
	s_addc_u32 s101, s101, 0
	global_load_dword v63, v178, s[100:101] nt
	s_add_u32 s100, s100, s89
	s_addc_u32 s101, s101, 0
	global_load_dword v64, v178, s[100:101] nt
	s_add_u32 s100, s100, s89
	s_addc_u32 s101, s101, 0
	global_load_dword v65, v178, s[100:101] nt
	s_add_u32 s100, s100, s89
	s_addc_u32 s101, s101, 0
	global_load_dword v66, v178, s[100:101] nt
	s_add_u32 s100, s100, s89
	s_addc_u32 s101, s101, 0
	global_load_dword v67, v178, s[100:101] nt
	s_add_u32 s100, s100, s89
	s_addc_u32 s101, s101, 0
	global_load_dword v68, v178, s[100:101] nt
	s_add_u32 s100, s100, s89
	s_addc_u32 s101, s101, 0
	global_load_dword v69, v178, s[100:101] nt
	s_add_u32 s100, s100, s89
	s_addc_u32 s101, s101, 0
	global_load_dword v70, v178, s[100:101] nt
	s_add_u32 s100, s100, s89
	s_addc_u32 s101, s101, 0
	global_load_dword v71, v178, s[100:101] nt
	s_add_u32 s100, s100, s89
	s_addc_u32 s101, s101, 0
	global_load_dword v72, v178, s[100:101] nt
	s_add_u32 s100, s100, s89
	s_addc_u32 s101, s101, 0
	global_load_dword v73, v178, s[100:101] nt
	s_add_u32 s100, s100, s89
	s_addc_u32 s101, s101, 0
	global_load_dword v74, v178, s[100:101] nt
	s_add_u32 s100, s100, s89
	s_addc_u32 s101, s101, 0
	global_load_dword v75, v178, s[100:101] nt
	s_add_u32 s100, s100, s89
	s_addc_u32 s101, s101, 0
	global_load_dword v76, v178, s[100:101] nt
	s_add_u32 s100, s100, s89
	s_addc_u32 s101, s101, 0
	global_load_dword v77, v178, s[100:101] nt
	s_add_u32 s100, s100, s89
	s_addc_u32 s101, s101, 0
	global_load_dword v78, v178, s[100:101] nt
	s_add_u32 s100, s100, s89
	s_addc_u32 s101, s101, 0
	global_load_dword v79, v178, s[100:101] nt
	s_add_u32 s100, s100, s89
	s_addc_u32 s101, s101, 0
	global_load_dword v80, v178, s[100:101] nt
	s_add_u32 s100, s100, s89
	s_addc_u32 s101, s101, 0
	global_load_dword v81, v178, s[100:101] nt
	s_add_u32 s100, s100, s89
	s_addc_u32 s101, s101, 0
	global_load_dword v82, v178, s[100:101] nt
	s_add_u32 s100, s100, s89
	s_addc_u32 s101, s101, 0
	global_load_dword v83, v178, s[100:101] nt
	s_add_u32 s100, s100, s89
	s_addc_u32 s101, s101, 0
	global_load_dword v84, v178, s[100:101] nt
	s_add_u32 s100, s100, s89
	s_addc_u32 s101, s101, 0
	global_load_dword v85, v178, s[100:101] nt
	s_add_u32 s100, s100, s89
	s_addc_u32 s101, s101, 0
	global_load_dword v86, v178, s[100:101] nt
	s_add_u32 s100, s100, s89
	s_addc_u32 s101, s101, 0
	global_load_dword v87, v178, s[100:101] nt
	s_add_u32 s100, s100, s89
	s_addc_u32 s101, s101, 0
	global_load_dword v88, v178, s[100:101] nt
	s_add_u32 s100, s100, s89
	s_addc_u32 s101, s101, 0
	global_load_dword v89, v178, s[100:101] nt
	s_add_u32 s100, s100, s89
	s_addc_u32 s101, s101, 0
	global_load_dword v90, v178, s[100:101] nt
	s_add_u32 s100, s100, s89
	s_addc_u32 s101, s101, 0
	global_load_dword v91, v178, s[100:101] nt
	s_add_u32 s100, s100, s89
	s_addc_u32 s101, s101, 0
	global_load_dword v92, v178, s[100:101] nt
	s_add_u32 s100, s100, s89
	s_addc_u32 s101, s101, 0
	global_load_dword v93, v178, s[100:101] nt
	s_add_u32 s100, s100, s89
	s_addc_u32 s101, s101, 0
	global_load_dword v94, v178, s[100:101] nt
	s_add_u32 s100, s100, s89
	s_addc_u32 s101, s101, 0
	global_load_dword v95, v178, s[100:101] nt
	s_add_u32 s100, s100, s89
	s_addc_u32 s101, s101, 0
	global_load_dword v96, v178, s[100:101] nt
	s_add_u32 s100, s100, s89
	s_addc_u32 s101, s101, 0
	global_load_dword v97, v178, s[100:101] nt
	s_add_u32 s100, s100, s89
	s_addc_u32 s101, s101, 0
	s_waitcnt vmcnt(48)
	v_mul_f32_e32 v34, 0x42000000, v34
	v_mul_f32_e32 v35, 0x42000000, v35
	v_mul_f32_e32 v36, 0x42000000, v36
	v_mul_f32_e32 v37, 0x42000000, v37
	v_mul_f32_e32 v38, 0x42000000, v38
	v_mul_f32_e32 v39, 0x42000000, v39
	v_mul_f32_e32 v40, 0x42000000, v40
	v_mul_f32_e32 v41, 0x42000000, v41
	v_mul_f32_e32 v42, 0x42000000, v42
	v_mul_f32_e32 v43, 0x42000000, v43
	v_mul_f32_e32 v44, 0x42000000, v44
	v_mul_f32_e32 v45, 0x42000000, v45
	v_mul_f32_e32 v46, 0x42000000, v46
	v_mul_f32_e32 v47, 0x42000000, v47
	v_mul_f32_e32 v48, 0x42000000, v48
	v_mul_f32_e32 v49, 0x42000000, v49
	v_cvt_pk_fp8_f32 v154, v34, v35
	v_cvt_pk_fp8_f32 v155, v38, v39
	v_cvt_pk_fp8_f32 v156, v42, v43
	v_cvt_pk_fp8_f32 v157, v46, v47
	v_cvt_pk_fp8_f32 v154, v36, v37 op_sel:[0,0,1]
	v_cvt_pk_fp8_f32 v155, v40, v41 op_sel:[0,0,1]
	v_cvt_pk_fp8_f32 v156, v44, v45 op_sel:[0,0,1]
	v_cvt_pk_fp8_f32 v157, v48, v49 op_sel:[0,0,1]
	s_waitcnt vmcnt(32)
	v_mul_f32_e32 v50, 0x42000000, v50
	v_mul_f32_e32 v51, 0x42000000, v51
	v_mul_f32_e32 v52, 0x42000000, v52
	v_mul_f32_e32 v53, 0x42000000, v53
	v_mul_f32_e32 v54, 0x42000000, v54
	v_mul_f32_e32 v55, 0x42000000, v55
	v_mul_f32_e32 v56, 0x42000000, v56
	v_mul_f32_e32 v57, 0x42000000, v57
	v_mul_f32_e32 v58, 0x42000000, v58
	v_mul_f32_e32 v59, 0x42000000, v59
	v_mul_f32_e32 v60, 0x42000000, v60
	v_mul_f32_e32 v61, 0x42000000, v61
	v_mul_f32_e32 v62, 0x42000000, v62
	v_mul_f32_e32 v63, 0x42000000, v63
	v_mul_f32_e32 v64, 0x42000000, v64
	v_mul_f32_e32 v65, 0x42000000, v65
	v_cvt_pk_fp8_f32 v158, v50, v51
	v_cvt_pk_fp8_f32 v159, v54, v55
	v_cvt_pk_fp8_f32 v160, v58, v59
	v_cvt_pk_fp8_f32 v161, v62, v63
	v_cvt_pk_fp8_f32 v158, v52, v53 op_sel:[0,0,1]
	v_cvt_pk_fp8_f32 v159, v56, v57 op_sel:[0,0,1]
	v_cvt_pk_fp8_f32 v160, v60, v61 op_sel:[0,0,1]
	v_cvt_pk_fp8_f32 v161, v64, v65 op_sel:[0,0,1]
	s_waitcnt vmcnt(16)
	v_mul_f32_e32 v66, 0x42000000, v66
	v_mul_f32_e32 v67, 0x42000000, v67
	v_mul_f32_e32 v68, 0x42000000, v68
	v_mul_f32_e32 v69, 0x42000000, v69
	v_mul_f32_e32 v70, 0x42000000, v70
	v_mul_f32_e32 v71, 0x42000000, v71
	v_mul_f32_e32 v72, 0x42000000, v72
	v_mul_f32_e32 v73, 0x42000000, v73
	v_mul_f32_e32 v74, 0x42000000, v74
	v_mul_f32_e32 v75, 0x42000000, v75
	v_mul_f32_e32 v76, 0x42000000, v76
	v_mul_f32_e32 v77, 0x42000000, v77
	v_mul_f32_e32 v78, 0x42000000, v78
	v_mul_f32_e32 v79, 0x42000000, v79
	v_mul_f32_e32 v80, 0x42000000, v80
	v_mul_f32_e32 v81, 0x42000000, v81
	v_cvt_pk_fp8_f32 v162, v66, v67
	v_cvt_pk_fp8_f32 v163, v70, v71
	v_cvt_pk_fp8_f32 v164, v74, v75
	v_cvt_pk_fp8_f32 v165, v78, v79
	v_cvt_pk_fp8_f32 v162, v68, v69 op_sel:[0,0,1]
	v_cvt_pk_fp8_f32 v163, v72, v73 op_sel:[0,0,1]
	v_cvt_pk_fp8_f32 v164, v76, v77 op_sel:[0,0,1]
	v_cvt_pk_fp8_f32 v165, v80, v81 op_sel:[0,0,1]
	s_waitcnt vmcnt(0)
	v_mul_f32_e32 v82, 0x42000000, v82
	v_mul_f32_e32 v83, 0x42000000, v83
	v_mul_f32_e32 v84, 0x42000000, v84
	v_mul_f32_e32 v85, 0x42000000, v85
	v_mul_f32_e32 v86, 0x42000000, v86
	v_mul_f32_e32 v87, 0x42000000, v87
	v_mul_f32_e32 v88, 0x42000000, v88
	v_mul_f32_e32 v89, 0x42000000, v89
	v_mul_f32_e32 v90, 0x42000000, v90
	v_mul_f32_e32 v91, 0x42000000, v91
	v_mul_f32_e32 v92, 0x42000000, v92
	v_mul_f32_e32 v93, 0x42000000, v93
	v_mul_f32_e32 v94, 0x42000000, v94
	v_mul_f32_e32 v95, 0x42000000, v95
	v_mul_f32_e32 v96, 0x42000000, v96
	v_mul_f32_e32 v97, 0x42000000, v97
	v_cvt_pk_fp8_f32 v166, v82, v83
	v_cvt_pk_fp8_f32 v167, v86, v87
	v_cvt_pk_fp8_f32 v168, v90, v91
	v_cvt_pk_fp8_f32 v169, v94, v95
	v_cvt_pk_fp8_f32 v166, v84, v85 op_sel:[0,0,1]
	v_cvt_pk_fp8_f32 v167, v88, v89 op_sel:[0,0,1]
	v_cvt_pk_fp8_f32 v168, v92, v93 op_sel:[0,0,1]
	v_cvt_pk_fp8_f32 v169, v96, v97 op_sel:[0,0,1]
	s_mov_b32 vcc_lo, 0xaaaaaaaa
	s_mov_b32 vcc_hi, 0xaaaaaaaa
	s_nop 1
	v_cndmask_b32_dpp v170, v154, v158, vcc quad_perm:[1,0,3,2] row_mask:0xf bank_mask:0xf
	v_cndmask_b32_dpp v174, v162, v166, vcc quad_perm:[1,0,3,2] row_mask:0xf bank_mask:0xf
	v_cndmask_b32_dpp v171, v155, v159, vcc quad_perm:[1,0,3,2] row_mask:0xf bank_mask:0xf
	v_cndmask_b32_dpp v175, v163, v167, vcc quad_perm:[1,0,3,2] row_mask:0xf bank_mask:0xf
	v_cndmask_b32_dpp v172, v156, v160, vcc quad_perm:[1,0,3,2] row_mask:0xf bank_mask:0xf
	v_cndmask_b32_dpp v176, v164, v168, vcc quad_perm:[1,0,3,2] row_mask:0xf bank_mask:0xf
	v_cndmask_b32_dpp v173, v157, v161, vcc quad_perm:[1,0,3,2] row_mask:0xf bank_mask:0xf
	v_cndmask_b32_dpp v177, v165, v169, vcc quad_perm:[1,0,3,2] row_mask:0xf bank_mask:0xf
	s_mov_b32 vcc_lo, 0x55555555
	s_mov_b32 vcc_hi, 0x55555555
	s_nop 1
	v_cndmask_b32_dpp v154, v158, v154, vcc quad_perm:[1,0,3,2] row_mask:0xf bank_mask:0xf
	v_cndmask_b32_dpp v162, v166, v162, vcc quad_perm:[1,0,3,2] row_mask:0xf bank_mask:0xf
	v_cndmask_b32_dpp v155, v159, v155, vcc quad_perm:[1,0,3,2] row_mask:0xf bank_mask:0xf
	v_cndmask_b32_dpp v163, v167, v163, vcc quad_perm:[1,0,3,2] row_mask:0xf bank_mask:0xf
	v_cndmask_b32_dpp v156, v160, v156, vcc quad_perm:[1,0,3,2] row_mask:0xf bank_mask:0xf
	v_cndmask_b32_dpp v164, v168, v164, vcc quad_perm:[1,0,3,2] row_mask:0xf bank_mask:0xf
	v_cndmask_b32_dpp v157, v161, v157, vcc quad_perm:[1,0,3,2] row_mask:0xf bank_mask:0xf
	v_cndmask_b32_dpp v165, v169, v165, vcc quad_perm:[1,0,3,2] row_mask:0xf bank_mask:0xf
	s_mov_b32 vcc_lo, 0xcccccccc
	s_mov_b32 vcc_hi, 0xcccccccc
	s_nop 1
	v_cndmask_b32_dpp v158, v154, v162, vcc quad_perm:[2,3,0,1] row_mask:0xf bank_mask:0xf
	v_cndmask_b32_dpp v166, v170, v174, vcc quad_perm:[2,3,0,1] row_mask:0xf bank_mask:0xf
	v_cndmask_b32_dpp v159, v155, v163, vcc quad_perm:[2,3,0,1] row_mask:0xf bank_mask:0xf
	v_cndmask_b32_dpp v167, v171, v175, vcc quad_perm:[2,3,0,1] row_mask:0xf bank_mask:0xf
	v_cndmask_b32_dpp v160, v156, v164, vcc quad_perm:[2,3,0,1] row_mask:0xf bank_mask:0xf
	v_cndmask_b32_dpp v168, v172, v176, vcc quad_perm:[2,3,0,1] row_mask:0xf bank_mask:0xf
	v_cndmask_b32_dpp v161, v157, v165, vcc quad_perm:[2,3,0,1] row_mask:0xf bank_mask:0xf
	v_cndmask_b32_dpp v169, v173, v177, vcc quad_perm:[2,3,0,1] row_mask:0xf bank_mask:0xf
	s_mov_b32 vcc_lo, 0x33333333
	s_mov_b32 vcc_hi, 0x33333333
	s_nop 1
	v_cndmask_b32_dpp v154, v162, v154, vcc quad_perm:[2,3,0,1] row_mask:0xf bank_mask:0xf
	v_cndmask_b32_dpp v170, v174, v170, vcc quad_perm:[2,3,0,1] row_mask:0xf bank_mask:0xf
	v_cndmask_b32_dpp v155, v163, v155, vcc quad_perm:[2,3,0,1] row_mask:0xf bank_mask:0xf
	v_cndmask_b32_dpp v171, v175, v171, vcc quad_perm:[2,3,0,1] row_mask:0xf bank_mask:0xf
	v_cndmask_b32_dpp v156, v164, v156, vcc quad_perm:[2,3,0,1] row_mask:0xf bank_mask:0xf
	v_cndmask_b32_dpp v172, v176, v172, vcc quad_perm:[2,3,0,1] row_mask:0xf bank_mask:0xf
	v_cndmask_b32_dpp v157, v165, v157, vcc quad_perm:[2,3,0,1] row_mask:0xf bank_mask:0xf
	v_cndmask_b32_dpp v173, v177, v173, vcc quad_perm:[2,3,0,1] row_mask:0xf bank_mask:0xf
	global_store_dwordx4 v179, v[154:157], s[82:83] nt
	global_store_dwordx4 v180, v[170:173], s[82:83] nt
	global_store_dwordx4 v181, v[158:161], s[82:83] nt
	global_store_dwordx4 v190, v[166:169], s[82:83] nt
	v_readlane_b32 s2, v239, 0
	s_lshr_b32 s2, s2, 6
	s_add_i32 s2, s2, 6
	s_cmp_gt_u32 s2, 11
	s_cbranch_scc1 .Lhw_seam4_done
	s_add_i32 s2, s2, 48
	s_mul_i32 s2, s2, s74
	v_readlane_b32 s9, v239, 23
	s_lshr_b32 s9, s9, 3
	s_add_i32 s2, s2, s9
	s_cmp_gt_u32 s2, 24575
	s_cbranch_scc1 .Lhw_seam4_done
	v_mbcnt_lo_u32_b32 v178, -1, 0
	v_mbcnt_hi_u32_b32 v178, -1, v178
	v_and_b32_e32 v179, 60, v178
	v_lshlrev_b32_e32 v179, 10, v179
	v_and_b32_e32 v180, 3, v178
	v_lshl_or_b32 v179, v180, 4, v179
	v_add_u32_e32 v180, 0x400, v179
	v_add_u32_e32 v181, 0x800, v179
	v_add_u32_e32 v190, 0xc00, v179
	v_lshlrev_b32_e32 v178, 2, v178
	s_cmp_lt_u32 s2, 16384
	s_cbranch_scc0 .Lhw_dn_s4_1
	s_lshr_b32 s9, s2, 9
	s_bfe_u32 s32, s2, 0x40005
	s_and_b32 s53, s2, 31
	s_lshl_b32 s69, s9, 23
	s_lshl_b32 s100, s32, 19
	s_add_i32 s69, s69, s100
	s_lshl_b32 s100, s53, 8
	s_add_i32 s69, s69, s100
	s_lshl_b32 s98, s9, 11
	s_bfe_u32 s100, s53, 0x30001
	s_lshl_b32 s100, s100, 8
	s_add_i32 s98, s98, s100
	s_lshr_b32 s100, s53, 4
	s_lshl_b32 s100, s100, 7
	s_add_i32 s98, s98, s100
	s_and_b32 s100, s53, 1
	s_lshl_b32 s100, s100, 6
	s_add_i32 s98, s98, s100
	s_lshl_b32 s98, s98, 10
	s_lshl_b32 s100, s32, 6
	s_add_i32 s98, s98, s100
	s_add_i32 s98, s98, 0x2000000
	v_readlane_b32 s82, v239, 11
	v_readlane_b32 s83, v239, 12
	s_movk_i32 s89, 8192
	s_branch .Lhw_go_s4_1

.Lhw_seam5:
	s_mov_b64 exec, -1
	v_readlane_b32 s2, v239, 0
	s_lshr_b32 s2, s2, 6
	s_add_i32 s2, s2, -1
	s_cmp_gt_u32 s2, 11
	s_cbranch_scc1 .Lhw_seam5_done
	s_add_i32 s2, s2, 60
	s_mul_i32 s2, s2, s74
	v_readlane_b32 s9, v239, 23
	s_lshr_b32 s9, s9, 3
	s_add_i32 s2, s2, s9
	s_cmp_gt_u32 s2, 24575
	s_cbranch_scc1 .Lhw_seam5_done
	v_mbcnt_lo_u32_b32 v178, -1, 0
	v_mbcnt_hi_u32_b32 v178, -1, v178
	v_and_b32_e32 v179, 60, v178
	v_lshlrev_b32_e32 v179, 10, v179
	v_and_b32_e32 v180, 3, v178
	v_lshl_or_b32 v179, v180, 4, v179
	v_add_u32_e32 v180, 0x400, v179
	v_add_u32_e32 v181, 0x800, v179
	v_add_u32_e32 v190, 0xc00, v179
	v_lshlrev_b32_e32 v178, 2, v178
	s_cmp_lt_u32 s2, 16384
	s_cbranch_scc0 .Lhw_dn_s5_0
	s_lshr_b32 s9, s2, 9
	s_bfe_u32 s32, s2, 0x40005
	s_and_b32 s53, s2, 31
	s_lshl_b32 s69, s9, 23
	s_lshl_b32 s100, s32, 19
	s_add_i32 s69, s69, s100
	s_lshl_b32 s100, s53, 8
	s_add_i32 s69, s69, s100
	s_lshl_b32 s98, s9, 11
	s_bfe_u32 s100, s53, 0x30001
	s_lshl_b32 s100, s100, 8
	s_add_i32 s98, s98, s100
	s_lshr_b32 s100, s53, 4
	s_lshl_b32 s100, s100, 7
	s_add_i32 s98, s98, s100
	s_and_b32 s100, s53, 1
	s_lshl_b32 s100, s100, 6
	s_add_i32 s98, s98, s100
	s_lshl_b32 s98, s98, 10
	s_lshl_b32 s100, s32, 6
	s_add_i32 s98, s98, s100
	s_add_i32 s98, s98, 0x2000000
	v_readlane_b32 s82, v239, 11
	v_readlane_b32 s83, v239, 12
	s_movk_i32 s89, 8192
	s_branch .Lhw_go_s5_0

.Lhw_go_s5_0:
	s_add_u32 s100, s82, s69
	s_addc_u32 s101, s83, 0
	v_readlane_b32 s82, v239, 44
	v_readlane_b32 s83, v239, 45
	s_add_u32 s82, s82, s98
	s_addc_u32 s83, s83, 0
	global_load_dword v34, v178, s[100:101] nt
	s_add_u32 s100, s100, s89
	s_addc_u32 s101, s101, 0
	global_load_dword v35, v178, s[100:101] nt
	s_add_u32 s100, s100, s89
	s_addc_u32 s101, s101, 0
	global_load_dword v36, v178, s[100:101] nt
	s_add_u32 s100, s100, s89
	s_addc_u32 s101, s101, 0
	global_load_dword v37, v178, s[100:101] nt
	s_add_u32 s100, s100, s89
	s_addc_u32 s101, s101, 0
	global_load_dword v38, v178, s[100:101] nt
	s_add_u32 s100, s100, s89
	s_addc_u32 s101, s101, 0
	global_load_dword v39, v178, s[100:101] nt
	s_add_u32 s100, s100, s89
	s_addc_u32 s101, s101, 0
	global_load_dword v40, v178, s[100:101] nt
	s_add_u32 s100, s100, s89
	s_addc_u32 s101, s101, 0
	global_load_dword v41, v178, s[100:101] nt
	s_add_u32 s100, s100, s89
	s_addc_u32 s101, s101, 0
	global_load_dword v42, v178, s[100:101] nt
	s_add_u32 s100, s100, s89
	s_addc_u32 s101, s101, 0
	global_load_dword v43, v178, s[100:101] nt
	s_add_u32 s100, s100, s89
	s_addc_u32 s101, s101, 0
	global_load_dword v44, v178, s[100:101] nt
	s_add_u32 s100, s100, s89
	s_addc_u32 s101, s101, 0
	global_load_dword v45, v178, s[100:101] nt
	s_add_u32 s100, s100, s89
	s_addc_u32 s101, s101, 0
	global_load_dword v46, v178, s[100:101] nt
	s_add_u32 s100, s100, s89
	s_addc_u32 s101, s101, 0
	global_load_dword v47, v178, s[100:101] nt
	s_add_u32 s100, s100, s89
	s_addc_u32 s101, s101, 0
	global_load_dword v48, v178, s[100:101] nt
	s_add_u32 s100, s100, s89
	s_addc_u32 s101, s101, 0
	global_load_dword v49, v178, s[100:101] nt
	s_add_u32 s100, s100, s89
	s_addc_u32 s101, s101, 0
	global_load_dword v50, v178, s[100:101] nt
	s_add_u32 s100, s100, s89
	s_addc_u32 s101, s101, 0
	global_load_dword v51, v178, s[100:101] nt
	s_add_u32 s100, s100, s89
	s_addc_u32 s101, s101, 0
	global_load_dword v52, v178, s[100:101] nt
	s_add_u32 s100, s100, s89
	s_addc_u32 s101, s101, 0
	global_load_dword v53, v178, s[100:101] nt
	s_add_u32 s100, s100, s89
	s_addc_u32 s101, s101, 0
	global_load_dword v54, v178, s[100:101] nt
	s_add_u32 s100, s100, s89
	s_addc_u32 s101, s101, 0
	global_load_dword v55, v178, s[100:101] nt
	s_add_u32 s100, s100, s89
	s_addc_u32 s101, s101, 0
	global_load_dword v56, v178, s[100:101] nt
	s_add_u32 s100, s100, s89
	s_addc_u32 s101, s101, 0
	global_load_dword v57, v178, s[100:101] nt
	s_add_u32 s100, s100, s89
	s_addc_u32 s101, s101, 0
	global_load_dword v58, v178, s[100:101] nt
	s_add_u32 s100, s100, s89
	s_addc_u32 s101, s101, 0
	global_load_dword v59, v178, s[100:101] nt
	s_add_u32 s100, s100, s89
	s_addc_u32 s101, s101, 0
	global_load_dword v60, v178, s[100:101] nt
	s_add_u32 s100, s100, s89
	s_addc_u32 s101, s101, 0
	global_load_dword v61, v178, s[100:101] nt
	s_add_u32 s100, s100, s89
	s_addc_u32 s101, s101, 0
	global_load_dword v62, v178, s[100:101] nt
	s_add_u32 s100, s100, s89
	s_addc_u32 s101, s101, 0
	global_load_dword v63, v178, s[100:101] nt
	s_add_u32 s100, s100, s89
	s_addc_u32 s101, s101, 0
	global_load_dword v64, v178, s[100:101] nt
	s_add_u32 s100, s100, s89
	s_addc_u32 s101, s101, 0
	global_load_dword v65, v178, s[100:101] nt
	s_add_u32 s100, s100, s89
	s_addc_u32 s101, s101, 0
	global_load_dword v66, v178, s[100:101] nt
	s_add_u32 s100, s100, s89
	s_addc_u32 s101, s101, 0
	global_load_dword v67, v178, s[100:101] nt
	s_add_u32 s100, s100, s89
	s_addc_u32 s101, s101, 0
	global_load_dword v68, v178, s[100:101] nt
	s_add_u32 s100, s100, s89
	s_addc_u32 s101, s101, 0
	global_load_dword v69, v178, s[100:101] nt
	s_add_u32 s100, s100, s89
	s_addc_u32 s101, s101, 0
	global_load_dword v70, v178, s[100:101] nt
	s_add_u32 s100, s100, s89
	s_addc_u32 s101, s101, 0
	global_load_dword v71, v178, s[100:101] nt
	s_add_u32 s100, s100, s89
	s_addc_u32 s101, s101, 0
	global_load_dword v72, v178, s[100:101] nt
	s_add_u32 s100, s100, s89
	s_addc_u32 s101, s101, 0
	global_load_dword v73, v178, s[100:101] nt
	s_add_u32 s100, s100, s89
	s_addc_u32 s101, s101, 0
	global_load_dword v74, v178, s[100:101] nt
	s_add_u32 s100, s100, s89
	s_addc_u32 s101, s101, 0
	global_load_dword v75, v178, s[100:101] nt
	s_add_u32 s100, s100, s89
	s_addc_u32 s101, s101, 0
	global_load_dword v76, v178, s[100:101] nt
	s_add_u32 s100, s100, s89
	s_addc_u32 s101, s101, 0
	global_load_dword v77, v178, s[100:101] nt
	s_add_u32 s100, s100, s89
	s_addc_u32 s101, s101, 0
	global_load_dword v78, v178, s[100:101] nt
	s_add_u32 s100, s100, s89
	s_addc_u32 s101, s101, 0
	global_load_dword v79, v178, s[100:101] nt
	s_add_u32 s100, s100, s89
	s_addc_u32 s101, s101, 0
	global_load_dword v80, v178, s[100:101] nt
	s_add_u32 s100, s100, s89
	s_addc_u32 s101, s101, 0
	global_load_dword v81, v178, s[100:101] nt
	s_add_u32 s100, s100, s89
	s_addc_u32 s101, s101, 0
	global_load_dword v82, v178, s[100:101] nt
	s_add_u32 s100, s100, s89
	s_addc_u32 s101, s101, 0
	global_load_dword v83, v178, s[100:101] nt
	s_add_u32 s100, s100, s89
	s_addc_u32 s101, s101, 0
	global_load_dword v84, v178, s[100:101] nt
	s_add_u32 s100, s100, s89
	s_addc_u32 s101, s101, 0
	global_load_dword v85, v178, s[100:101] nt
	s_add_u32 s100, s100, s89
	s_addc_u32 s101, s101, 0
	global_load_dword v86, v178, s[100:101] nt
	s_add_u32 s100, s100, s89
	s_addc_u32 s101, s101, 0
	global_load_dword v87, v178, s[100:101] nt
	s_add_u32 s100, s100, s89
	s_addc_u32 s101, s101, 0
	global_load_dword v88, v178, s[100:101] nt
	s_add_u32 s100, s100, s89
	s_addc_u32 s101, s101, 0
	global_load_dword v89, v178, s[100:101] nt
	s_add_u32 s100, s100, s89
	s_addc_u32 s101, s101, 0
	global_load_dword v90, v178, s[100:101] nt
	s_add_u32 s100, s100, s89
	s_addc_u32 s101, s101, 0
	global_load_dword v91, v178, s[100:101] nt
	s_add_u32 s100, s100, s89
	s_addc_u32 s101, s101, 0
	global_load_dword v92, v178, s[100:101] nt
	s_add_u32 s100, s100, s89
	s_addc_u32 s101, s101, 0
	global_load_dword v93, v178, s[100:101] nt
	s_add_u32 s100, s100, s89
	s_addc_u32 s101, s101, 0
	global_load_dword v94, v178, s[100:101] nt
	s_add_u32 s100, s100, s89
	s_addc_u32 s101, s101, 0
	global_load_dword v95, v178, s[100:101] nt
	s_add_u32 s100, s100, s89
	s_addc_u32 s101, s101, 0
	global_load_dword v96, v178, s[100:101] nt
	s_add_u32 s100, s100, s89
	s_addc_u32 s101, s101, 0
	global_load_dword v97, v178, s[100:101] nt
	s_add_u32 s100, s100, s89
	s_addc_u32 s101, s101, 0
	s_waitcnt vmcnt(48)
	v_mul_f32_e32 v34, 0x42000000, v34
	v_mul_f32_e32 v35, 0x42000000, v35
	v_mul_f32_e32 v36, 0x42000000, v36
	v_mul_f32_e32 v37, 0x42000000, v37
	v_mul_f32_e32 v38, 0x42000000, v38
	v_mul_f32_e32 v39, 0x42000000, v39
	v_mul_f32_e32 v40, 0x42000000, v40
	v_mul_f32_e32 v41, 0x42000000, v41
	v_mul_f32_e32 v42, 0x42000000, v42
	v_mul_f32_e32 v43, 0x42000000, v43
	v_mul_f32_e32 v44, 0x42000000, v44
	v_mul_f32_e32 v45, 0x42000000, v45
	v_mul_f32_e32 v46, 0x42000000, v46
	v_mul_f32_e32 v47, 0x42000000, v47
	v_mul_f32_e32 v48, 0x42000000, v48
	v_mul_f32_e32 v49, 0x42000000, v49
	v_cvt_pk_fp8_f32 v154, v34, v35
	v_cvt_pk_fp8_f32 v155, v38, v39
	v_cvt_pk_fp8_f32 v156, v42, v43
	v_cvt_pk_fp8_f32 v157, v46, v47
	v_cvt_pk_fp8_f32 v154, v36, v37 op_sel:[0,0,1]
	v_cvt_pk_fp8_f32 v155, v40, v41 op_sel:[0,0,1]
	v_cvt_pk_fp8_f32 v156, v44, v45 op_sel:[0,0,1]
	v_cvt_pk_fp8_f32 v157, v48, v49 op_sel:[0,0,1]
	s_waitcnt vmcnt(32)
	v_mul_f32_e32 v50, 0x42000000, v50
	v_mul_f32_e32 v51, 0x42000000, v51
	v_mul_f32_e32 v52, 0x42000000, v52
	v_mul_f32_e32 v53, 0x42000000, v53
	v_mul_f32_e32 v54, 0x42000000, v54
	v_mul_f32_e32 v55, 0x42000000, v55
	v_mul_f32_e32 v56, 0x42000000, v56
	v_mul_f32_e32 v57, 0x42000000, v57
	v_mul_f32_e32 v58, 0x42000000, v58
	v_mul_f32_e32 v59, 0x42000000, v59
	v_mul_f32_e32 v60, 0x42000000, v60
	v_mul_f32_e32 v61, 0x42000000, v61
	v_mul_f32_e32 v62, 0x42000000, v62
	v_mul_f32_e32 v63, 0x42000000, v63
	v_mul_f32_e32 v64, 0x42000000, v64
	v_mul_f32_e32 v65, 0x42000000, v65
	v_cvt_pk_fp8_f32 v158, v50, v51
	v_cvt_pk_fp8_f32 v159, v54, v55
	v_cvt_pk_fp8_f32 v160, v58, v59
	v_cvt_pk_fp8_f32 v161, v62, v63
	v_cvt_pk_fp8_f32 v158, v52, v53 op_sel:[0,0,1]
	v_cvt_pk_fp8_f32 v159, v56, v57 op_sel:[0,0,1]
	v_cvt_pk_fp8_f32 v160, v60, v61 op_sel:[0,0,1]
	v_cvt_pk_fp8_f32 v161, v64, v65 op_sel:[0,0,1]
	s_waitcnt vmcnt(16)
	v_mul_f32_e32 v66, 0x42000000, v66
	v_mul_f32_e32 v67, 0x42000000, v67
	v_mul_f32_e32 v68, 0x42000000, v68
	v_mul_f32_e32 v69, 0x42000000, v69
	v_mul_f32_e32 v70, 0x42000000, v70
	v_mul_f32_e32 v71, 0x42000000, v71
	v_mul_f32_e32 v72, 0x42000000, v72
	v_mul_f32_e32 v73, 0x42000000, v73
	v_mul_f32_e32 v74, 0x42000000, v74
	v_mul_f32_e32 v75, 0x42000000, v75
	v_mul_f32_e32 v76, 0x42000000, v76
	v_mul_f32_e32 v77, 0x42000000, v77
	v_mul_f32_e32 v78, 0x42000000, v78
	v_mul_f32_e32 v79, 0x42000000, v79
	v_mul_f32_e32 v80, 0x42000000, v80
	v_mul_f32_e32 v81, 0x42000000, v81
	v_cvt_pk_fp8_f32 v162, v66, v67
	v_cvt_pk_fp8_f32 v163, v70, v71
	v_cvt_pk_fp8_f32 v164, v74, v75
	v_cvt_pk_fp8_f32 v165, v78, v79
	v_cvt_pk_fp8_f32 v162, v68, v69 op_sel:[0,0,1]
	v_cvt_pk_fp8_f32 v163, v72, v73 op_sel:[0,0,1]
	v_cvt_pk_fp8_f32 v164, v76, v77 op_sel:[0,0,1]
	v_cvt_pk_fp8_f32 v165, v80, v81 op_sel:[0,0,1]
	s_waitcnt vmcnt(0)
	v_mul_f32_e32 v82, 0x42000000, v82
	v_mul_f32_e32 v83, 0x42000000, v83
	v_mul_f32_e32 v84, 0x42000000, v84
	v_mul_f32_e32 v85, 0x42000000, v85
	v_mul_f32_e32 v86, 0x42000000, v86
	v_mul_f32_e32 v87, 0x42000000, v87
	v_mul_f32_e32 v88, 0x42000000, v88
	v_mul_f32_e32 v89, 0x42000000, v89
	v_mul_f32_e32 v90, 0x42000000, v90
	v_mul_f32_e32 v91, 0x42000000, v91
	v_mul_f32_e32 v92, 0x42000000, v92
	v_mul_f32_e32 v93, 0x42000000, v93
	v_mul_f32_e32 v94, 0x42000000, v94
	v_mul_f32_e32 v95, 0x42000000, v95
	v_mul_f32_e32 v96, 0x42000000, v96
	v_mul_f32_e32 v97, 0x42000000, v97
	v_cvt_pk_fp8_f32 v166, v82, v83
	v_cvt_pk_fp8_f32 v167, v86, v87
	v_cvt_pk_fp8_f32 v168, v90, v91
	v_cvt_pk_fp8_f32 v169, v94, v95
	v_cvt_pk_fp8_f32 v166, v84, v85 op_sel:[0,0,1]
	v_cvt_pk_fp8_f32 v167, v88, v89 op_sel:[0,0,1]
	v_cvt_pk_fp8_f32 v168, v92, v93 op_sel:[0,0,1]
	v_cvt_pk_fp8_f32 v169, v96, v97 op_sel:[0,0,1]
	s_mov_b32 vcc_lo, 0xaaaaaaaa
	s_mov_b32 vcc_hi, 0xaaaaaaaa
	s_nop 1
	v_cndmask_b32_dpp v170, v154, v158, vcc quad_perm:[1,0,3,2] row_mask:0xf bank_mask:0xf
	v_cndmask_b32_dpp v174, v162, v166, vcc quad_perm:[1,0,3,2] row_mask:0xf bank_mask:0xf
	v_cndmask_b32_dpp v171, v155, v159, vcc quad_perm:[1,0,3,2] row_mask:0xf bank_mask:0xf
	v_cndmask_b32_dpp v175, v163, v167, vcc quad_perm:[1,0,3,2] row_mask:0xf bank_mask:0xf
	v_cndmask_b32_dpp v172, v156, v160, vcc quad_perm:[1,0,3,2] row_mask:0xf bank_mask:0xf
	v_cndmask_b32_dpp v176, v164, v168, vcc quad_perm:[1,0,3,2] row_mask:0xf bank_mask:0xf
	v_cndmask_b32_dpp v173, v157, v161, vcc quad_perm:[1,0,3,2] row_mask:0xf bank_mask:0xf
	v_cndmask_b32_dpp v177, v165, v169, vcc quad_perm:[1,0,3,2] row_mask:0xf bank_mask:0xf
	s_mov_b32 vcc_lo, 0x55555555
	s_mov_b32 vcc_hi, 0x55555555
	s_nop 1
	v_cndmask_b32_dpp v154, v158, v154, vcc quad_perm:[1,0,3,2] row_mask:0xf bank_mask:0xf
	v_cndmask_b32_dpp v162, v166, v162, vcc quad_perm:[1,0,3,2] row_mask:0xf bank_mask:0xf
	v_cndmask_b32_dpp v155, v159, v155, vcc quad_perm:[1,0,3,2] row_mask:0xf bank_mask:0xf
	v_cndmask_b32_dpp v163, v167, v163, vcc quad_perm:[1,0,3,2] row_mask:0xf bank_mask:0xf
	v_cndmask_b32_dpp v156, v160, v156, vcc quad_perm:[1,0,3,2] row_mask:0xf bank_mask:0xf
	v_cndmask_b32_dpp v164, v168, v164, vcc quad_perm:[1,0,3,2] row_mask:0xf bank_mask:0xf
	v_cndmask_b32_dpp v157, v161, v157, vcc quad_perm:[1,0,3,2] row_mask:0xf bank_mask:0xf
	v_cndmask_b32_dpp v165, v169, v165, vcc quad_perm:[1,0,3,2] row_mask:0xf bank_mask:0xf
	s_mov_b32 vcc_lo, 0xcccccccc
	s_mov_b32 vcc_hi, 0xcccccccc
	s_nop 1
	v_cndmask_b32_dpp v158, v154, v162, vcc quad_perm:[2,3,0,1] row_mask:0xf bank_mask:0xf
	v_cndmask_b32_dpp v166, v170, v174, vcc quad_perm:[2,3,0,1] row_mask:0xf bank_mask:0xf
	v_cndmask_b32_dpp v159, v155, v163, vcc quad_perm:[2,3,0,1] row_mask:0xf bank_mask:0xf
	v_cndmask_b32_dpp v167, v171, v175, vcc quad_perm:[2,3,0,1] row_mask:0xf bank_mask:0xf
	v_cndmask_b32_dpp v160, v156, v164, vcc quad_perm:[2,3,0,1] row_mask:0xf bank_mask:0xf
	v_cndmask_b32_dpp v168, v172, v176, vcc quad_perm:[2,3,0,1] row_mask:0xf bank_mask:0xf
	v_cndmask_b32_dpp v161, v157, v165, vcc quad_perm:[2,3,0,1] row_mask:0xf bank_mask:0xf
	v_cndmask_b32_dpp v169, v173, v177, vcc quad_perm:[2,3,0,1] row_mask:0xf bank_mask:0xf
	s_mov_b32 vcc_lo, 0x33333333
	s_mov_b32 vcc_hi, 0x33333333
	s_nop 1
	v_cndmask_b32_dpp v154, v162, v154, vcc quad_perm:[2,3,0,1] row_mask:0xf bank_mask:0xf
	v_cndmask_b32_dpp v170, v174, v170, vcc quad_perm:[2,3,0,1] row_mask:0xf bank_mask:0xf
	v_cndmask_b32_dpp v155, v163, v155, vcc quad_perm:[2,3,0,1] row_mask:0xf bank_mask:0xf
	v_cndmask_b32_dpp v171, v175, v171, vcc quad_perm:[2,3,0,1] row_mask:0xf bank_mask:0xf
	v_cndmask_b32_dpp v156, v164, v156, vcc quad_perm:[2,3,0,1] row_mask:0xf bank_mask:0xf
	v_cndmask_b32_dpp v172, v176, v172, vcc quad_perm:[2,3,0,1] row_mask:0xf bank_mask:0xf
	v_cndmask_b32_dpp v157, v165, v157, vcc quad_perm:[2,3,0,1] row_mask:0xf bank_mask:0xf
	v_cndmask_b32_dpp v173, v177, v173, vcc quad_perm:[2,3,0,1] row_mask:0xf bank_mask:0xf
	global_store_dwordx4 v179, v[154:157], s[82:83] nt
	global_store_dwordx4 v180, v[170:173], s[82:83] nt
	global_store_dwordx4 v181, v[158:161], s[82:83] nt
	global_store_dwordx4 v190, v[166:169], s[82:83] nt
	v_readlane_b32 s2, v239, 0
	s_lshr_b32 s2, s2, 6
	s_add_i32 s2, s2, 6
	s_cmp_gt_u32 s2, 11
	s_cbranch_scc1 .Lhw_seam5_done
	s_add_i32 s2, s2, 60
	s_mul_i32 s2, s2, s74
	v_readlane_b32 s9, v239, 23
	s_lshr_b32 s9, s9, 3
	s_add_i32 s2, s2, s9
	s_cmp_gt_u32 s2, 24575
	s_cbranch_scc1 .Lhw_seam5_done
	v_mbcnt_lo_u32_b32 v178, -1, 0
	v_mbcnt_hi_u32_b32 v178, -1, v178
	v_and_b32_e32 v179, 60, v178
	v_lshlrev_b32_e32 v179, 10, v179
	v_and_b32_e32 v180, 3, v178
	v_lshl_or_b32 v179, v180, 4, v179
	v_add_u32_e32 v180, 0x400, v179
	v_add_u32_e32 v181, 0x800, v179
	v_add_u32_e32 v190, 0xc00, v179
	v_lshlrev_b32_e32 v178, 2, v178
	s_cmp_lt_u32 s2, 16384
	s_cbranch_scc0 .Lhw_dn_s5_1
	s_lshr_b32 s9, s2, 9
	s_bfe_u32 s32, s2, 0x40005
	s_and_b32 s53, s2, 31
	s_lshl_b32 s69, s9, 23
	s_lshl_b32 s100, s32, 19
	s_add_i32 s69, s69, s100
	s_lshl_b32 s100, s53, 8
	s_add_i32 s69, s69, s100
	s_lshl_b32 s98, s9, 11
	s_bfe_u32 s100, s53, 0x30001
	s_lshl_b32 s100, s100, 8
	s_add_i32 s98, s98, s100
	s_lshr_b32 s100, s53, 4
	s_lshl_b32 s100, s100, 7
	s_add_i32 s98, s98, s100
	s_and_b32 s100, s53, 1
	s_lshl_b32 s100, s100, 6
	s_add_i32 s98, s98, s100
	s_lshl_b32 s98, s98, 10
	s_lshl_b32 s100, s32, 6
	s_add_i32 s98, s98, s100
	s_add_i32 s98, s98, 0x2000000
	v_readlane_b32 s82, v239, 11
	v_readlane_b32 s83, v239, 12
	s_movk_i32 s89, 8192
	s_branch .Lhw_go_s5_1

.Lhw_seam6:
	s_mov_b64 exec, -1
	v_readlane_b32 s2, v239, 0
	s_lshr_b32 s2, s2, 6
	s_add_i32 s2, s2, -1
	s_cmp_gt_u32 s2, 11
	s_cbranch_scc1 .Lhw_seam6_done
	s_add_i32 s2, s2, 72
	s_mul_i32 s2, s2, s74
	v_readlane_b32 s9, v239, 23
	s_lshr_b32 s9, s9, 3
	s_add_i32 s2, s2, s9
	s_cmp_gt_u32 s2, 24575
	s_cbranch_scc1 .Lhw_seam6_done
	v_mbcnt_lo_u32_b32 v178, -1, 0
	v_mbcnt_hi_u32_b32 v178, -1, v178
	v_and_b32_e32 v179, 60, v178
	v_lshlrev_b32_e32 v179, 10, v179
	v_and_b32_e32 v180, 3, v178
	v_lshl_or_b32 v179, v180, 4, v179
	v_add_u32_e32 v180, 0x400, v179
	v_add_u32_e32 v181, 0x800, v179
	v_add_u32_e32 v190, 0xc00, v179
	v_lshlrev_b32_e32 v178, 2, v178
	s_cmp_lt_u32 s2, 16384
	s_cbranch_scc0 .Lhw_dn_s6_0
	s_lshr_b32 s9, s2, 9
	s_bfe_u32 s32, s2, 0x40005
	s_and_b32 s53, s2, 31
	s_lshl_b32 s69, s9, 23
	s_lshl_b32 s100, s32, 19
	s_add_i32 s69, s69, s100
	s_lshl_b32 s100, s53, 8
	s_add_i32 s69, s69, s100
	s_lshl_b32 s98, s9, 11
	s_bfe_u32 s100, s53, 0x30001
	s_lshl_b32 s100, s100, 8
	s_add_i32 s98, s98, s100
	s_lshr_b32 s100, s53, 4
	s_lshl_b32 s100, s100, 7
	s_add_i32 s98, s98, s100
	s_and_b32 s100, s53, 1
	s_lshl_b32 s100, s100, 6
	s_add_i32 s98, s98, s100
	s_lshl_b32 s98, s98, 10
	s_lshl_b32 s100, s32, 6
	s_add_i32 s98, s98, s100
	s_add_i32 s98, s98, 0x2000000
	v_readlane_b32 s82, v239, 11
	v_readlane_b32 s83, v239, 12
	s_movk_i32 s89, 8192
	s_branch .Lhw_go_s6_0

.Lhw_go_s6_0:
	s_add_u32 s100, s82, s69
	s_addc_u32 s101, s83, 0
	v_readlane_b32 s82, v239, 44
	v_readlane_b32 s83, v239, 45
	s_add_u32 s82, s82, s98
	s_addc_u32 s83, s83, 0
	global_load_dword v34, v178, s[100:101] nt
	s_add_u32 s100, s100, s89
	s_addc_u32 s101, s101, 0
	global_load_dword v35, v178, s[100:101] nt
	s_add_u32 s100, s100, s89
	s_addc_u32 s101, s101, 0
	global_load_dword v36, v178, s[100:101] nt
	s_add_u32 s100, s100, s89
	s_addc_u32 s101, s101, 0
	global_load_dword v37, v178, s[100:101] nt
	s_add_u32 s100, s100, s89
	s_addc_u32 s101, s101, 0
	global_load_dword v38, v178, s[100:101] nt
	s_add_u32 s100, s100, s89
	s_addc_u32 s101, s101, 0
	global_load_dword v39, v178, s[100:101] nt
	s_add_u32 s100, s100, s89
	s_addc_u32 s101, s101, 0
	global_load_dword v40, v178, s[100:101] nt
	s_add_u32 s100, s100, s89
	s_addc_u32 s101, s101, 0
	global_load_dword v41, v178, s[100:101] nt
	s_add_u32 s100, s100, s89
	s_addc_u32 s101, s101, 0
	global_load_dword v42, v178, s[100:101] nt
	s_add_u32 s100, s100, s89
	s_addc_u32 s101, s101, 0
	global_load_dword v43, v178, s[100:101] nt
	s_add_u32 s100, s100, s89
	s_addc_u32 s101, s101, 0
	global_load_dword v44, v178, s[100:101] nt
	s_add_u32 s100, s100, s89
	s_addc_u32 s101, s101, 0
	global_load_dword v45, v178, s[100:101] nt
	s_add_u32 s100, s100, s89
	s_addc_u32 s101, s101, 0
	global_load_dword v46, v178, s[100:101] nt
	s_add_u32 s100, s100, s89
	s_addc_u32 s101, s101, 0
	global_load_dword v47, v178, s[100:101] nt
	s_add_u32 s100, s100, s89
	s_addc_u32 s101, s101, 0
	global_load_dword v48, v178, s[100:101] nt
	s_add_u32 s100, s100, s89
	s_addc_u32 s101, s101, 0
	global_load_dword v49, v178, s[100:101] nt
	s_add_u32 s100, s100, s89
	s_addc_u32 s101, s101, 0
	global_load_dword v50, v178, s[100:101] nt
	s_add_u32 s100, s100, s89
	s_addc_u32 s101, s101, 0
	global_load_dword v51, v178, s[100:101] nt
	s_add_u32 s100, s100, s89
	s_addc_u32 s101, s101, 0
	global_load_dword v52, v178, s[100:101] nt
	s_add_u32 s100, s100, s89
	s_addc_u32 s101, s101, 0
	global_load_dword v53, v178, s[100:101] nt
	s_add_u32 s100, s100, s89
	s_addc_u32 s101, s101, 0
	global_load_dword v54, v178, s[100:101] nt
	s_add_u32 s100, s100, s89
	s_addc_u32 s101, s101, 0
	global_load_dword v55, v178, s[100:101] nt
	s_add_u32 s100, s100, s89
	s_addc_u32 s101, s101, 0
	global_load_dword v56, v178, s[100:101] nt
	s_add_u32 s100, s100, s89
	s_addc_u32 s101, s101, 0
	global_load_dword v57, v178, s[100:101] nt
	s_add_u32 s100, s100, s89
	s_addc_u32 s101, s101, 0
	global_load_dword v58, v178, s[100:101] nt
	s_add_u32 s100, s100, s89
	s_addc_u32 s101, s101, 0
	global_load_dword v59, v178, s[100:101] nt
	s_add_u32 s100, s100, s89
	s_addc_u32 s101, s101, 0
	global_load_dword v60, v178, s[100:101] nt
	s_add_u32 s100, s100, s89
	s_addc_u32 s101, s101, 0
	global_load_dword v61, v178, s[100:101] nt
	s_add_u32 s100, s100, s89
	s_addc_u32 s101, s101, 0
	global_load_dword v62, v178, s[100:101] nt
	s_add_u32 s100, s100, s89
	s_addc_u32 s101, s101, 0
	global_load_dword v63, v178, s[100:101] nt
	s_add_u32 s100, s100, s89
	s_addc_u32 s101, s101, 0
	global_load_dword v64, v178, s[100:101] nt
	s_add_u32 s100, s100, s89
	s_addc_u32 s101, s101, 0
	global_load_dword v65, v178, s[100:101] nt
	s_add_u32 s100, s100, s89
	s_addc_u32 s101, s101, 0
	global_load_dword v66, v178, s[100:101] nt
	s_add_u32 s100, s100, s89
	s_addc_u32 s101, s101, 0
	global_load_dword v67, v178, s[100:101] nt
	s_add_u32 s100, s100, s89
	s_addc_u32 s101, s101, 0
	global_load_dword v68, v178, s[100:101] nt
	s_add_u32 s100, s100, s89
	s_addc_u32 s101, s101, 0
	global_load_dword v69, v178, s[100:101] nt
	s_add_u32 s100, s100, s89
	s_addc_u32 s101, s101, 0
	global_load_dword v70, v178, s[100:101] nt
	s_add_u32 s100, s100, s89
	s_addc_u32 s101, s101, 0
	global_load_dword v71, v178, s[100:101] nt
	s_add_u32 s100, s100, s89
	s_addc_u32 s101, s101, 0
	global_load_dword v72, v178, s[100:101] nt
	s_add_u32 s100, s100, s89
	s_addc_u32 s101, s101, 0
	global_load_dword v73, v178, s[100:101] nt
	s_add_u32 s100, s100, s89
	s_addc_u32 s101, s101, 0
	global_load_dword v74, v178, s[100:101] nt
	s_add_u32 s100, s100, s89
	s_addc_u32 s101, s101, 0
	global_load_dword v75, v178, s[100:101] nt
	s_add_u32 s100, s100, s89
	s_addc_u32 s101, s101, 0
	global_load_dword v76, v178, s[100:101] nt
	s_add_u32 s100, s100, s89
	s_addc_u32 s101, s101, 0
	global_load_dword v77, v178, s[100:101] nt
	s_add_u32 s100, s100, s89
	s_addc_u32 s101, s101, 0
	global_load_dword v78, v178, s[100:101] nt
	s_add_u32 s100, s100, s89
	s_addc_u32 s101, s101, 0
	global_load_dword v79, v178, s[100:101] nt
	s_add_u32 s100, s100, s89
	s_addc_u32 s101, s101, 0
	global_load_dword v80, v178, s[100:101] nt
	s_add_u32 s100, s100, s89
	s_addc_u32 s101, s101, 0
	global_load_dword v81, v178, s[100:101] nt
	s_add_u32 s100, s100, s89
	s_addc_u32 s101, s101, 0
	global_load_dword v82, v178, s[100:101] nt
	s_add_u32 s100, s100, s89
	s_addc_u32 s101, s101, 0
	global_load_dword v83, v178, s[100:101] nt
	s_add_u32 s100, s100, s89
	s_addc_u32 s101, s101, 0
	global_load_dword v84, v178, s[100:101] nt
	s_add_u32 s100, s100, s89
	s_addc_u32 s101, s101, 0
	global_load_dword v85, v178, s[100:101] nt
	s_add_u32 s100, s100, s89
	s_addc_u32 s101, s101, 0
	global_load_dword v86, v178, s[100:101] nt
	s_add_u32 s100, s100, s89
	s_addc_u32 s101, s101, 0
	global_load_dword v87, v178, s[100:101] nt
	s_add_u32 s100, s100, s89
	s_addc_u32 s101, s101, 0
	global_load_dword v88, v178, s[100:101] nt
	s_add_u32 s100, s100, s89
	s_addc_u32 s101, s101, 0
	global_load_dword v89, v178, s[100:101] nt
	s_add_u32 s100, s100, s89
	s_addc_u32 s101, s101, 0
	global_load_dword v90, v178, s[100:101] nt
	s_add_u32 s100, s100, s89
	s_addc_u32 s101, s101, 0
	global_load_dword v91, v178, s[100:101] nt
	s_add_u32 s100, s100, s89
	s_addc_u32 s101, s101, 0
	global_load_dword v92, v178, s[100:101] nt
	s_add_u32 s100, s100, s89
	s_addc_u32 s101, s101, 0
	global_load_dword v93, v178, s[100:101] nt
	s_add_u32 s100, s100, s89
	s_addc_u32 s101, s101, 0
	global_load_dword v94, v178, s[100:101] nt
	s_add_u32 s100, s100, s89
	s_addc_u32 s101, s101, 0
	global_load_dword v95, v178, s[100:101] nt
	s_add_u32 s100, s100, s89
	s_addc_u32 s101, s101, 0
	global_load_dword v96, v178, s[100:101] nt
	s_add_u32 s100, s100, s89
	s_addc_u32 s101, s101, 0
	global_load_dword v97, v178, s[100:101] nt
	s_add_u32 s100, s100, s89
	s_addc_u32 s101, s101, 0
	s_waitcnt vmcnt(48)
	v_mul_f32_e32 v34, 0x42000000, v34
	v_mul_f32_e32 v35, 0x42000000, v35
	v_mul_f32_e32 v36, 0x42000000, v36
	v_mul_f32_e32 v37, 0x42000000, v37
	v_mul_f32_e32 v38, 0x42000000, v38
	v_mul_f32_e32 v39, 0x42000000, v39
	v_mul_f32_e32 v40, 0x42000000, v40
	v_mul_f32_e32 v41, 0x42000000, v41
	v_mul_f32_e32 v42, 0x42000000, v42
	v_mul_f32_e32 v43, 0x42000000, v43
	v_mul_f32_e32 v44, 0x42000000, v44
	v_mul_f32_e32 v45, 0x42000000, v45
	v_mul_f32_e32 v46, 0x42000000, v46
	v_mul_f32_e32 v47, 0x42000000, v47
	v_mul_f32_e32 v48, 0x42000000, v48
	v_mul_f32_e32 v49, 0x42000000, v49
	v_cvt_pk_fp8_f32 v154, v34, v35
	v_cvt_pk_fp8_f32 v155, v38, v39
	v_cvt_pk_fp8_f32 v156, v42, v43
	v_cvt_pk_fp8_f32 v157, v46, v47
	v_cvt_pk_fp8_f32 v154, v36, v37 op_sel:[0,0,1]
	v_cvt_pk_fp8_f32 v155, v40, v41 op_sel:[0,0,1]
	v_cvt_pk_fp8_f32 v156, v44, v45 op_sel:[0,0,1]
	v_cvt_pk_fp8_f32 v157, v48, v49 op_sel:[0,0,1]
	s_waitcnt vmcnt(32)
	v_mul_f32_e32 v50, 0x42000000, v50
	v_mul_f32_e32 v51, 0x42000000, v51
	v_mul_f32_e32 v52, 0x42000000, v52
	v_mul_f32_e32 v53, 0x42000000, v53
	v_mul_f32_e32 v54, 0x42000000, v54
	v_mul_f32_e32 v55, 0x42000000, v55
	v_mul_f32_e32 v56, 0x42000000, v56
	v_mul_f32_e32 v57, 0x42000000, v57
	v_mul_f32_e32 v58, 0x42000000, v58
	v_mul_f32_e32 v59, 0x42000000, v59
	v_mul_f32_e32 v60, 0x42000000, v60
	v_mul_f32_e32 v61, 0x42000000, v61
	v_mul_f32_e32 v62, 0x42000000, v62
	v_mul_f32_e32 v63, 0x42000000, v63
	v_mul_f32_e32 v64, 0x42000000, v64
	v_mul_f32_e32 v65, 0x42000000, v65
	v_cvt_pk_fp8_f32 v158, v50, v51
	v_cvt_pk_fp8_f32 v159, v54, v55
	v_cvt_pk_fp8_f32 v160, v58, v59
	v_cvt_pk_fp8_f32 v161, v62, v63
	v_cvt_pk_fp8_f32 v158, v52, v53 op_sel:[0,0,1]
	v_cvt_pk_fp8_f32 v159, v56, v57 op_sel:[0,0,1]
	v_cvt_pk_fp8_f32 v160, v60, v61 op_sel:[0,0,1]
	v_cvt_pk_fp8_f32 v161, v64, v65 op_sel:[0,0,1]
	s_waitcnt vmcnt(16)
	v_mul_f32_e32 v66, 0x42000000, v66
	v_mul_f32_e32 v67, 0x42000000, v67
	v_mul_f32_e32 v68, 0x42000000, v68
	v_mul_f32_e32 v69, 0x42000000, v69
	v_mul_f32_e32 v70, 0x42000000, v70
	v_mul_f32_e32 v71, 0x42000000, v71
	v_mul_f32_e32 v72, 0x42000000, v72
	v_mul_f32_e32 v73, 0x42000000, v73
	v_mul_f32_e32 v74, 0x42000000, v74
	v_mul_f32_e32 v75, 0x42000000, v75
	v_mul_f32_e32 v76, 0x42000000, v76
	v_mul_f32_e32 v77, 0x42000000, v77
	v_mul_f32_e32 v78, 0x42000000, v78
	v_mul_f32_e32 v79, 0x42000000, v79
	v_mul_f32_e32 v80, 0x42000000, v80
	v_mul_f32_e32 v81, 0x42000000, v81
	v_cvt_pk_fp8_f32 v162, v66, v67
	v_cvt_pk_fp8_f32 v163, v70, v71
	v_cvt_pk_fp8_f32 v164, v74, v75
	v_cvt_pk_fp8_f32 v165, v78, v79
	v_cvt_pk_fp8_f32 v162, v68, v69 op_sel:[0,0,1]
	v_cvt_pk_fp8_f32 v163, v72, v73 op_sel:[0,0,1]
	v_cvt_pk_fp8_f32 v164, v76, v77 op_sel:[0,0,1]
	v_cvt_pk_fp8_f32 v165, v80, v81 op_sel:[0,0,1]
	s_waitcnt vmcnt(0)
	v_mul_f32_e32 v82, 0x42000000, v82
	v_mul_f32_e32 v83, 0x42000000, v83
	v_mul_f32_e32 v84, 0x42000000, v84
	v_mul_f32_e32 v85, 0x42000000, v85
	v_mul_f32_e32 v86, 0x42000000, v86
	v_mul_f32_e32 v87, 0x42000000, v87
	v_mul_f32_e32 v88, 0x42000000, v88
	v_mul_f32_e32 v89, 0x42000000, v89
	v_mul_f32_e32 v90, 0x42000000, v90
	v_mul_f32_e32 v91, 0x42000000, v91
	v_mul_f32_e32 v92, 0x42000000, v92
	v_mul_f32_e32 v93, 0x42000000, v93
	v_mul_f32_e32 v94, 0x42000000, v94
	v_mul_f32_e32 v95, 0x42000000, v95
	v_mul_f32_e32 v96, 0x42000000, v96
	v_mul_f32_e32 v97, 0x42000000, v97
	v_cvt_pk_fp8_f32 v166, v82, v83
	v_cvt_pk_fp8_f32 v167, v86, v87
	v_cvt_pk_fp8_f32 v168, v90, v91
	v_cvt_pk_fp8_f32 v169, v94, v95
	v_cvt_pk_fp8_f32 v166, v84, v85 op_sel:[0,0,1]
	v_cvt_pk_fp8_f32 v167, v88, v89 op_sel:[0,0,1]
	v_cvt_pk_fp8_f32 v168, v92, v93 op_sel:[0,0,1]
	v_cvt_pk_fp8_f32 v169, v96, v97 op_sel:[0,0,1]
	s_mov_b32 vcc_lo, 0xaaaaaaaa
	s_mov_b32 vcc_hi, 0xaaaaaaaa
	s_nop 1
	v_cndmask_b32_dpp v170, v154, v158, vcc quad_perm:[1,0,3,2] row_mask:0xf bank_mask:0xf
	v_cndmask_b32_dpp v174, v162, v166, vcc quad_perm:[1,0,3,2] row_mask:0xf bank_mask:0xf
	v_cndmask_b32_dpp v171, v155, v159, vcc quad_perm:[1,0,3,2] row_mask:0xf bank_mask:0xf
	v_cndmask_b32_dpp v175, v163, v167, vcc quad_perm:[1,0,3,2] row_mask:0xf bank_mask:0xf
	v_cndmask_b32_dpp v172, v156, v160, vcc quad_perm:[1,0,3,2] row_mask:0xf bank_mask:0xf
	v_cndmask_b32_dpp v176, v164, v168, vcc quad_perm:[1,0,3,2] row_mask:0xf bank_mask:0xf
	v_cndmask_b32_dpp v173, v157, v161, vcc quad_perm:[1,0,3,2] row_mask:0xf bank_mask:0xf
	v_cndmask_b32_dpp v177, v165, v169, vcc quad_perm:[1,0,3,2] row_mask:0xf bank_mask:0xf
	s_mov_b32 vcc_lo, 0x55555555
	s_mov_b32 vcc_hi, 0x55555555
	s_nop 1
	v_cndmask_b32_dpp v154, v158, v154, vcc quad_perm:[1,0,3,2] row_mask:0xf bank_mask:0xf
	v_cndmask_b32_dpp v162, v166, v162, vcc quad_perm:[1,0,3,2] row_mask:0xf bank_mask:0xf
	v_cndmask_b32_dpp v155, v159, v155, vcc quad_perm:[1,0,3,2] row_mask:0xf bank_mask:0xf
	v_cndmask_b32_dpp v163, v167, v163, vcc quad_perm:[1,0,3,2] row_mask:0xf bank_mask:0xf
	v_cndmask_b32_dpp v156, v160, v156, vcc quad_perm:[1,0,3,2] row_mask:0xf bank_mask:0xf
	v_cndmask_b32_dpp v164, v168, v164, vcc quad_perm:[1,0,3,2] row_mask:0xf bank_mask:0xf
	v_cndmask_b32_dpp v157, v161, v157, vcc quad_perm:[1,0,3,2] row_mask:0xf bank_mask:0xf
	v_cndmask_b32_dpp v165, v169, v165, vcc quad_perm:[1,0,3,2] row_mask:0xf bank_mask:0xf
	s_mov_b32 vcc_lo, 0xcccccccc
	s_mov_b32 vcc_hi, 0xcccccccc
	s_nop 1
	v_cndmask_b32_dpp v158, v154, v162, vcc quad_perm:[2,3,0,1] row_mask:0xf bank_mask:0xf
	v_cndmask_b32_dpp v166, v170, v174, vcc quad_perm:[2,3,0,1] row_mask:0xf bank_mask:0xf
	v_cndmask_b32_dpp v159, v155, v163, vcc quad_perm:[2,3,0,1] row_mask:0xf bank_mask:0xf
	v_cndmask_b32_dpp v167, v171, v175, vcc quad_perm:[2,3,0,1] row_mask:0xf bank_mask:0xf
	v_cndmask_b32_dpp v160, v156, v164, vcc quad_perm:[2,3,0,1] row_mask:0xf bank_mask:0xf
	v_cndmask_b32_dpp v168, v172, v176, vcc quad_perm:[2,3,0,1] row_mask:0xf bank_mask:0xf
	v_cndmask_b32_dpp v161, v157, v165, vcc quad_perm:[2,3,0,1] row_mask:0xf bank_mask:0xf
	v_cndmask_b32_dpp v169, v173, v177, vcc quad_perm:[2,3,0,1] row_mask:0xf bank_mask:0xf
	s_mov_b32 vcc_lo, 0x33333333
	s_mov_b32 vcc_hi, 0x33333333
	s_nop 1
	v_cndmask_b32_dpp v154, v162, v154, vcc quad_perm:[2,3,0,1] row_mask:0xf bank_mask:0xf
	v_cndmask_b32_dpp v170, v174, v170, vcc quad_perm:[2,3,0,1] row_mask:0xf bank_mask:0xf
	v_cndmask_b32_dpp v155, v163, v155, vcc quad_perm:[2,3,0,1] row_mask:0xf bank_mask:0xf
	v_cndmask_b32_dpp v171, v175, v171, vcc quad_perm:[2,3,0,1] row_mask:0xf bank_mask:0xf
	v_cndmask_b32_dpp v156, v164, v156, vcc quad_perm:[2,3,0,1] row_mask:0xf bank_mask:0xf
	v_cndmask_b32_dpp v172, v176, v172, vcc quad_perm:[2,3,0,1] row_mask:0xf bank_mask:0xf
	v_cndmask_b32_dpp v157, v165, v157, vcc quad_perm:[2,3,0,1] row_mask:0xf bank_mask:0xf
	v_cndmask_b32_dpp v173, v177, v173, vcc quad_perm:[2,3,0,1] row_mask:0xf bank_mask:0xf
	global_store_dwordx4 v179, v[154:157], s[82:83] nt
	global_store_dwordx4 v180, v[170:173], s[82:83] nt
	global_store_dwordx4 v181, v[158:161], s[82:83] nt
	global_store_dwordx4 v190, v[166:169], s[82:83] nt
	v_readlane_b32 s2, v239, 0
	s_lshr_b32 s2, s2, 6
	s_add_i32 s2, s2, 6
	s_cmp_gt_u32 s2, 11
	s_cbranch_scc1 .Lhw_seam6_done
	s_add_i32 s2, s2, 72
	s_mul_i32 s2, s2, s74
	v_readlane_b32 s9, v239, 23
	s_lshr_b32 s9, s9, 3
	s_add_i32 s2, s2, s9
	s_cmp_gt_u32 s2, 24575
	s_cbranch_scc1 .Lhw_seam6_done
	v_mbcnt_lo_u32_b32 v178, -1, 0
	v_mbcnt_hi_u32_b32 v178, -1, v178
	v_and_b32_e32 v179, 60, v178
	v_lshlrev_b32_e32 v179, 10, v179
	v_and_b32_e32 v180, 3, v178
	v_lshl_or_b32 v179, v180, 4, v179
	v_add_u32_e32 v180, 0x400, v179
	v_add_u32_e32 v181, 0x800, v179
	v_add_u32_e32 v190, 0xc00, v179
	v_lshlrev_b32_e32 v178, 2, v178
	s_cmp_lt_u32 s2, 16384
	s_cbranch_scc0 .Lhw_dn_s6_1
	s_lshr_b32 s9, s2, 9
	s_bfe_u32 s32, s2, 0x40005
	s_and_b32 s53, s2, 31
	s_lshl_b32 s69, s9, 23
	s_lshl_b32 s100, s32, 19
	s_add_i32 s69, s69, s100
	s_lshl_b32 s100, s53, 8
	s_add_i32 s69, s69, s100
	s_lshl_b32 s98, s9, 11
	s_bfe_u32 s100, s53, 0x30001
	s_lshl_b32 s100, s100, 8
	s_add_i32 s98, s98, s100
	s_lshr_b32 s100, s53, 4
	s_lshl_b32 s100, s100, 7
	s_add_i32 s98, s98, s100
	s_and_b32 s100, s53, 1
	s_lshl_b32 s100, s100, 6
	s_add_i32 s98, s98, s100
	s_lshl_b32 s98, s98, 10
	s_lshl_b32 s100, s32, 6
	s_add_i32 s98, s98, s100
	s_add_i32 s98, s98, 0x2000000
	v_readlane_b32 s82, v239, 11
	v_readlane_b32 s83, v239, 12
	s_movk_i32 s89, 8192
	s_branch .Lhw_go_s6_1

.Lhw_seam7:
	s_mov_b64 exec, -1
	v_readlane_b32 s2, v239, 0
	s_lshr_b32 s2, s2, 6
	s_add_i32 s2, s2, -1
	s_cmp_gt_u32 s2, 11
	s_cbranch_scc1 .Lhw_seam7_done
	s_add_i32 s2, s2, 84
	s_mul_i32 s2, s2, s74
	v_readlane_b32 s9, v239, 23
	s_lshr_b32 s9, s9, 3
	s_add_i32 s2, s2, s9
	s_cmp_gt_u32 s2, 24575
	s_cbranch_scc1 .Lhw_seam7_done
	v_mbcnt_lo_u32_b32 v178, -1, 0
	v_mbcnt_hi_u32_b32 v178, -1, v178
	v_and_b32_e32 v179, 60, v178
	v_lshlrev_b32_e32 v179, 10, v179
	v_and_b32_e32 v180, 3, v178
	v_lshl_or_b32 v179, v180, 4, v179
	v_add_u32_e32 v180, 0x400, v179
	v_add_u32_e32 v181, 0x800, v179
	v_add_u32_e32 v190, 0xc00, v179
	v_lshlrev_b32_e32 v178, 2, v178
	s_cmp_lt_u32 s2, 16384
	s_cbranch_scc0 .Lhw_dn_s7_0
	s_lshr_b32 s9, s2, 9
	s_bfe_u32 s32, s2, 0x40005
	s_and_b32 s53, s2, 31
	s_lshl_b32 s69, s9, 23
	s_lshl_b32 s100, s32, 19
	s_add_i32 s69, s69, s100
	s_lshl_b32 s100, s53, 8
	s_add_i32 s69, s69, s100
	s_lshl_b32 s98, s9, 11
	s_bfe_u32 s100, s53, 0x30001
	s_lshl_b32 s100, s100, 8
	s_add_i32 s98, s98, s100
	s_lshr_b32 s100, s53, 4
	s_lshl_b32 s100, s100, 7
	s_add_i32 s98, s98, s100
	s_and_b32 s100, s53, 1
	s_lshl_b32 s100, s100, 6
	s_add_i32 s98, s98, s100
	s_lshl_b32 s98, s98, 10
	s_lshl_b32 s100, s32, 6
	s_add_i32 s98, s98, s100
	s_add_i32 s98, s98, 0x2000000
	v_readlane_b32 s82, v239, 11
	v_readlane_b32 s83, v239, 12
	s_movk_i32 s89, 8192
	s_branch .Lhw_go_s7_0

.Lhw_go_s7_0:
	s_add_u32 s100, s82, s69
	s_addc_u32 s101, s83, 0
	v_readlane_b32 s82, v239, 44
	v_readlane_b32 s83, v239, 45
	s_add_u32 s82, s82, s98
	s_addc_u32 s83, s83, 0
	global_load_dword v34, v178, s[100:101] nt
	s_add_u32 s100, s100, s89
	s_addc_u32 s101, s101, 0
	global_load_dword v35, v178, s[100:101] nt
	s_add_u32 s100, s100, s89
	s_addc_u32 s101, s101, 0
	global_load_dword v36, v178, s[100:101] nt
	s_add_u32 s100, s100, s89
	s_addc_u32 s101, s101, 0
	global_load_dword v37, v178, s[100:101] nt
	s_add_u32 s100, s100, s89
	s_addc_u32 s101, s101, 0
	global_load_dword v38, v178, s[100:101] nt
	s_add_u32 s100, s100, s89
	s_addc_u32 s101, s101, 0
	global_load_dword v39, v178, s[100:101] nt
	s_add_u32 s100, s100, s89
	s_addc_u32 s101, s101, 0
	global_load_dword v40, v178, s[100:101] nt
	s_add_u32 s100, s100, s89
	s_addc_u32 s101, s101, 0
	global_load_dword v41, v178, s[100:101] nt
	s_add_u32 s100, s100, s89
	s_addc_u32 s101, s101, 0
	global_load_dword v42, v178, s[100:101] nt
	s_add_u32 s100, s100, s89
	s_addc_u32 s101, s101, 0
	global_load_dword v43, v178, s[100:101] nt
	s_add_u32 s100, s100, s89
	s_addc_u32 s101, s101, 0
	global_load_dword v44, v178, s[100:101] nt
	s_add_u32 s100, s100, s89
	s_addc_u32 s101, s101, 0
	global_load_dword v45, v178, s[100:101] nt
	s_add_u32 s100, s100, s89
	s_addc_u32 s101, s101, 0
	global_load_dword v46, v178, s[100:101] nt
	s_add_u32 s100, s100, s89
	s_addc_u32 s101, s101, 0
	global_load_dword v47, v178, s[100:101] nt
	s_add_u32 s100, s100, s89
	s_addc_u32 s101, s101, 0
	global_load_dword v48, v178, s[100:101] nt
	s_add_u32 s100, s100, s89
	s_addc_u32 s101, s101, 0
	global_load_dword v49, v178, s[100:101] nt
	s_add_u32 s100, s100, s89
	s_addc_u32 s101, s101, 0
	global_load_dword v50, v178, s[100:101] nt
	s_add_u32 s100, s100, s89
	s_addc_u32 s101, s101, 0
	global_load_dword v51, v178, s[100:101] nt
	s_add_u32 s100, s100, s89
	s_addc_u32 s101, s101, 0
	global_load_dword v52, v178, s[100:101] nt
	s_add_u32 s100, s100, s89
	s_addc_u32 s101, s101, 0
	global_load_dword v53, v178, s[100:101] nt
	s_add_u32 s100, s100, s89
	s_addc_u32 s101, s101, 0
	global_load_dword v54, v178, s[100:101] nt
	s_add_u32 s100, s100, s89
	s_addc_u32 s101, s101, 0
	global_load_dword v55, v178, s[100:101] nt
	s_add_u32 s100, s100, s89
	s_addc_u32 s101, s101, 0
	global_load_dword v56, v178, s[100:101] nt
	s_add_u32 s100, s100, s89
	s_addc_u32 s101, s101, 0
	global_load_dword v57, v178, s[100:101] nt
	s_add_u32 s100, s100, s89
	s_addc_u32 s101, s101, 0
	global_load_dword v58, v178, s[100:101] nt
	s_add_u32 s100, s100, s89
	s_addc_u32 s101, s101, 0
	global_load_dword v59, v178, s[100:101] nt
	s_add_u32 s100, s100, s89
	s_addc_u32 s101, s101, 0
	global_load_dword v60, v178, s[100:101] nt
	s_add_u32 s100, s100, s89
	s_addc_u32 s101, s101, 0
	global_load_dword v61, v178, s[100:101] nt
	s_add_u32 s100, s100, s89
	s_addc_u32 s101, s101, 0
	global_load_dword v62, v178, s[100:101] nt
	s_add_u32 s100, s100, s89
	s_addc_u32 s101, s101, 0
	global_load_dword v63, v178, s[100:101] nt
	s_add_u32 s100, s100, s89
	s_addc_u32 s101, s101, 0
	global_load_dword v64, v178, s[100:101] nt
	s_add_u32 s100, s100, s89
	s_addc_u32 s101, s101, 0
	global_load_dword v65, v178, s[100:101] nt
	s_add_u32 s100, s100, s89
	s_addc_u32 s101, s101, 0
	global_load_dword v66, v178, s[100:101] nt
	s_add_u32 s100, s100, s89
	s_addc_u32 s101, s101, 0
	global_load_dword v67, v178, s[100:101] nt
	s_add_u32 s100, s100, s89
	s_addc_u32 s101, s101, 0
	global_load_dword v68, v178, s[100:101] nt
	s_add_u32 s100, s100, s89
	s_addc_u32 s101, s101, 0
	global_load_dword v69, v178, s[100:101] nt
	s_add_u32 s100, s100, s89
	s_addc_u32 s101, s101, 0
	global_load_dword v70, v178, s[100:101] nt
	s_add_u32 s100, s100, s89
	s_addc_u32 s101, s101, 0
	global_load_dword v71, v178, s[100:101] nt
	s_add_u32 s100, s100, s89
	s_addc_u32 s101, s101, 0
	global_load_dword v72, v178, s[100:101] nt
	s_add_u32 s100, s100, s89
	s_addc_u32 s101, s101, 0
	global_load_dword v73, v178, s[100:101] nt
	s_add_u32 s100, s100, s89
	s_addc_u32 s101, s101, 0
	global_load_dword v74, v178, s[100:101] nt
	s_add_u32 s100, s100, s89
	s_addc_u32 s101, s101, 0
	global_load_dword v75, v178, s[100:101] nt
	s_add_u32 s100, s100, s89
	s_addc_u32 s101, s101, 0
	global_load_dword v76, v178, s[100:101] nt
	s_add_u32 s100, s100, s89
	s_addc_u32 s101, s101, 0
	global_load_dword v77, v178, s[100:101] nt
	s_add_u32 s100, s100, s89
	s_addc_u32 s101, s101, 0
	global_load_dword v78, v178, s[100:101] nt
	s_add_u32 s100, s100, s89
	s_addc_u32 s101, s101, 0
	global_load_dword v79, v178, s[100:101] nt
	s_add_u32 s100, s100, s89
	s_addc_u32 s101, s101, 0
	global_load_dword v80, v178, s[100:101] nt
	s_add_u32 s100, s100, s89
	s_addc_u32 s101, s101, 0
	global_load_dword v81, v178, s[100:101] nt
	s_add_u32 s100, s100, s89
	s_addc_u32 s101, s101, 0
	global_load_dword v82, v178, s[100:101] nt
	s_add_u32 s100, s100, s89
	s_addc_u32 s101, s101, 0
	global_load_dword v83, v178, s[100:101] nt
	s_add_u32 s100, s100, s89
	s_addc_u32 s101, s101, 0
	global_load_dword v84, v178, s[100:101] nt
	s_add_u32 s100, s100, s89
	s_addc_u32 s101, s101, 0
	global_load_dword v85, v178, s[100:101] nt
	s_add_u32 s100, s100, s89
	s_addc_u32 s101, s101, 0
	global_load_dword v86, v178, s[100:101] nt
	s_add_u32 s100, s100, s89
	s_addc_u32 s101, s101, 0
	global_load_dword v87, v178, s[100:101] nt
	s_add_u32 s100, s100, s89
	s_addc_u32 s101, s101, 0
	global_load_dword v88, v178, s[100:101] nt
	s_add_u32 s100, s100, s89
	s_addc_u32 s101, s101, 0
	global_load_dword v89, v178, s[100:101] nt
	s_add_u32 s100, s100, s89
	s_addc_u32 s101, s101, 0
	global_load_dword v90, v178, s[100:101] nt
	s_add_u32 s100, s100, s89
	s_addc_u32 s101, s101, 0
	global_load_dword v91, v178, s[100:101] nt
	s_add_u32 s100, s100, s89
	s_addc_u32 s101, s101, 0
	global_load_dword v92, v178, s[100:101] nt
	s_add_u32 s100, s100, s89
	s_addc_u32 s101, s101, 0
	global_load_dword v93, v178, s[100:101] nt
	s_add_u32 s100, s100, s89
	s_addc_u32 s101, s101, 0
	global_load_dword v94, v178, s[100:101] nt
	s_add_u32 s100, s100, s89
	s_addc_u32 s101, s101, 0
	global_load_dword v95, v178, s[100:101] nt
	s_add_u32 s100, s100, s89
	s_addc_u32 s101, s101, 0
	global_load_dword v96, v178, s[100:101] nt
	s_add_u32 s100, s100, s89
	s_addc_u32 s101, s101, 0
	global_load_dword v97, v178, s[100:101] nt
	s_add_u32 s100, s100, s89
	s_addc_u32 s101, s101, 0
	s_waitcnt vmcnt(48)
	v_mul_f32_e32 v34, 0x42000000, v34
	v_mul_f32_e32 v35, 0x42000000, v35
	v_mul_f32_e32 v36, 0x42000000, v36
	v_mul_f32_e32 v37, 0x42000000, v37
	v_mul_f32_e32 v38, 0x42000000, v38
	v_mul_f32_e32 v39, 0x42000000, v39
	v_mul_f32_e32 v40, 0x42000000, v40
	v_mul_f32_e32 v41, 0x42000000, v41
	v_mul_f32_e32 v42, 0x42000000, v42
	v_mul_f32_e32 v43, 0x42000000, v43
	v_mul_f32_e32 v44, 0x42000000, v44
	v_mul_f32_e32 v45, 0x42000000, v45
	v_mul_f32_e32 v46, 0x42000000, v46
	v_mul_f32_e32 v47, 0x42000000, v47
	v_mul_f32_e32 v48, 0x42000000, v48
	v_mul_f32_e32 v49, 0x42000000, v49
	v_cvt_pk_fp8_f32 v154, v34, v35
	v_cvt_pk_fp8_f32 v155, v38, v39
	v_cvt_pk_fp8_f32 v156, v42, v43
	v_cvt_pk_fp8_f32 v157, v46, v47
	v_cvt_pk_fp8_f32 v154, v36, v37 op_sel:[0,0,1]
	v_cvt_pk_fp8_f32 v155, v40, v41 op_sel:[0,0,1]
	v_cvt_pk_fp8_f32 v156, v44, v45 op_sel:[0,0,1]
	v_cvt_pk_fp8_f32 v157, v48, v49 op_sel:[0,0,1]
	s_waitcnt vmcnt(32)
	v_mul_f32_e32 v50, 0x42000000, v50
	v_mul_f32_e32 v51, 0x42000000, v51
	v_mul_f32_e32 v52, 0x42000000, v52
	v_mul_f32_e32 v53, 0x42000000, v53
	v_mul_f32_e32 v54, 0x42000000, v54
	v_mul_f32_e32 v55, 0x42000000, v55
	v_mul_f32_e32 v56, 0x42000000, v56
	v_mul_f32_e32 v57, 0x42000000, v57
	v_mul_f32_e32 v58, 0x42000000, v58
	v_mul_f32_e32 v59, 0x42000000, v59
	v_mul_f32_e32 v60, 0x42000000, v60
	v_mul_f32_e32 v61, 0x42000000, v61
	v_mul_f32_e32 v62, 0x42000000, v62
	v_mul_f32_e32 v63, 0x42000000, v63
	v_mul_f32_e32 v64, 0x42000000, v64
	v_mul_f32_e32 v65, 0x42000000, v65
	v_cvt_pk_fp8_f32 v158, v50, v51
	v_cvt_pk_fp8_f32 v159, v54, v55
	v_cvt_pk_fp8_f32 v160, v58, v59
	v_cvt_pk_fp8_f32 v161, v62, v63
	v_cvt_pk_fp8_f32 v158, v52, v53 op_sel:[0,0,1]
	v_cvt_pk_fp8_f32 v159, v56, v57 op_sel:[0,0,1]
	v_cvt_pk_fp8_f32 v160, v60, v61 op_sel:[0,0,1]
	v_cvt_pk_fp8_f32 v161, v64, v65 op_sel:[0,0,1]
	s_waitcnt vmcnt(16)
	v_mul_f32_e32 v66, 0x42000000, v66
	v_mul_f32_e32 v67, 0x42000000, v67
	v_mul_f32_e32 v68, 0x42000000, v68
	v_mul_f32_e32 v69, 0x42000000, v69
	v_mul_f32_e32 v70, 0x42000000, v70
	v_mul_f32_e32 v71, 0x42000000, v71
	v_mul_f32_e32 v72, 0x42000000, v72
	v_mul_f32_e32 v73, 0x42000000, v73
	v_mul_f32_e32 v74, 0x42000000, v74
	v_mul_f32_e32 v75, 0x42000000, v75
	v_mul_f32_e32 v76, 0x42000000, v76
	v_mul_f32_e32 v77, 0x42000000, v77
	v_mul_f32_e32 v78, 0x42000000, v78
	v_mul_f32_e32 v79, 0x42000000, v79
	v_mul_f32_e32 v80, 0x42000000, v80
	v_mul_f32_e32 v81, 0x42000000, v81
	v_cvt_pk_fp8_f32 v162, v66, v67
	v_cvt_pk_fp8_f32 v163, v70, v71
	v_cvt_pk_fp8_f32 v164, v74, v75
	v_cvt_pk_fp8_f32 v165, v78, v79
	v_cvt_pk_fp8_f32 v162, v68, v69 op_sel:[0,0,1]
	v_cvt_pk_fp8_f32 v163, v72, v73 op_sel:[0,0,1]
	v_cvt_pk_fp8_f32 v164, v76, v77 op_sel:[0,0,1]
	v_cvt_pk_fp8_f32 v165, v80, v81 op_sel:[0,0,1]
	s_waitcnt vmcnt(0)
	v_mul_f32_e32 v82, 0x42000000, v82
	v_mul_f32_e32 v83, 0x42000000, v83
	v_mul_f32_e32 v84, 0x42000000, v84
	v_mul_f32_e32 v85, 0x42000000, v85
	v_mul_f32_e32 v86, 0x42000000, v86
	v_mul_f32_e32 v87, 0x42000000, v87
	v_mul_f32_e32 v88, 0x42000000, v88
	v_mul_f32_e32 v89, 0x42000000, v89
	v_mul_f32_e32 v90, 0x42000000, v90
	v_mul_f32_e32 v91, 0x42000000, v91
	v_mul_f32_e32 v92, 0x42000000, v92
	v_mul_f32_e32 v93, 0x42000000, v93
	v_mul_f32_e32 v94, 0x42000000, v94
	v_mul_f32_e32 v95, 0x42000000, v95
	v_mul_f32_e32 v96, 0x42000000, v96
	v_mul_f32_e32 v97, 0x42000000, v97
	v_cvt_pk_fp8_f32 v166, v82, v83
	v_cvt_pk_fp8_f32 v167, v86, v87
	v_cvt_pk_fp8_f32 v168, v90, v91
	v_cvt_pk_fp8_f32 v169, v94, v95
	v_cvt_pk_fp8_f32 v166, v84, v85 op_sel:[0,0,1]
	v_cvt_pk_fp8_f32 v167, v88, v89 op_sel:[0,0,1]
	v_cvt_pk_fp8_f32 v168, v92, v93 op_sel:[0,0,1]
	v_cvt_pk_fp8_f32 v169, v96, v97 op_sel:[0,0,1]
	s_mov_b32 vcc_lo, 0xaaaaaaaa
	s_mov_b32 vcc_hi, 0xaaaaaaaa
	s_nop 1
	v_cndmask_b32_dpp v170, v154, v158, vcc quad_perm:[1,0,3,2] row_mask:0xf bank_mask:0xf
	v_cndmask_b32_dpp v174, v162, v166, vcc quad_perm:[1,0,3,2] row_mask:0xf bank_mask:0xf
	v_cndmask_b32_dpp v171, v155, v159, vcc quad_perm:[1,0,3,2] row_mask:0xf bank_mask:0xf
	v_cndmask_b32_dpp v175, v163, v167, vcc quad_perm:[1,0,3,2] row_mask:0xf bank_mask:0xf
	v_cndmask_b32_dpp v172, v156, v160, vcc quad_perm:[1,0,3,2] row_mask:0xf bank_mask:0xf
	v_cndmask_b32_dpp v176, v164, v168, vcc quad_perm:[1,0,3,2] row_mask:0xf bank_mask:0xf
	v_cndmask_b32_dpp v173, v157, v161, vcc quad_perm:[1,0,3,2] row_mask:0xf bank_mask:0xf
	v_cndmask_b32_dpp v177, v165, v169, vcc quad_perm:[1,0,3,2] row_mask:0xf bank_mask:0xf
	s_mov_b32 vcc_lo, 0x55555555
	s_mov_b32 vcc_hi, 0x55555555
	s_nop 1
	v_cndmask_b32_dpp v154, v158, v154, vcc quad_perm:[1,0,3,2] row_mask:0xf bank_mask:0xf
	v_cndmask_b32_dpp v162, v166, v162, vcc quad_perm:[1,0,3,2] row_mask:0xf bank_mask:0xf
	v_cndmask_b32_dpp v155, v159, v155, vcc quad_perm:[1,0,3,2] row_mask:0xf bank_mask:0xf
	v_cndmask_b32_dpp v163, v167, v163, vcc quad_perm:[1,0,3,2] row_mask:0xf bank_mask:0xf
	v_cndmask_b32_dpp v156, v160, v156, vcc quad_perm:[1,0,3,2] row_mask:0xf bank_mask:0xf
	v_cndmask_b32_dpp v164, v168, v164, vcc quad_perm:[1,0,3,2] row_mask:0xf bank_mask:0xf
	v_cndmask_b32_dpp v157, v161, v157, vcc quad_perm:[1,0,3,2] row_mask:0xf bank_mask:0xf
	v_cndmask_b32_dpp v165, v169, v165, vcc quad_perm:[1,0,3,2] row_mask:0xf bank_mask:0xf
	s_mov_b32 vcc_lo, 0xcccccccc
	s_mov_b32 vcc_hi, 0xcccccccc
	s_nop 1
	v_cndmask_b32_dpp v158, v154, v162, vcc quad_perm:[2,3,0,1] row_mask:0xf bank_mask:0xf
	v_cndmask_b32_dpp v166, v170, v174, vcc quad_perm:[2,3,0,1] row_mask:0xf bank_mask:0xf
	v_cndmask_b32_dpp v159, v155, v163, vcc quad_perm:[2,3,0,1] row_mask:0xf bank_mask:0xf
	v_cndmask_b32_dpp v167, v171, v175, vcc quad_perm:[2,3,0,1] row_mask:0xf bank_mask:0xf
	v_cndmask_b32_dpp v160, v156, v164, vcc quad_perm:[2,3,0,1] row_mask:0xf bank_mask:0xf
	v_cndmask_b32_dpp v168, v172, v176, vcc quad_perm:[2,3,0,1] row_mask:0xf bank_mask:0xf
	v_cndmask_b32_dpp v161, v157, v165, vcc quad_perm:[2,3,0,1] row_mask:0xf bank_mask:0xf
	v_cndmask_b32_dpp v169, v173, v177, vcc quad_perm:[2,3,0,1] row_mask:0xf bank_mask:0xf
	s_mov_b32 vcc_lo, 0x33333333
	s_mov_b32 vcc_hi, 0x33333333
	s_nop 1
	v_cndmask_b32_dpp v154, v162, v154, vcc quad_perm:[2,3,0,1] row_mask:0xf bank_mask:0xf
	v_cndmask_b32_dpp v170, v174, v170, vcc quad_perm:[2,3,0,1] row_mask:0xf bank_mask:0xf
	v_cndmask_b32_dpp v155, v163, v155, vcc quad_perm:[2,3,0,1] row_mask:0xf bank_mask:0xf
	v_cndmask_b32_dpp v171, v175, v171, vcc quad_perm:[2,3,0,1] row_mask:0xf bank_mask:0xf
	v_cndmask_b32_dpp v156, v164, v156, vcc quad_perm:[2,3,0,1] row_mask:0xf bank_mask:0xf
	v_cndmask_b32_dpp v172, v176, v172, vcc quad_perm:[2,3,0,1] row_mask:0xf bank_mask:0xf
	v_cndmask_b32_dpp v157, v165, v157, vcc quad_perm:[2,3,0,1] row_mask:0xf bank_mask:0xf
	v_cndmask_b32_dpp v173, v177, v173, vcc quad_perm:[2,3,0,1] row_mask:0xf bank_mask:0xf
	global_store_dwordx4 v179, v[154:157], s[82:83] nt
	global_store_dwordx4 v180, v[170:173], s[82:83] nt
	global_store_dwordx4 v181, v[158:161], s[82:83] nt
	global_store_dwordx4 v190, v[166:169], s[82:83] nt
	v_readlane_b32 s2, v239, 0
	s_lshr_b32 s2, s2, 6
	s_add_i32 s2, s2, 6
	s_cmp_gt_u32 s2, 11
	s_cbranch_scc1 .Lhw_seam7_done
	s_add_i32 s2, s2, 84
	s_mul_i32 s2, s2, s74
	v_readlane_b32 s9, v239, 23
	s_lshr_b32 s9, s9, 3
	s_add_i32 s2, s2, s9
	s_cmp_gt_u32 s2, 24575
	s_cbranch_scc1 .Lhw_seam7_done
	v_mbcnt_lo_u32_b32 v178, -1, 0
	v_mbcnt_hi_u32_b32 v178, -1, v178
	v_and_b32_e32 v179, 60, v178
	v_lshlrev_b32_e32 v179, 10, v179
	v_and_b32_e32 v180, 3, v178
	v_lshl_or_b32 v179, v180, 4, v179
	v_add_u32_e32 v180, 0x400, v179
	v_add_u32_e32 v181, 0x800, v179
	v_add_u32_e32 v190, 0xc00, v179
	v_lshlrev_b32_e32 v178, 2, v178
	s_cmp_lt_u32 s2, 16384
	s_cbranch_scc0 .Lhw_dn_s7_1
	s_lshr_b32 s9, s2, 9
	s_bfe_u32 s32, s2, 0x40005
	s_and_b32 s53, s2, 31
	s_lshl_b32 s69, s9, 23
	s_lshl_b32 s100, s32, 19
	s_add_i32 s69, s69, s100
	s_lshl_b32 s100, s53, 8
	s_add_i32 s69, s69, s100
	s_lshl_b32 s98, s9, 11
	s_bfe_u32 s100, s53, 0x30001
	s_lshl_b32 s100, s100, 8
	s_add_i32 s98, s98, s100
	s_lshr_b32 s100, s53, 4
	s_lshl_b32 s100, s100, 7
	s_add_i32 s98, s98, s100
	s_and_b32 s100, s53, 1
	s_lshl_b32 s100, s100, 6
	s_add_i32 s98, s98, s100
	s_lshl_b32 s98, s98, 10
	s_lshl_b32 s100, s32, 6
	s_add_i32 s98, s98, s100
	s_add_i32 s98, s98, 0x2000000
	v_readlane_b32 s82, v239, 11
	v_readlane_b32 s83, v239, 12
	s_movk_i32 s89, 8192
	s_branch .Lhw_go_s7_1
